# vaccH: SDWA shift/convert ops replaced by two plain VALU ops each (both halves)
# baseline (speedup 1.0000x reference)
; #define LAS __attribute__((address_space(3)))
; template <bool RUN_L = true, bool RUN_G = true, bool DRY = false>
; __device__ __forceinline__ void phase_vaccH(unsigned char* ws, LAS unsigned char* lds, int layer, int G) {
;     ...
;     for (int cg = blockIdx.x; cg < NGRP; cg += G) {
;         __syncthreads();
;         { const u32x4* src = (const u32x4*)(pvl + (size_t)cg * (NEXP * 8)) + tid; u32x4 t_[16];
; #pragma unroll
;           for (int i = 0; i < 16; ++i) t_[i] = src[512 * i];
; #pragma unroll
;           for (int i = 0; i < 16; ++i) ((LAS u32x4*)lds)[tid + 512 * i] = t_[i]; }
;         __syncthreads();
;         if (wid < 4) { if (RUN_L) {
.LBB0_1231:
	s_ashr_i32 s29, s28, 31
	s_lshl_b64 s[22:23], s[28:29], 17
	s_waitcnt vmcnt(15)
	v_lshl_add_u64 v[58:59], v[130:131], 0, s[22:23]
	s_waitcnt vmcnt(2)
	v_add_co_u32_e32 v6, vcc, 0x2000, v58
	s_mov_b32 s8, 0x12000
	s_nop 0
	v_addc_co_u32_e32 v7, vcc, 0, v59, vcc
	v_add_co_u32_e32 v10, vcc, 0x4000, v58
	s_waitcnt vmcnt(2)
	s_nop 0
	v_addc_co_u32_e32 v11, vcc, 0, v59, vcc
	v_add_co_u32_e32 v14, vcc, 0x6000, v58
	s_barrier
	s_nop 0
	v_addc_co_u32_e32 v15, vcc, 0, v59, vcc
	v_add_co_u32_e32 v18, vcc, 0x8000, v58
	s_nop 1
	v_addc_co_u32_e32 v19, vcc, 0, v59, vcc
	v_add_co_u32_e32 v22, vcc, 0xa000, v58
	global_load_dwordx4 v[2:5], v[58:59], off
	s_nop 0
	global_load_dwordx4 v[6:9], v[6:7], off
	v_addc_co_u32_e32 v23, vcc, 0, v59, vcc
	v_add_co_u32_e32 v26, vcc, 0xc000, v58
	global_load_dwordx4 v[10:13], v[10:11], off
	s_nop 0
	global_load_dwordx4 v[14:17], v[14:15], off
	v_addc_co_u32_e32 v27, vcc, 0, v59, vcc
	v_add_co_u32_e32 v30, vcc, 0xe000, v58
	global_load_dwordx4 v[18:21], v[18:19], off
	s_nop 0
	global_load_dwordx4 v[22:25], v[22:23], off
	v_addc_co_u32_e32 v31, vcc, 0, v59, vcc
	v_add_co_u32_e32 v34, vcc, s56, v58
	global_load_dwordx4 v[26:29], v[26:27], off
	s_nop 0
	global_load_dwordx4 v[30:33], v[30:31], off
	v_addc_co_u32_e32 v35, vcc, 0, v59, vcc
	v_add_co_u32_e32 v38, vcc, s8, v58
	s_mov_b32 s8, 0x14000
	s_nop 0
	v_addc_co_u32_e32 v39, vcc, 0, v59, vcc
	v_add_co_u32_e32 v42, vcc, s8, v58
	s_mov_b32 s8, 0x16000
	s_nop 0
	v_addc_co_u32_e32 v43, vcc, 0, v59, vcc
	v_add_co_u32_e32 v46, vcc, s8, v58
	s_mov_b32 s8, 0x1a000
	s_nop 0
	v_addc_co_u32_e32 v47, vcc, 0, v59, vcc
	s_waitcnt vmcnt(9)
	v_add_co_u32_e32 v50, vcc, s57, v58
	global_load_dwordx4 v[34:37], v[34:35], off
	s_nop 0
	global_load_dwordx4 v[38:41], v[38:39], off
	s_waitcnt vmcnt(10)
	v_addc_co_u32_e32 v51, vcc, 0, v59, vcc
	v_add_co_u32_e32 v54, vcc, s8, v58
	s_mov_b32 s8, 0x1c000
	s_nop 0
	v_addc_co_u32_e32 v55, vcc, 0, v59, vcc
	v_add_co_u32_e32 v60, vcc, s8, v58
	global_load_dwordx4 v[42:45], v[42:43], off
	s_nop 0
	global_load_dwordx4 v[46:49], v[46:47], off
	v_addc_co_u32_e32 v61, vcc, 0, v59, vcc
	v_add_co_u32_e32 v62, vcc, s58, v58
	global_load_dwordx4 v[50:53], v[50:51], off
	s_nop 0
	global_load_dwordx4 v[54:57], v[54:55], off
	v_addc_co_u32_e32 v63, vcc, 0, v59, vcc
	global_load_dwordx4 v[58:61], v[60:61], off
	s_nop 0
	global_load_dwordx4 v[62:65], v[62:63], off
	s_mov_b64 s[30:31], -1
	s_and_b64 vcc, exec, s[10:11]
	s_waitcnt vmcnt(15)
	ds_write_b128 v158, v[2:5]
	s_waitcnt vmcnt(14)
	ds_write_b128 v158, v[6:9] offset:8192
	s_waitcnt vmcnt(13)
	ds_write_b128 v158, v[10:13] offset:16384
	s_waitcnt vmcnt(12)
	ds_write_b128 v158, v[14:17] offset:24576
	s_waitcnt vmcnt(11)
	ds_write_b128 v158, v[18:21] offset:32768
	s_waitcnt vmcnt(10)
	ds_write_b128 v158, v[22:25] offset:40960
	s_waitcnt vmcnt(9)
	ds_write_b128 v158, v[26:29] offset:49152
	s_waitcnt vmcnt(8)
	ds_write_b128 v158, v[30:33] offset:57344
	s_waitcnt vmcnt(7)
	ds_write_b128 v160, v[34:37]
	s_waitcnt vmcnt(6)
	ds_write_b128 v161, v[38:41]
	s_waitcnt vmcnt(5)
	ds_write_b128 v162, v[42:45]
	s_waitcnt vmcnt(4)
	ds_write_b128 v163, v[46:49]
	s_waitcnt vmcnt(3)
	ds_write_b128 v164, v[50:53]
	s_waitcnt vmcnt(2)
	ds_write_b128 v165, v[54:57]
	s_waitcnt vmcnt(1)
	ds_write_b128 v166, v[58:61]
	s_waitcnt vmcnt(0)
	ds_write_b128 v167, v[62:65]
	s_waitcnt lgkmcnt(0)
	s_barrier
	s_cbranch_vccz .LBB0_1238
	s_or_b64 s[6:7], s[12:13], s[6:7]
	s_and_b64 vcc, exec, s[6:7]
	s_cbranch_vccnz .LBB0_1237
; #define VD_IDS(pw, IT) do { const int t_ = (IT) - ((IT) / MROWS) * MROWS; const unsigned* wp_ = WLP + (size_t)t_ * 128 + r8 * 16 + (lane & 3); \
;         pw[0] = wp_[0]; pw[1] = wp_[4]; pw[2] = wp_[8]; pw[3] = wp_[12]; } while (0)
; #define VD_IDS(pw, IT) do { const int t_ = (IT) - ((IT) / MROWS) * MROWS; const unsigned* wp_ = WLP + (size_t)t_ * 128 + r8 * 16 + (lane & 3); \
;         pw[0] = wp_[0]; pw[1] = wp_[4]; pw[2] = wp_[8]; pw[3] = wp_[12]; } while (0)
; template <bool RUN_L = true, bool RUN_G = true, bool DRY = false>
; __device__ __forceinline__ void phase_vaccH(unsigned char* ws, LAS unsigned char* lds, int layer, int G) {
;     ...
;             if (g < NIT) {
;                 u32x4 ra[16], rc[16]; unsigned pka[16], pkc[16]; f32x2 hva, hvc; f32x2* hpa; f32x2* hpc;
;                 unsigned pw0[4], pw1[4];
;                 VD_IDS(pw0, g);
;                 { const int i1c = g + NG < NIT ? g + NG : g; VD_IDS(pw1, i1c); }
;                 VD_ISSUE(ra, pka, hva, hpa, pw0, g);
	global_load_dword v2, v[136:137], off
	global_load_dword v3, v[136:137], off offset:16
	global_load_dword v4, v[136:137], off offset:32
	global_load_dword v5, v[136:137], off offset:48
	global_load_dword v191, v[138:139], off offset:48
	global_load_dword v193, v[138:139], off offset:32
	global_load_dword v194, v[138:139], off offset:16
	global_load_dword v195, v[138:139], off
	v_mov_b64_e32 v[156:157], v[142:143]
	s_mov_b32 s6, s35
	s_waitcnt vmcnt(7)
	v_mov_b32_dpp v187, v2 quad_perm:[0,0,0,0] row_mask:0xf bank_mask:0xf bound_ctrl:1
	v_mov_b32_dpp v186, v2 quad_perm:[1,1,1,1] row_mask:0xf bank_mask:0xf bound_ctrl:1
	v_mov_b32_dpp v185, v2 quad_perm:[2,2,2,2] row_mask:0xf bank_mask:0xf bound_ctrl:1
	s_waitcnt vmcnt(4)
	v_mov_b32_dpp v172, v5 quad_perm:[3,3,3,3] row_mask:0xf bank_mask:0xf bound_ctrl:1
	v_mov_b32_dpp v173, v5 quad_perm:[2,2,2,2] row_mask:0xf bank_mask:0xf bound_ctrl:1
	v_lshrrev_b32_e32 v132, 16, v172
	v_lshlrev_b32_e32 v132, v168, v132
	v_mov_b32_dpp v184, v2 quad_perm:[3,3,3,3] row_mask:0xf bank_mask:0xf bound_ctrl:1
	v_mov_b32_dpp v183, v3 quad_perm:[0,0,0,0] row_mask:0xf bank_mask:0xf bound_ctrl:1
	v_mov_b32_dpp v182, v3 quad_perm:[1,1,1,1] row_mask:0xf bank_mask:0xf bound_ctrl:1
	v_mov_b32_dpp v181, v3 quad_perm:[2,2,2,2] row_mask:0xf bank_mask:0xf bound_ctrl:1
	v_mov_b32_dpp v180, v3 quad_perm:[3,3,3,3] row_mask:0xf bank_mask:0xf bound_ctrl:1
	v_mov_b32_dpp v174, v5 quad_perm:[1,1,1,1] row_mask:0xf bank_mask:0xf bound_ctrl:1
	v_lshl_add_u64 v[2:3], v[140:141], 0, v[132:133]
	v_lshrrev_b32_e32 v132, 16, v173
	v_lshlrev_b32_e32 v132, v168, v132
	v_mov_b32_dpp v175, v5 quad_perm:[0,0,0,0] row_mask:0xf bank_mask:0xf bound_ctrl:1
	v_lshl_add_u64 v[6:7], v[140:141], 0, v[132:133]
	v_lshrrev_b32_e32 v132, 16, v174
	v_lshlrev_b32_e32 v132, v168, v132
	v_mov_b32_dpp v176, v4 quad_perm:[3,3,3,3] row_mask:0xf bank_mask:0xf bound_ctrl:1
	v_lshl_add_u64 v[10:11], v[140:141], 0, v[132:133]
	v_lshrrev_b32_e32 v132, 16, v175
	v_lshlrev_b32_e32 v132, v168, v132
	v_mov_b32_dpp v177, v4 quad_perm:[2,2,2,2] row_mask:0xf bank_mask:0xf bound_ctrl:1
	v_lshl_add_u64 v[14:15], v[140:141], 0, v[132:133]
	v_lshrrev_b32_e32 v132, 16, v176
	v_lshlrev_b32_e32 v132, v168, v132
	v_mov_b32_dpp v178, v4 quad_perm:[1,1,1,1] row_mask:0xf bank_mask:0xf bound_ctrl:1
	v_lshl_add_u64 v[18:19], v[140:141], 0, v[132:133]
	v_lshrrev_b32_e32 v132, 16, v177
	v_lshlrev_b32_e32 v132, v168, v132
	v_mov_b32_dpp v179, v4 quad_perm:[0,0,0,0] row_mask:0xf bank_mask:0xf bound_ctrl:1
	v_lshl_add_u64 v[22:23], v[140:141], 0, v[132:133]
	v_lshrrev_b32_e32 v132, 16, v178
	v_lshlrev_b32_e32 v132, v168, v132
	v_lshl_add_u64 v[26:27], v[140:141], 0, v[132:133]
	v_lshrrev_b32_e32 v132, 16, v179
	v_lshlrev_b32_e32 v132, v168, v132
	v_lshl_add_u64 v[30:31], v[140:141], 0, v[132:133]
	v_lshrrev_b32_e32 v132, 16, v180
	v_lshlrev_b32_e32 v132, v168, v132
	v_lshl_add_u64 v[34:35], v[140:141], 0, v[132:133]
	v_lshrrev_b32_e32 v132, 16, v181
	v_lshlrev_b32_e32 v132, v168, v132
	v_lshl_add_u64 v[38:39], v[140:141], 0, v[132:133]
	v_lshrrev_b32_e32 v132, 16, v182
	v_lshlrev_b32_e32 v132, v168, v132
	v_lshl_add_u64 v[42:43], v[140:141], 0, v[132:133]
	v_lshrrev_b32_e32 v132, 16, v183
	v_lshlrev_b32_e32 v132, v168, v132
	v_lshl_add_u64 v[46:47], v[140:141], 0, v[132:133]
	v_lshrrev_b32_e32 v132, 16, v184
	v_lshlrev_b32_e32 v132, v168, v132
	v_lshl_add_u64 v[50:51], v[140:141], 0, v[132:133]
	v_lshrrev_b32_e32 v132, 16, v185
	v_lshlrev_b32_e32 v132, v168, v132
	v_lshl_add_u64 v[54:55], v[140:141], 0, v[132:133]
	v_lshrrev_b32_e32 v132, 16, v186
	v_lshlrev_b32_e32 v132, v168, v132
	v_lshl_add_u64 v[58:59], v[140:141], 0, v[132:133]
	v_lshrrev_b32_e32 v132, 16, v187
	v_lshlrev_b32_e32 v132, v168, v132
	v_lshl_add_u64 v[62:63], v[140:141], 0, v[132:133]
	global_load_dwordx2 v[150:151], v[142:143], off
	s_nop 0
	global_load_dwordx4 v[2:5], v[2:3], off
	s_nop 0
	global_load_dwordx4 v[6:9], v[6:7], off
	s_nop 0
	global_load_dwordx4 v[10:13], v[10:11], off
	s_nop 0
	global_load_dwordx4 v[14:17], v[14:15], off
	s_nop 0
	global_load_dwordx4 v[18:21], v[18:19], off
	s_nop 0
	global_load_dwordx4 v[22:25], v[22:23], off
	s_nop 0
	global_load_dwordx4 v[26:29], v[26:27], off
	s_nop 0
	global_load_dwordx4 v[30:33], v[30:31], off
	s_nop 0
	global_load_dwordx4 v[34:37], v[34:35], off
	s_nop 0
	global_load_dwordx4 v[38:41], v[38:39], off
	s_nop 0
	global_load_dwordx4 v[42:45], v[42:43], off
	s_nop 0
	global_load_dwordx4 v[46:49], v[46:47], off
	s_nop 0
	global_load_dwordx4 v[50:53], v[50:51], off
	s_nop 0
	global_load_dwordx4 v[54:57], v[54:55], off
	s_nop 0
	global_load_dwordx4 v[58:61], v[58:59], off
	s_nop 0
	global_load_dwordx4 v[62:65], v[62:63], off
	s_branch .LBB0_1235

; #define VD_IDS(pw, IT) do { const int t_ = (IT) - ((IT) / MROWS) * MROWS; const unsigned* wp_ = WLP + (size_t)t_ * 128 + r8 * 16 + (lane & 3); \
;         pw[0] = wp_[0]; pw[1] = wp_[4]; pw[2] = wp_[8]; pw[3] = wp_[12]; } while (0)
; #define VD_IDS(pw, IT) do { const int t_ = (IT) - ((IT) / MROWS) * MROWS; const unsigned* wp_ = WLP + (size_t)t_ * 128 + r8 * 16 + (lane & 3); \
;         pw[0] = wp_[0]; pw[1] = wp_[4]; pw[2] = wp_[8]; pw[3] = wp_[12]; } while (0)
; template <bool RUN_L = true, bool RUN_G = true, bool DRY = false>
; __device__ __forceinline__ void phase_vaccH(unsigned char* ws, LAS unsigned char* lds, int layer, int G) {
;     ...
;                 for (int item = g; item < NIT; item += 2 * NG) {
;                     const int i1 = item + NG, i2 = item + 2 * NG, i3 = item + 3 * NG;
;                     const bool v1 = i1 < NIT;
;                     const int i1c = v1 ? i1 : item, i2c = i2 < NIT ? i2 : item, i3c = i3 < NIT ? i3 : item;
;                     VD_IDS(pw0, i2c);
;                     __builtin_amdgcn_sched_barrier(0);
;                     VD_ISSUE(rc, pkc, hvc, hpc, pw1, i1c);
;                     __builtin_amdgcn_sched_barrier(0);
;                     VD_COMP(ra, pka, hva, hpa, true);
.LBB0_1235:
	s_add_i32 s8, s6, s54
	s_add_i32 s7, s59, s6
	s_add_i32 s29, s60, s6
	s_cmpk_lt_i32 s8, 0x4020
	s_cselect_b32 s30, s8, s6
	s_cmpk_lt_i32 s7, 0x4020
	s_cselect_b32 s7, s7, s6
	s_mul_hi_i32 s22, s7, 0x7fc01ff1
	s_lshr_b32 s23, s22, 31
	s_ashr_i32 s22, s22, 12
	s_add_i32 s31, s22, s23
	s_mul_i32 s22, s31, 0xffffdff0
	s_add_i32 s22, s22, s7
	s_ashr_i32 s23, s22, 31
	s_lshl_b64 s[24:25], s[22:23], 9
	v_lshl_add_u64 v[66:67], v[144:145], 0, s[24:25]
	global_load_dword v211, v[66:67], off
	global_load_dword v210, v[66:67], off offset:16
	global_load_dword v209, v[66:67], off offset:32
	global_load_dword v208, v[66:67], off offset:48
	s_mul_hi_i32 s7, s30, 0x7fc01ff1
	s_lshr_b32 s24, s7, 31
	s_ashr_i32 s7, s7, 12
	s_add_i32 s7, s7, s24
	s_lshl_b32 s24, s7, 10
	s_or_b32 s24, s24, s55
	s_ashr_i32 s25, s24, 31
	s_cmpk_lt_i32 s29, 0x4020
	s_mulk_i32 s7, 0xdff0
	s_cselect_b32 s29, s29, s6
	s_add_i32 s6, s7, s30
	s_ashr_i32 s7, s6, 31
	s_lshl_b64 s[6:7], s[6:7], 14
	s_add_u32 s30, s94, s6
	s_addc_u32 s33, s95, s7
	s_lshl_b64 s[6:7], s[24:25], 2
	s_add_u32 s52, s30, s6
	s_mul_hi_i32 s6, s29, 0x7fc01ff1
	s_addc_u32 s53, s33, s7
	s_lshr_b32 s7, s6, 31
	s_ashr_i32 s6, s6, 12
	s_add_i32 s6, s6, s7
	s_mulk_i32 s6, 0x2010
	s_sub_i32 s6, s29, s6
	s_ashr_i32 s7, s6, 31
	s_lshl_b64 s[46:47], s[6:7], 9
	s_lshl_b32 s6, s31, 10
	s_or_b32 s30, s6, s55
	s_ashr_i32 s31, s30, 31
	s_lshl_b64 s[6:7], s[22:23], 14
	s_add_u32 s22, s94, s6
	s_addc_u32 s23, s95, s7
	s_lshl_b64 s[6:7], s[30:31], 2
	s_add_u32 s6, s22, s6
	s_addc_u32 s7, s23, s7
	s_cmpk_gt_i32 s8, 0x401f
	s_waitcnt vmcnt(21)
	v_mov_b32_dpp v207, v195 quad_perm:[0,0,0,0] row_mask:0xf bank_mask:0xf bound_ctrl:1
	v_mov_b32_dpp v206, v195 quad_perm:[1,1,1,1] row_mask:0xf bank_mask:0xf bound_ctrl:1
	v_lshl_add_u64 v[66:67], v[134:135], 0, s[24:25]
	v_lshrrev_b32_e32 v132, 16, v207
	v_lshlrev_b32_e32 v132, v168, v132
	v_mov_b32_dpp v205, v195 quad_perm:[2,2,2,2] row_mask:0xf bank_mask:0xf bound_ctrl:1
	s_waitcnt lgkmcnt(0)
	v_lshl_add_u64 v[68:69], v[66:67], 0, v[132:133]
	v_lshrrev_b32_e32 v132, 16, v206
	v_lshlrev_b32_e32 v132, v168, v132
	v_mov_b32_dpp v204, v195 quad_perm:[3,3,3,3] row_mask:0xf bank_mask:0xf bound_ctrl:1
	v_lshl_add_u64 v[70:71], v[66:67], 0, v[132:133]
	v_lshrrev_b32_e32 v132, 16, v205
	v_lshlrev_b32_e32 v132, v168, v132
	v_mov_b32_dpp v203, v194 quad_perm:[0,0,0,0] row_mask:0xf bank_mask:0xf bound_ctrl:1
	global_load_dwordx4 v[126:129], v[68:69], off
	global_load_dwordx4 v[122:125], v[70:71], off
	v_lshl_add_u64 v[68:69], v[66:67], 0, v[132:133]
	v_lshrrev_b32_e32 v132, 16, v204
	v_lshlrev_b32_e32 v132, v168, v132
	v_mov_b32_dpp v202, v194 quad_perm:[1,1,1,1] row_mask:0xf bank_mask:0xf bound_ctrl:1
	v_lshl_add_u64 v[70:71], v[66:67], 0, v[132:133]
	v_lshrrev_b32_e32 v132, 16, v203
	v_lshlrev_b32_e32 v132, v168, v132
	v_mov_b32_dpp v201, v194 quad_perm:[2,2,2,2] row_mask:0xf bank_mask:0xf bound_ctrl:1
	global_load_dwordx4 v[118:121], v[68:69], off
	global_load_dwordx4 v[114:117], v[70:71], off
	v_lshl_add_u64 v[68:69], v[66:67], 0, v[132:133]
	v_lshrrev_b32_e32 v132, 16, v202
	v_lshlrev_b32_e32 v132, v168, v132
	v_mov_b32_dpp v200, v194 quad_perm:[3,3,3,3] row_mask:0xf bank_mask:0xf bound_ctrl:1
	v_lshl_add_u64 v[70:71], v[66:67], 0, v[132:133]
	v_lshrrev_b32_e32 v132, 16, v201
	v_lshlrev_b32_e32 v132, v168, v132
	v_mov_b32_dpp v199, v193 quad_perm:[0,0,0,0] row_mask:0xf bank_mask:0xf bound_ctrl:1
	global_load_dwordx4 v[110:113], v[68:69], off
	global_load_dwordx4 v[106:109], v[70:71], off
	v_lshl_add_u64 v[68:69], v[66:67], 0, v[132:133]
	v_lshrrev_b32_e32 v132, 16, v200
	v_lshlrev_b32_e32 v132, v168, v132
	v_mov_b32_dpp v198, v193 quad_perm:[1,1,1,1] row_mask:0xf bank_mask:0xf bound_ctrl:1
	v_lshl_add_u64 v[70:71], v[66:67], 0, v[132:133]
	v_lshrrev_b32_e32 v132, 16, v199
	v_lshlrev_b32_e32 v132, v168, v132
	v_mov_b32_dpp v197, v193 quad_perm:[2,2,2,2] row_mask:0xf bank_mask:0xf bound_ctrl:1
	global_load_dwordx4 v[102:105], v[68:69], off
	global_load_dwordx4 v[98:101], v[70:71], off
	v_lshl_add_u64 v[68:69], v[66:67], 0, v[132:133]
	v_lshrrev_b32_e32 v132, 16, v198
	v_lshlrev_b32_e32 v132, v168, v132
	v_mov_b32_dpp v196, v193 quad_perm:[3,3,3,3] row_mask:0xf bank_mask:0xf bound_ctrl:1
	v_lshl_add_u64 v[70:71], v[66:67], 0, v[132:133]
	v_lshrrev_b32_e32 v132, 16, v197
	v_lshlrev_b32_e32 v132, v168, v132
	v_mov_b32_dpp v192, v191 quad_perm:[0,0,0,0] row_mask:0xf bank_mask:0xf bound_ctrl:1
	global_load_dwordx4 v[94:97], v[68:69], off
	global_load_dwordx4 v[90:93], v[70:71], off
	v_lshl_add_u64 v[68:69], v[66:67], 0, v[132:133]
	v_lshrrev_b32_e32 v132, 16, v196
	v_lshlrev_b32_e32 v132, v168, v132
	v_mov_b32_dpp v190, v191 quad_perm:[1,1,1,1] row_mask:0xf bank_mask:0xf bound_ctrl:1
	v_lshl_add_u64 v[70:71], v[66:67], 0, v[132:133]
	v_lshrrev_b32_e32 v132, 16, v192
	v_lshlrev_b32_e32 v132, v168, v132
	v_mov_b32_e32 v147, v133
	v_mov_b32_dpp v189, v191 quad_perm:[2,2,2,2] row_mask:0xf bank_mask:0xf bound_ctrl:1
	global_load_dwordx4 v[86:89], v[68:69], off
	global_load_dwordx4 v[82:85], v[70:71], off
	v_lshl_add_u64 v[68:69], v[66:67], 0, v[132:133]
	v_lshrrev_b32_e32 v132, 16, v190
	v_lshlrev_b32_e32 v132, v168, v132
	v_lshl_add_u64 v[152:153], s[52:53], 0, v[146:147]
	v_mov_b32_e32 v149, v133
	v_mov_b32_dpp v188, v191 quad_perm:[3,3,3,3] row_mask:0xf bank_mask:0xf bound_ctrl:1
	v_lshl_add_u64 v[70:71], v[66:67], 0, v[132:133]
	v_lshrrev_b32_e32 v132, 16, v189
	v_lshlrev_b32_e32 v132, v168, v132
	v_lshl_add_u64 v[154:155], v[152:153], 0, v[148:149]
	global_load_dwordx4 v[78:81], v[68:69], off
	global_load_dwordx4 v[74:77], v[70:71], off
	v_lshl_add_u64 v[68:69], v[66:67], 0, v[132:133]
	v_lshrrev_b32_e32 v132, 16, v188
	v_lshlrev_b32_e32 v132, v168, v132
	v_add_co_u32_e32 v152, vcc, s61, v154
	v_lshl_add_u64 v[66:67], v[66:67], 0, v[132:133]
	s_nop 0
	v_addc_co_u32_e32 v153, vcc, 0, v155, vcc
	global_load_dwordx4 v[70:73], v[68:69], off
	s_nop 0
	global_load_dwordx4 v[66:69], v[66:67], off
	s_nop 0
	global_load_dwordx2 v[152:153], v[152:153], off
	v_perm_b32 v132, v187, v187, s63
	s_waitcnt vmcnt(21)
	v_perm_b32 v187, 0, v62, v169
	v_perm_b32 v62, 0, v62, v170
	v_perm_b32 v191, 0, v63, v169
	v_perm_b32 v63, 0, v63, v170
	v_perm_b32 v193, 0, v64, v169
	v_perm_b32 v64, 0, v64, v170
	v_perm_b32 v194, 0, v65, v169
	v_perm_b32 v65, 0, v65, v170
	v_pk_fma_f16 v187, v187, v132, 0
	v_pk_fma_f16 v62, v62, v132, 0
	v_pk_fma_f16 v191, v191, v132, 0
	v_pk_fma_f16 v63, v63, v132, 0
	v_pk_fma_f16 v193, v193, v132, 0
	v_pk_fma_f16 v64, v64, v132, 0
	v_pk_fma_f16 v194, v194, v132, 0
	v_pk_fma_f16 v65, v65, v132, 0
	v_perm_b32 v132, v186, v186, s63
	v_perm_b32 v186, 0, v58, v169
	v_perm_b32 v58, 0, v58, v170
	v_pk_fma_f16 v58, v58, v132, v62
	v_perm_b32 v62, 0, v59, v169
	v_perm_b32 v59, 0, v59, v170
	v_pk_fma_f16 v59, v59, v132, v63
	v_perm_b32 v63, 0, v60, v169
	v_perm_b32 v60, 0, v60, v170
	v_pk_fma_f16 v60, v60, v132, v64
	v_perm_b32 v64, 0, v61, v169
	v_perm_b32 v61, 0, v61, v170
	v_pk_fma_f16 v186, v186, v132, v187
	v_pk_fma_f16 v62, v62, v132, v191
	v_pk_fma_f16 v63, v63, v132, v193
	v_pk_fma_f16 v64, v64, v132, v194
	v_pk_fma_f16 v61, v61, v132, v65
	v_perm_b32 v65, v185, v185, s63
	v_perm_b32 v132, 0, v54, v169
	v_perm_b32 v54, 0, v54, v170
	v_pk_fma_f16 v54, v54, v65, v58
	v_perm_b32 v58, 0, v55, v169
	v_perm_b32 v55, 0, v55, v170
	v_pk_fma_f16 v55, v55, v65, v59
	v_perm_b32 v59, 0, v56, v169
	v_perm_b32 v56, 0, v56, v170
	v_pk_fma_f16 v56, v56, v65, v60
	v_perm_b32 v60, 0, v57, v169
	v_perm_b32 v57, 0, v57, v170
	v_pk_fma_f16 v58, v58, v65, v62
	v_pk_fma_f16 v57, v57, v65, v61
	v_perm_b32 v61, v184, v184, s63
	v_perm_b32 v62, 0, v50, v169
	v_perm_b32 v50, 0, v50, v170
	v_pk_fma_f16 v50, v50, v61, v54
	v_perm_b32 v54, 0, v51, v169
	v_perm_b32 v51, 0, v51, v170
	v_pk_fma_f16 v51, v51, v61, v55
	v_perm_b32 v55, 0, v52, v169
	v_perm_b32 v52, 0, v52, v170
	v_pk_fma_f16 v52, v52, v61, v56
	v_perm_b32 v56, 0, v53, v169
	v_perm_b32 v53, 0, v53, v170
	v_pk_fma_f16 v54, v54, v61, v58
	v_pk_fma_f16 v53, v53, v61, v57
	v_perm_b32 v57, v183, v183, s63
	v_perm_b32 v58, 0, v46, v169
	v_perm_b32 v46, 0, v46, v170
	v_pk_fma_f16 v46, v46, v57, v50
	v_perm_b32 v50, 0, v47, v169
	v_perm_b32 v47, 0, v47, v170
	v_pk_fma_f16 v47, v47, v57, v51
	v_perm_b32 v51, 0, v48, v169
	v_perm_b32 v48, 0, v48, v170
	v_pk_fma_f16 v48, v48, v57, v52
	v_perm_b32 v52, 0, v49, v169
	v_perm_b32 v49, 0, v49, v170
	v_pk_fma_f16 v50, v50, v57, v54
	v_pk_fma_f16 v49, v49, v57, v53
	v_perm_b32 v53, v182, v182, s63
	v_perm_b32 v54, 0, v42, v169
	v_perm_b32 v42, 0, v42, v170
	v_pk_fma_f16 v42, v42, v53, v46
	v_perm_b32 v46, 0, v43, v169
	v_perm_b32 v43, 0, v43, v170
	v_pk_fma_f16 v43, v43, v53, v47
	v_perm_b32 v47, 0, v44, v169
	v_perm_b32 v44, 0, v44, v170
	v_pk_fma_f16 v44, v44, v53, v48
	v_perm_b32 v48, 0, v45, v169
	v_perm_b32 v45, 0, v45, v170
	v_pk_fma_f16 v46, v46, v53, v50
	v_pk_fma_f16 v45, v45, v53, v49
	v_perm_b32 v49, v181, v181, s63
	v_perm_b32 v50, 0, v38, v169
	v_perm_b32 v38, 0, v38, v170
	v_pk_fma_f16 v38, v38, v49, v42
	v_perm_b32 v42, 0, v39, v169
	v_perm_b32 v39, 0, v39, v170
	v_pk_fma_f16 v39, v39, v49, v43
	v_perm_b32 v43, 0, v40, v169
	v_perm_b32 v40, 0, v40, v170
	v_pk_fma_f16 v40, v40, v49, v44
	v_perm_b32 v44, 0, v41, v169
	v_perm_b32 v41, 0, v41, v170
	v_pk_fma_f16 v42, v42, v49, v46
	v_pk_fma_f16 v41, v41, v49, v45
	v_perm_b32 v45, v180, v180, s63
	v_perm_b32 v46, 0, v34, v169
	v_perm_b32 v34, 0, v34, v170
	v_pk_fma_f16 v34, v34, v45, v38
	v_perm_b32 v38, 0, v35, v169
	v_perm_b32 v35, 0, v35, v170
	v_pk_fma_f16 v35, v35, v45, v39
	v_perm_b32 v39, 0, v36, v169
	v_perm_b32 v36, 0, v36, v170
	v_pk_fma_f16 v36, v36, v45, v40
	v_perm_b32 v40, 0, v37, v169
	v_perm_b32 v37, 0, v37, v170
	v_pk_fma_f16 v38, v38, v45, v42
	v_pk_fma_f16 v37, v37, v45, v41
	v_perm_b32 v41, v179, v179, s63
	v_perm_b32 v42, 0, v30, v169
	v_perm_b32 v30, 0, v30, v170
	v_pk_fma_f16 v30, v30, v41, v34
	v_perm_b32 v34, 0, v31, v169
	v_perm_b32 v31, 0, v31, v170
	v_pk_fma_f16 v31, v31, v41, v35
	v_perm_b32 v35, 0, v32, v169
	v_perm_b32 v32, 0, v32, v170
	v_pk_fma_f16 v32, v32, v41, v36
	v_perm_b32 v36, 0, v33, v169
	v_perm_b32 v33, 0, v33, v170
	v_pk_fma_f16 v34, v34, v41, v38
	v_pk_fma_f16 v33, v33, v41, v37
	v_perm_b32 v37, v178, v178, s63
	v_perm_b32 v38, 0, v26, v169
	v_perm_b32 v26, 0, v26, v170
	v_pk_fma_f16 v26, v26, v37, v30
	v_perm_b32 v30, 0, v27, v169
	v_perm_b32 v27, 0, v27, v170
	v_pk_fma_f16 v27, v27, v37, v31
	v_perm_b32 v31, 0, v28, v169
	v_perm_b32 v28, 0, v28, v170
	v_pk_fma_f16 v28, v28, v37, v32
	v_perm_b32 v32, 0, v29, v169
	v_perm_b32 v29, 0, v29, v170
	v_pk_fma_f16 v30, v30, v37, v34
	v_pk_fma_f16 v29, v29, v37, v33
	v_perm_b32 v33, v177, v177, s63
	v_perm_b32 v34, 0, v22, v169
	v_perm_b32 v22, 0, v22, v170
	v_pk_fma_f16 v22, v22, v33, v26
	v_perm_b32 v26, 0, v23, v169
	v_perm_b32 v23, 0, v23, v170
	v_pk_fma_f16 v23, v23, v33, v27
	v_perm_b32 v27, 0, v24, v169
	v_perm_b32 v24, 0, v24, v170
	v_pk_fma_f16 v24, v24, v33, v28
	v_perm_b32 v28, 0, v25, v169
	v_perm_b32 v25, 0, v25, v170
	v_pk_fma_f16 v26, v26, v33, v30
	v_pk_fma_f16 v25, v25, v33, v29
	v_perm_b32 v29, v176, v176, s63
	v_perm_b32 v30, 0, v18, v169
	v_perm_b32 v18, 0, v18, v170
	v_pk_fma_f16 v18, v18, v29, v22
	v_perm_b32 v22, 0, v19, v169
	v_perm_b32 v19, 0, v19, v170
	v_pk_fma_f16 v19, v19, v29, v23
	v_perm_b32 v23, 0, v20, v169
	v_perm_b32 v20, 0, v20, v170
	v_pk_fma_f16 v20, v20, v29, v24
	v_perm_b32 v24, 0, v21, v169
	v_perm_b32 v21, 0, v21, v170
	v_pk_fma_f16 v22, v22, v29, v26
	v_pk_fma_f16 v21, v21, v29, v25
	v_perm_b32 v25, v175, v175, s63
	v_perm_b32 v26, 0, v14, v169
	v_perm_b32 v14, 0, v14, v170
	v_pk_fma_f16 v14, v14, v25, v18
	v_perm_b32 v18, 0, v15, v169
	v_perm_b32 v15, 0, v15, v170
; #define VD_IDS(pw, IT) do { const int t_ = (IT) - ((IT) / MROWS) * MROWS; const unsigned* wp_ = WLP + (size_t)t_ * 128 + r8 * 16 + (lane & 3); \
;         pw[0] = wp_[0]; pw[1] = wp_[4]; pw[2] = wp_[8]; pw[3] = wp_[12]; } while (0)
; #define VD_IDS(pw, IT) do { const int t_ = (IT) - ((IT) / MROWS) * MROWS; const unsigned* wp_ = WLP + (size_t)t_ * 128 + r8 * 16 + (lane & 3); \
;         pw[0] = wp_[0]; pw[1] = wp_[4]; pw[2] = wp_[8]; pw[3] = wp_[12]; } while (0)
; template <bool RUN_L = true, bool RUN_G = true, bool DRY = false>
; __device__ __forceinline__ void phase_vaccH(unsigned char* ws, LAS unsigned char* lds, int layer, int G) {
;     ...
;                     VD_IDS(pw1, i3c);
;                     __builtin_amdgcn_sched_barrier(0);
;                     VD_ISSUE(ra, pka, hva, hpa, pw0, i2c);
	v_pk_fma_f16 v15, v15, v25, v19
	v_perm_b32 v19, 0, v16, v169
	v_perm_b32 v16, 0, v16, v170
	v_pk_fma_f16 v132, v132, v65, v186
	v_pk_fma_f16 v59, v59, v65, v63
	v_pk_fma_f16 v60, v60, v65, v64
	v_pk_fma_f16 v16, v16, v25, v20
	v_perm_b32 v20, 0, v17, v169
	v_perm_b32 v17, 0, v17, v170
	v_pk_fma_f16 v62, v62, v61, v132
	v_pk_fma_f16 v55, v55, v61, v59
	v_pk_fma_f16 v56, v56, v61, v60
	v_pk_fma_f16 v18, v18, v25, v22
	v_pk_fma_f16 v17, v17, v25, v21
	v_perm_b32 v21, v174, v174, s63
	v_perm_b32 v22, 0, v10, v169
	v_perm_b32 v10, 0, v10, v170
	v_pk_fma_f16 v58, v58, v57, v62
	v_pk_fma_f16 v51, v51, v57, v55
	v_pk_fma_f16 v52, v52, v57, v56
	v_pk_fma_f16 v10, v10, v21, v14
	v_perm_b32 v14, 0, v11, v169
	v_perm_b32 v11, 0, v11, v170
	v_pk_fma_f16 v54, v54, v53, v58
	v_pk_fma_f16 v47, v47, v53, v51
	v_pk_fma_f16 v48, v48, v53, v52
	v_pk_fma_f16 v11, v11, v21, v15
	v_perm_b32 v15, 0, v12, v169
	v_perm_b32 v12, 0, v12, v170
	v_pk_fma_f16 v50, v50, v49, v54
	v_pk_fma_f16 v43, v43, v49, v47
	v_pk_fma_f16 v44, v44, v49, v48
	v_pk_fma_f16 v12, v12, v21, v16
	v_perm_b32 v16, 0, v13, v169
	v_perm_b32 v13, 0, v13, v170
	v_pk_fma_f16 v46, v46, v45, v50
	v_pk_fma_f16 v39, v39, v45, v43
	v_pk_fma_f16 v40, v40, v45, v44
	v_pk_fma_f16 v14, v14, v21, v18
	v_pk_fma_f16 v13, v13, v21, v17
	v_perm_b32 v17, v173, v173, s63
	v_perm_b32 v18, 0, v6, v169
	v_perm_b32 v6, 0, v6, v170
	v_pk_fma_f16 v42, v42, v41, v46
	v_pk_fma_f16 v35, v35, v41, v39
	v_pk_fma_f16 v36, v36, v41, v40
	v_pk_fma_f16 v6, v6, v17, v10
	v_perm_b32 v10, 0, v7, v169
	v_perm_b32 v7, 0, v7, v170
	v_pk_fma_f16 v38, v38, v37, v42
	v_pk_fma_f16 v31, v31, v37, v35
	v_pk_fma_f16 v32, v32, v37, v36
	v_pk_fma_f16 v7, v7, v17, v11
	v_perm_b32 v11, 0, v8, v169
	v_perm_b32 v8, 0, v8, v170
	v_pk_fma_f16 v34, v34, v33, v38
	v_pk_fma_f16 v27, v27, v33, v31
	v_pk_fma_f16 v28, v28, v33, v32
	v_pk_fma_f16 v8, v8, v17, v12
	v_perm_b32 v12, 0, v9, v169
	v_perm_b32 v9, 0, v9, v170
	v_pk_fma_f16 v30, v30, v29, v34
	v_pk_fma_f16 v23, v23, v29, v27
	v_pk_fma_f16 v24, v24, v29, v28
	v_pk_fma_f16 v10, v10, v17, v14
	v_pk_fma_f16 v9, v9, v17, v13
	v_perm_b32 v13, v172, v172, s63
	v_perm_b32 v14, 0, v2, v169
	v_perm_b32 v2, 0, v2, v170
	v_pk_fma_f16 v26, v26, v25, v30
	v_pk_fma_f16 v19, v19, v25, v23
	v_pk_fma_f16 v20, v20, v25, v24
	v_pk_fma_f16 v2, v2, v13, v6
	v_perm_b32 v6, 0, v3, v169
	v_perm_b32 v3, 0, v3, v170
	v_pk_fma_f16 v22, v22, v21, v26
	v_pk_fma_f16 v15, v15, v21, v19
	v_pk_fma_f16 v16, v16, v21, v20
	v_pk_fma_f16 v3, v3, v13, v7
	v_perm_b32 v7, 0, v4, v169
	v_perm_b32 v4, 0, v4, v170
	v_pk_fma_f16 v18, v18, v17, v22
	v_pk_fma_f16 v11, v11, v17, v15
	v_pk_fma_f16 v12, v12, v17, v16
	v_pk_fma_f16 v4, v4, v13, v8
	v_perm_b32 v8, 0, v5, v169
	v_perm_b32 v5, 0, v5, v170
	v_pk_fma_f16 v14, v14, v13, v18
	v_pk_fma_f16 v6, v6, v13, v10
	v_pk_fma_f16 v7, v7, v13, v11
	v_pk_fma_f16 v8, v8, v13, v12
	v_pk_fma_f16 v5, v5, v13, v9
	v_cvt_f32_f16_e32 v9, v14
	v_lshrrev_b32_e32 v10, 16, v14
	v_cvt_f32_f16_e32 v10, v10
	v_cvt_f32_f16_e32 v11, v2
	v_lshrrev_b32_e32 v12, 16, v2
	v_cvt_f32_f16_e32 v12, v12
	v_cvt_f32_f16_e32 v13, v6
	v_lshrrev_b32_e32 v14, 16, v6
	v_cvt_f32_f16_e32 v14, v14
	v_cvt_f32_f16_e32 v15, v3
	v_lshrrev_b32_e32 v16, 16, v3
	v_cvt_f32_f16_e32 v16, v16
	v_cvt_f32_f16_e32 v2, v7
	v_lshrrev_b32_e32 v3, 16, v7
	v_cvt_f32_f16_e32 v3, v3
	v_cvt_f32_f16_e32 v6, v4
	v_lshrrev_b32_e32 v7, 16, v4
	v_cvt_f32_f16_e32 v7, v7
	v_cvt_f32_f16_e32 v17, v8
	v_lshrrev_b32_e32 v8, 16, v8
	v_cvt_f32_f16_e32 v8, v8
	v_cvt_f32_f16_e32 v18, v5
	v_lshrrev_b32_e32 v19, 16, v5
	v_cvt_f32_f16_e32 v19, v19
	v_permlane32_swap_b32_e32 v9, v2
	v_permlane32_swap_b32_e32 v10, v3
	v_permlane32_swap_b32_e32 v11, v6
	v_permlane32_swap_b32_e32 v12, v7
	v_permlane32_swap_b32_e32 v13, v17
	v_permlane32_swap_b32_e32 v14, v8
	v_permlane32_swap_b32_e32 v15, v18
	v_permlane32_swap_b32_e32 v16, v19
	v_add_f32_e32 v2, v9, v2
	v_add_f32_e32 v3, v10, v3
	v_add_f32_e32 v4, v11, v6
	v_add_f32_e32 v5, v12, v7
	v_add_f32_e32 v6, v13, v17
	v_add_f32_e32 v7, v14, v8
	v_add_f32_e32 v8, v15, v18
	v_add_f32_e32 v9, v16, v19
	v_permlane16_swap_b32_e32 v2, v6
	v_permlane16_swap_b32_e32 v3, v7
	v_permlane16_swap_b32_e32 v4, v8
	v_permlane16_swap_b32_e32 v5, v9
	v_pk_add_f32 v[2:3], v[2:3], v[6:7]
	v_pk_add_f32 v[4:5], v[4:5], v[8:9]
	s_nop 0
	v_cndmask_b32_e64 v6, v2, v4, s[4:5]
	v_cndmask_b32_e64 v7, v3, v5, s[4:5]
	ds_bpermute_b32 v6, v159, v6
	ds_bpermute_b32 v7, v159, v7
	v_cndmask_b32_e64 v3, v5, v3, s[4:5]
	v_cndmask_b32_e64 v2, v4, v2, s[4:5]
	s_waitcnt lgkmcnt(0)
	v_pk_add_f32 v[2:3], v[2:3], v[6:7]
	s_nop 0
	v_pk_add_f32 v[2:3], v[150:151], v[2:3]
	global_store_dwordx2 v[156:157], v[2:3], off
	v_lshl_add_u64 v[2:3], v[144:145], 0, s[46:47]
	global_load_dword v195, v[2:3], off
	global_load_dword v194, v[2:3], off offset:16
	global_load_dword v193, v[2:3], off offset:32
	global_load_dword v191, v[2:3], off offset:48
	s_waitcnt vmcnt(25)
	v_mov_b32_dpp v187, v211 quad_perm:[0,0,0,0] row_mask:0xf bank_mask:0xf bound_ctrl:1
	v_mov_b32_dpp v186, v211 quad_perm:[1,1,1,1] row_mask:0xf bank_mask:0xf bound_ctrl:1
	v_lshl_add_u64 v[2:3], v[134:135], 0, s[30:31]
	v_lshrrev_b32_e32 v132, 16, v187
	v_lshlrev_b32_e32 v132, v168, v132
	v_mov_b32_dpp v185, v211 quad_perm:[2,2,2,2] row_mask:0xf bank_mask:0xf bound_ctrl:1
	v_lshl_add_u64 v[4:5], v[2:3], 0, v[132:133]
	v_lshrrev_b32_e32 v132, 16, v186
	v_lshlrev_b32_e32 v132, v168, v132
	v_mov_b32_dpp v184, v211 quad_perm:[3,3,3,3] row_mask:0xf bank_mask:0xf bound_ctrl:1
	v_lshl_add_u64 v[6:7], v[2:3], 0, v[132:133]
	v_lshrrev_b32_e32 v132, 16, v185
	v_lshlrev_b32_e32 v132, v168, v132
	s_waitcnt vmcnt(24)
	v_mov_b32_dpp v183, v210 quad_perm:[0,0,0,0] row_mask:0xf bank_mask:0xf bound_ctrl:1
	global_load_dwordx4 v[62:65], v[4:5], off
	global_load_dwordx4 v[58:61], v[6:7], off
	v_lshl_add_u64 v[4:5], v[2:3], 0, v[132:133]
	v_lshrrev_b32_e32 v132, 16, v184
	v_lshlrev_b32_e32 v132, v168, v132
	v_mov_b32_dpp v182, v210 quad_perm:[1,1,1,1] row_mask:0xf bank_mask:0xf bound_ctrl:1
	v_lshl_add_u64 v[6:7], v[2:3], 0, v[132:133]
	v_lshrrev_b32_e32 v132, 16, v183
	v_lshlrev_b32_e32 v132, v168, v132
	v_mov_b32_dpp v181, v210 quad_perm:[2,2,2,2] row_mask:0xf bank_mask:0xf bound_ctrl:1
	global_load_dwordx4 v[54:57], v[4:5], off
	global_load_dwordx4 v[50:53], v[6:7], off
	v_lshl_add_u64 v[4:5], v[2:3], 0, v[132:133]
	v_lshrrev_b32_e32 v132, 16, v182
	v_lshlrev_b32_e32 v132, v168, v132
	v_mov_b32_dpp v180, v210 quad_perm:[3,3,3,3] row_mask:0xf bank_mask:0xf bound_ctrl:1
	v_lshl_add_u64 v[6:7], v[2:3], 0, v[132:133]
	v_lshrrev_b32_e32 v132, 16, v181
	v_lshlrev_b32_e32 v132, v168, v132
	s_waitcnt vmcnt(27)
	v_mov_b32_dpp v179, v209 quad_perm:[0,0,0,0] row_mask:0xf bank_mask:0xf bound_ctrl:1
	global_load_dwordx4 v[46:49], v[4:5], off
	global_load_dwordx4 v[42:45], v[6:7], off
	v_lshl_add_u64 v[4:5], v[2:3], 0, v[132:133]
	v_lshrrev_b32_e32 v132, 16, v180
	v_lshlrev_b32_e32 v132, v168, v132
	v_mov_b32_dpp v178, v209 quad_perm:[1,1,1,1] row_mask:0xf bank_mask:0xf bound_ctrl:1
	v_lshl_add_u64 v[6:7], v[2:3], 0, v[132:133]
	v_lshrrev_b32_e32 v132, 16, v179
	v_lshlrev_b32_e32 v132, v168, v132
	v_mov_b32_dpp v177, v209 quad_perm:[2,2,2,2] row_mask:0xf bank_mask:0xf bound_ctrl:1
	global_load_dwordx4 v[38:41], v[4:5], off
	global_load_dwordx4 v[34:37], v[6:7], off
	v_lshl_add_u64 v[4:5], v[2:3], 0, v[132:133]
	v_lshrrev_b32_e32 v132, 16, v178
	v_lshlrev_b32_e32 v132, v168, v132
	v_mov_b32_dpp v176, v209 quad_perm:[3,3,3,3] row_mask:0xf bank_mask:0xf bound_ctrl:1
	v_lshl_add_u64 v[6:7], v[2:3], 0, v[132:133]
	v_lshrrev_b32_e32 v132, 16, v177
	v_lshlrev_b32_e32 v132, v168, v132
	s_waitcnt vmcnt(30)
	v_mov_b32_dpp v175, v208 quad_perm:[0,0,0,0] row_mask:0xf bank_mask:0xf bound_ctrl:1
	global_load_dwordx4 v[30:33], v[4:5], off
	global_load_dwordx4 v[26:29], v[6:7], off
	v_lshl_add_u64 v[4:5], v[2:3], 0, v[132:133]
	v_lshrrev_b32_e32 v132, 16, v176
	v_lshlrev_b32_e32 v132, v168, v132
	v_mov_b32_dpp v174, v208 quad_perm:[1,1,1,1] row_mask:0xf bank_mask:0xf bound_ctrl:1
	v_lshl_add_u64 v[6:7], v[2:3], 0, v[132:133]
	v_lshrrev_b32_e32 v132, 16, v175
	v_lshlrev_b32_e32 v132, v168, v132
	v_mov_b32_dpp v173, v208 quad_perm:[2,2,2,2] row_mask:0xf bank_mask:0xf bound_ctrl:1
	global_load_dwordx4 v[22:25], v[4:5], off
	global_load_dwordx4 v[18:21], v[6:7], off
	v_lshl_add_u64 v[4:5], v[2:3], 0, v[132:133]
	v_lshrrev_b32_e32 v132, 16, v174
	v_lshlrev_b32_e32 v132, v168, v132
	v_lshl_add_u64 v[150:151], s[6:7], 0, v[146:147]
	v_mov_b32_dpp v172, v208 quad_perm:[3,3,3,3] row_mask:0xf bank_mask:0xf bound_ctrl:1
	v_lshl_add_u64 v[6:7], v[2:3], 0, v[132:133]
	v_lshrrev_b32_e32 v132, 16, v173
	v_lshlrev_b32_e32 v132, v168, v132
	v_lshl_add_u64 v[156:157], v[150:151], 0, v[148:149]
	global_load_dwordx4 v[14:17], v[4:5], off
	global_load_dwordx4 v[10:13], v[6:7], off
	v_lshl_add_u64 v[4:5], v[2:3], 0, v[132:133]
	v_lshrrev_b32_e32 v132, 16, v172
	v_lshlrev_b32_e32 v132, v168, v132
	v_add_co_u32_e32 v150, vcc, s61, v156
	v_lshl_add_u64 v[2:3], v[2:3], 0, v[132:133]
	s_nop 0
	v_addc_co_u32_e32 v151, vcc, 0, v157, vcc
	global_load_dwordx4 v[6:9], v[4:5], off
	s_nop 0
	global_load_dwordx4 v[2:5], v[2:3], off
	s_nop 0
	global_load_dwordx2 v[150:151], v[150:151], off
	v_perm_b32 v132, v207, v207, s63
	s_waitcnt vmcnt(38)
	v_perm_b32 v147, 0, v126, v169
	v_perm_b32 v126, 0, v126, v170
	v_perm_b32 v149, 0, v127, v169
	v_perm_b32 v127, 0, v127, v170
	v_perm_b32 v207, 0, v128, v169
	v_perm_b32 v128, 0, v128, v170
	v_perm_b32 v208, 0, v129, v169
	v_perm_b32 v129, 0, v129, v170
	v_pk_fma_f16 v147, v132, v147, 0
	v_pk_fma_f16 v126, v132, v126, 0
	v_pk_fma_f16 v149, v132, v149, 0
	v_pk_fma_f16 v127, v132, v127, 0
	v_pk_fma_f16 v207, v132, v207, 0
	v_pk_fma_f16 v128, v132, v128, 0
	v_pk_fma_f16 v208, v132, v208, 0
	v_pk_fma_f16 v129, v132, v129, 0
	v_perm_b32 v132, v206, v206, s63
	s_waitcnt vmcnt(37)
	v_perm_b32 v206, 0, v122, v169
	v_perm_b32 v122, 0, v122, v170
	v_pk_fma_f16 v122, v132, v122, v126
	v_perm_b32 v126, 0, v123, v169
	v_perm_b32 v123, 0, v123, v170
	v_pk_fma_f16 v123, v132, v123, v127
	v_perm_b32 v127, 0, v124, v169
	v_perm_b32 v124, 0, v124, v170
	v_pk_fma_f16 v124, v132, v124, v128
	v_perm_b32 v128, 0, v125, v169
	v_perm_b32 v125, 0, v125, v170
	v_pk_fma_f16 v147, v132, v206, v147
	v_pk_fma_f16 v126, v132, v126, v149
	v_pk_fma_f16 v127, v132, v127, v207
	v_pk_fma_f16 v128, v132, v128, v208
	v_pk_fma_f16 v125, v132, v125, v129
	v_perm_b32 v129, v205, v205, s63
	s_waitcnt vmcnt(36)
	v_perm_b32 v132, 0, v118, v169
	v_perm_b32 v118, 0, v118, v170
	v_pk_fma_f16 v118, v129, v118, v122
	v_perm_b32 v122, 0, v119, v169
	v_perm_b32 v119, 0, v119, v170
	v_pk_fma_f16 v119, v129, v119, v123
	v_perm_b32 v123, 0, v120, v169
	v_perm_b32 v120, 0, v120, v170
	v_pk_fma_f16 v120, v129, v120, v124
	v_perm_b32 v124, 0, v121, v169
	v_perm_b32 v121, 0, v121, v170
	v_pk_fma_f16 v122, v129, v122, v126
	v_pk_fma_f16 v121, v129, v121, v125
	v_perm_b32 v125, v204, v204, s63
	s_waitcnt vmcnt(35)
	v_perm_b32 v126, 0, v114, v169
	v_perm_b32 v114, 0, v114, v170
	v_pk_fma_f16 v114, v125, v114, v118
	v_perm_b32 v118, 0, v115, v169
	v_perm_b32 v115, 0, v115, v170
	v_pk_fma_f16 v115, v125, v115, v119
	v_perm_b32 v119, 0, v116, v169
	v_perm_b32 v116, 0, v116, v170
	v_pk_fma_f16 v116, v125, v116, v120
	v_perm_b32 v120, 0, v117, v169
	v_perm_b32 v117, 0, v117, v170
	v_pk_fma_f16 v118, v125, v118, v122
	v_pk_fma_f16 v117, v125, v117, v121
	v_perm_b32 v121, v203, v203, s63
	s_waitcnt vmcnt(34)
	v_perm_b32 v122, 0, v110, v169
	v_perm_b32 v110, 0, v110, v170
	v_pk_fma_f16 v110, v121, v110, v114
	v_perm_b32 v114, 0, v111, v169
	v_perm_b32 v111, 0, v111, v170
	v_pk_fma_f16 v111, v121, v111, v115
	v_perm_b32 v115, 0, v112, v169
	v_perm_b32 v112, 0, v112, v170
	v_pk_fma_f16 v112, v121, v112, v116
	v_perm_b32 v116, 0, v113, v169
	v_perm_b32 v113, 0, v113, v170
	v_pk_fma_f16 v114, v121, v114, v118
	v_pk_fma_f16 v113, v121, v113, v117
	v_perm_b32 v117, v202, v202, s63
	s_waitcnt vmcnt(33)
	v_perm_b32 v118, 0, v106, v169
	v_perm_b32 v106, 0, v106, v170
	v_pk_fma_f16 v106, v117, v106, v110
	v_perm_b32 v110, 0, v107, v169
	v_perm_b32 v107, 0, v107, v170
	v_pk_fma_f16 v107, v117, v107, v111
	v_perm_b32 v111, 0, v108, v169
	v_perm_b32 v108, 0, v108, v170
	v_pk_fma_f16 v108, v117, v108, v112
	v_perm_b32 v112, 0, v109, v169
	v_perm_b32 v109, 0, v109, v170
	v_pk_fma_f16 v110, v117, v110, v114
	v_pk_fma_f16 v109, v117, v109, v113
	v_perm_b32 v113, v201, v201, s63
	s_waitcnt vmcnt(32)
	v_perm_b32 v114, 0, v102, v169
	v_perm_b32 v102, 0, v102, v170
	v_pk_fma_f16 v102, v113, v102, v106
	v_perm_b32 v106, 0, v103, v169
	v_perm_b32 v103, 0, v103, v170
	v_pk_fma_f16 v103, v113, v103, v107
	v_perm_b32 v107, 0, v104, v169
	v_perm_b32 v104, 0, v104, v170
	v_pk_fma_f16 v104, v113, v104, v108
	v_perm_b32 v108, 0, v105, v169
	v_perm_b32 v105, 0, v105, v170
	v_pk_fma_f16 v106, v113, v106, v110
	v_pk_fma_f16 v105, v113, v105, v109
	v_perm_b32 v109, v200, v200, s63
	s_waitcnt vmcnt(31)
	v_perm_b32 v110, 0, v98, v169
	v_perm_b32 v98, 0, v98, v170
	v_pk_fma_f16 v98, v109, v98, v102
	v_perm_b32 v102, 0, v99, v169
	v_perm_b32 v99, 0, v99, v170
	v_pk_fma_f16 v99, v109, v99, v103
	v_perm_b32 v103, 0, v100, v169
	v_perm_b32 v100, 0, v100, v170
	v_pk_fma_f16 v100, v109, v100, v104
	v_perm_b32 v104, 0, v101, v169
	v_perm_b32 v101, 0, v101, v170
	v_pk_fma_f16 v102, v109, v102, v106
	v_pk_fma_f16 v101, v109, v101, v105
	v_perm_b32 v105, v199, v199, s63
	s_waitcnt vmcnt(30)
	v_perm_b32 v106, 0, v94, v169
	v_perm_b32 v94, 0, v94, v170
	v_pk_fma_f16 v94, v105, v94, v98
	v_perm_b32 v98, 0, v95, v169
	v_perm_b32 v95, 0, v95, v170
	v_pk_fma_f16 v95, v105, v95, v99
	v_perm_b32 v99, 0, v96, v169
	v_perm_b32 v96, 0, v96, v170
	v_pk_fma_f16 v96, v105, v96, v100
	v_perm_b32 v100, 0, v97, v169
	v_perm_b32 v97, 0, v97, v170
	v_pk_fma_f16 v98, v105, v98, v102
	v_pk_fma_f16 v97, v105, v97, v101
	v_perm_b32 v101, v198, v198, s63
	s_waitcnt vmcnt(29)
	v_perm_b32 v102, 0, v90, v169
	v_perm_b32 v90, 0, v90, v170
	v_pk_fma_f16 v90, v101, v90, v94
	v_perm_b32 v94, 0, v91, v169
	v_perm_b32 v91, 0, v91, v170
	v_pk_fma_f16 v91, v101, v91, v95
	v_perm_b32 v95, 0, v92, v169
	v_perm_b32 v92, 0, v92, v170
	v_pk_fma_f16 v92, v101, v92, v96
	v_perm_b32 v96, 0, v93, v169
	v_perm_b32 v93, 0, v93, v170
	v_pk_fma_f16 v94, v101, v94, v98
	v_pk_fma_f16 v93, v101, v93, v97
	v_perm_b32 v97, v197, v197, s63
	s_waitcnt vmcnt(28)
	v_perm_b32 v98, 0, v86, v169
	v_perm_b32 v86, 0, v86, v170
	v_pk_fma_f16 v86, v97, v86, v90
	v_perm_b32 v90, 0, v87, v169
	v_perm_b32 v87, 0, v87, v170
	v_pk_fma_f16 v87, v97, v87, v91
	v_perm_b32 v91, 0, v88, v169
	v_perm_b32 v88, 0, v88, v170
	v_pk_fma_f16 v88, v97, v88, v92
	v_perm_b32 v92, 0, v89, v169
	v_perm_b32 v89, 0, v89, v170
	v_pk_fma_f16 v90, v97, v90, v94
	v_pk_fma_f16 v89, v97, v89, v93
	v_perm_b32 v93, v196, v196, s63
	s_waitcnt vmcnt(27)
	v_perm_b32 v94, 0, v82, v169
	v_perm_b32 v82, 0, v82, v170
	v_pk_fma_f16 v82, v93, v82, v86
	v_perm_b32 v86, 0, v83, v169
	v_perm_b32 v83, 0, v83, v170
	v_pk_fma_f16 v83, v93, v83, v87
	v_perm_b32 v87, 0, v84, v169
	v_perm_b32 v84, 0, v84, v170
	v_pk_fma_f16 v84, v93, v84, v88
	v_perm_b32 v88, 0, v85, v169
	v_perm_b32 v85, 0, v85, v170
	v_pk_fma_f16 v86, v93, v86, v90
	v_pk_fma_f16 v85, v93, v85, v89
	v_perm_b32 v89, v192, v192, s63
	s_waitcnt vmcnt(26)
	v_perm_b32 v90, 0, v78, v169
	v_perm_b32 v78, 0, v78, v170
	v_pk_fma_f16 v78, v89, v78, v82
	v_perm_b32 v82, 0, v79, v169
	v_perm_b32 v79, 0, v79, v170
	v_pk_fma_f16 v79, v89, v79, v83
	v_perm_b32 v83, 0, v80, v169
	v_perm_b32 v80, 0, v80, v170
	v_pk_fma_f16 v132, v129, v132, v147
	v_pk_fma_f16 v123, v129, v123, v127
	v_pk_fma_f16 v124, v129, v124, v128
	v_pk_fma_f16 v80, v89, v80, v84
	v_perm_b32 v84, 0, v81, v169
	v_perm_b32 v81, 0, v81, v170
	v_pk_fma_f16 v126, v125, v126, v132
	v_pk_fma_f16 v119, v125, v119, v123
	v_pk_fma_f16 v120, v125, v120, v124
	v_pk_fma_f16 v82, v89, v82, v86
	v_pk_fma_f16 v81, v89, v81, v85
	v_perm_b32 v85, v190, v190, s63
	s_waitcnt vmcnt(25)
; template <bool RUN_L = true, bool RUN_G = true, bool DRY = false>
; __device__ __forceinline__ void phase_vaccH(unsigned char* ws, LAS unsigned char* lds, int layer, int G) {
;     ...
;                     VD_COMP(rc, pkc, hvc, hpc, v1);
	v_perm_b32 v86, 0, v74, v169
	v_perm_b32 v74, 0, v74, v170
	v_pk_fma_f16 v122, v121, v122, v126
	v_pk_fma_f16 v115, v121, v115, v119
	v_pk_fma_f16 v116, v121, v116, v120
	v_pk_fma_f16 v74, v85, v74, v78
	v_perm_b32 v78, 0, v75, v169
	v_perm_b32 v75, 0, v75, v170
	v_pk_fma_f16 v118, v117, v118, v122
	v_pk_fma_f16 v111, v117, v111, v115
	v_pk_fma_f16 v112, v117, v112, v116
	v_pk_fma_f16 v75, v85, v75, v79
	v_perm_b32 v79, 0, v76, v169
	v_perm_b32 v76, 0, v76, v170
	v_pk_fma_f16 v114, v113, v114, v118
	v_pk_fma_f16 v107, v113, v107, v111
	v_pk_fma_f16 v108, v113, v108, v112
	v_pk_fma_f16 v76, v85, v76, v80
	v_perm_b32 v80, 0, v77, v169
	v_perm_b32 v77, 0, v77, v170
	v_pk_fma_f16 v110, v109, v110, v114
	v_pk_fma_f16 v103, v109, v103, v107
	v_pk_fma_f16 v104, v109, v104, v108
	v_pk_fma_f16 v78, v85, v78, v82
	v_pk_fma_f16 v77, v85, v77, v81
	v_perm_b32 v81, v189, v189, s63
	s_waitcnt vmcnt(24)
	v_perm_b32 v82, 0, v70, v169
	v_perm_b32 v70, 0, v70, v170
	v_pk_fma_f16 v106, v105, v106, v110
	v_pk_fma_f16 v99, v105, v99, v103
	v_pk_fma_f16 v100, v105, v100, v104
	v_pk_fma_f16 v70, v81, v70, v74
	v_perm_b32 v74, 0, v71, v169
	v_perm_b32 v71, 0, v71, v170
	v_pk_fma_f16 v102, v101, v102, v106
	v_pk_fma_f16 v95, v101, v95, v99
	v_pk_fma_f16 v96, v101, v96, v100
	v_pk_fma_f16 v71, v81, v71, v75
	v_perm_b32 v75, 0, v72, v169
	v_perm_b32 v72, 0, v72, v170
	v_pk_fma_f16 v98, v97, v98, v102
	v_pk_fma_f16 v91, v97, v91, v95
	v_pk_fma_f16 v92, v97, v92, v96
	v_pk_fma_f16 v72, v81, v72, v76
	v_perm_b32 v76, 0, v73, v169
	v_perm_b32 v73, 0, v73, v170
	v_pk_fma_f16 v94, v93, v94, v98
	v_pk_fma_f16 v87, v93, v87, v91
	v_pk_fma_f16 v88, v93, v88, v92
	v_pk_fma_f16 v74, v81, v74, v78
	v_pk_fma_f16 v73, v81, v73, v77
	v_perm_b32 v77, v188, v188, s63
	s_waitcnt vmcnt(23)
	v_perm_b32 v78, 0, v66, v169
	v_perm_b32 v66, 0, v66, v170
	v_pk_fma_f16 v90, v89, v90, v94
	v_pk_fma_f16 v83, v89, v83, v87
	v_pk_fma_f16 v84, v89, v84, v88
	v_pk_fma_f16 v66, v77, v66, v70
	v_perm_b32 v70, 0, v67, v169
	v_perm_b32 v67, 0, v67, v170
	v_pk_fma_f16 v86, v85, v86, v90
	v_pk_fma_f16 v79, v85, v79, v83
	v_pk_fma_f16 v80, v85, v80, v84
	v_pk_fma_f16 v67, v77, v67, v71
	v_perm_b32 v71, 0, v68, v169
	v_perm_b32 v68, 0, v68, v170
	v_pk_fma_f16 v82, v81, v82, v86
	v_pk_fma_f16 v75, v81, v75, v79
	v_pk_fma_f16 v76, v81, v76, v80
	v_pk_fma_f16 v68, v77, v68, v72
	v_perm_b32 v72, 0, v69, v169
	v_perm_b32 v69, 0, v69, v170
	v_pk_fma_f16 v78, v77, v78, v82
	v_pk_fma_f16 v70, v77, v70, v74
	v_pk_fma_f16 v71, v77, v71, v75
	v_pk_fma_f16 v72, v77, v72, v76
	v_pk_fma_f16 v69, v77, v69, v73
	v_cvt_f32_f16_e32 v73, v78
	v_lshrrev_b32_e32 v74, 16, v78
	v_cvt_f32_f16_e32 v74, v74
	v_cvt_f32_f16_e32 v75, v66
	v_lshrrev_b32_e32 v76, 16, v66
	v_cvt_f32_f16_e32 v76, v76
	v_cvt_f32_f16_e32 v77, v70
	v_lshrrev_b32_e32 v78, 16, v70
	v_cvt_f32_f16_e32 v78, v78
	v_cvt_f32_f16_e32 v79, v67
	v_lshrrev_b32_e32 v80, 16, v67
	v_cvt_f32_f16_e32 v80, v80
	v_cvt_f32_f16_e32 v66, v71
	v_lshrrev_b32_e32 v67, 16, v71
	v_cvt_f32_f16_e32 v67, v67
	v_cvt_f32_f16_e32 v70, v68
	v_lshrrev_b32_e32 v71, 16, v68
	v_cvt_f32_f16_e32 v71, v71
	v_cvt_f32_f16_e32 v81, v72
	v_lshrrev_b32_e32 v72, 16, v72
	v_cvt_f32_f16_e32 v72, v72
	v_cvt_f32_f16_e32 v82, v69
	v_lshrrev_b32_e32 v83, 16, v69
	v_cvt_f32_f16_e32 v83, v83
	v_permlane32_swap_b32_e32 v73, v66
	v_permlane32_swap_b32_e32 v74, v67
	v_permlane32_swap_b32_e32 v75, v70
	v_permlane32_swap_b32_e32 v76, v71
	v_permlane32_swap_b32_e32 v77, v81
	v_permlane32_swap_b32_e32 v78, v72
	v_permlane32_swap_b32_e32 v79, v82
	v_permlane32_swap_b32_e32 v80, v83
	v_add_f32_e32 v66, v73, v66
	v_add_f32_e32 v67, v74, v67
	v_add_f32_e32 v68, v75, v70
	v_add_f32_e32 v69, v76, v71
	v_add_f32_e32 v70, v77, v81
	v_add_f32_e32 v71, v78, v72
	v_add_f32_e32 v72, v79, v82
	v_add_f32_e32 v73, v80, v83
	v_permlane16_swap_b32_e32 v66, v70
	v_permlane16_swap_b32_e32 v67, v71
	v_permlane16_swap_b32_e32 v68, v72
	v_permlane16_swap_b32_e32 v69, v73
	v_pk_add_f32 v[66:67], v[66:67], v[70:71]
	v_pk_add_f32 v[70:71], v[68:69], v[72:73]
	s_nop 0
	v_cndmask_b32_e64 v68, v66, v70, s[4:5]
	v_cndmask_b32_e64 v69, v67, v71, s[4:5]
	ds_bpermute_b32 v68, v159, v68
	ds_bpermute_b32 v69, v159, v69
	s_cbranch_scc1 .LBB0_1234
	v_cndmask_b32_e64 v67, v71, v67, s[4:5]
	v_cndmask_b32_e64 v66, v70, v66, s[4:5]
	s_waitcnt lgkmcnt(0)
	v_pk_add_f32 v[66:67], v[66:67], v[68:69]
	v_lshl_add_u64 v[72:73], v[154:155], 0, s[14:15]
	s_waitcnt vmcnt(22)
	v_pk_add_f32 v[66:67], v[152:153], v[66:67]
	global_store_dwordx2 v[72:73], v[66:67], off
	s_branch .LBB0_1234

; #define VL_LOAD(wr, C) do { _Pragma("unroll") for (int i = 0; i < 16; ++i) wr[i] = wp[(size_t)((C) * 16 + i) * MROWS]; } while (0)
; #define VL_LOAD(wr, C) do { _Pragma("unroll") for (int i = 0; i < 16; ++i) wr[i] = wp[(size_t)((C) * 16 + i) * MROWS]; } while (0)
; template <bool RUN_L = true, bool RUN_G = true, bool DRY = false>
; __device__ __forceinline__ void phase_vaccH(unsigned char* ws, LAS unsigned char* lds, int layer, int G) {
;     ...
;                 VL_LOAD(wa, 0);
; #pragma unroll 1
;                 for (int c = 0; c < 8; c += 2) {
;                     VL_LOAD(wb, c + 1);
;                     __builtin_amdgcn_sched_barrier(0);
;                     VL_CHUNK(wa);
.LBB0_1242:
	global_load_dword v24, v238, s[76:77]
	s_add_u32 s78, s76, s62
	s_addc_u32 s79, s77, 0
	global_load_dword v31, v238, s[78:79] offset:64
	v_mov_b32_e32 v19, v29
	s_add_u32 s78, s76, s56
	s_addc_u32 s79, s77, 0
	global_load_dword v30, v238, s[78:79] offset:128
	v_mov_b32_e32 v18, v28
	s_add_u32 s78, s76, s57
	s_addc_u32 s79, s77, 0
	global_load_dword v29, v238, s[78:79] offset:192
	v_mov_b32_e32 v17, v35
	s_add_u32 s78, s76, s64
	s_addc_u32 s79, s77, 0
	global_load_dword v28, v238, s[78:79] offset:256
	v_mov_b32_e32 v16, v34
	s_add_u32 s78, s76, s65
	s_addc_u32 s79, s77, 0
	global_load_dword v27, v238, s[78:79] offset:320
	s_add_u32 s78, s76, s66
	s_addc_u32 s79, s77, 0
	global_load_dword v26, v238, s[78:79] offset:384
	s_add_u32 s78, s76, s67
	s_addc_u32 s79, s77, 0
	global_load_dword v25, v238, s[78:79] offset:448
	s_add_u32 s78, s76, s68
	s_addc_u32 s79, s77, 0
	global_load_dword v54, v238, s[78:79] offset:512
	s_add_u32 s78, s76, s69
	s_addc_u32 s79, s77, 0
	global_load_dword v53, v238, s[78:79] offset:576
	s_add_u32 s78, s76, s70
	s_addc_u32 s79, s77, 0
	global_load_dword v52, v238, s[78:79] offset:640
	s_add_u32 s78, s76, s71
	s_addc_u32 s79, s77, 0
	global_load_dword v35, v238, s[78:79] offset:704
	s_add_u32 s78, s76, s72
	s_addc_u32 s79, s77, 0
	global_load_dword v34, v238, s[78:79] offset:768
	s_add_u32 s78, s76, s73
	s_addc_u32 s79, s77, 0
	global_load_dword v33, v238, s[78:79] offset:832
	s_add_u32 s78, s76, s74
	s_addc_u32 s79, s77, 0
	global_load_dword v32, v238, s[78:79] offset:896
	s_add_u32 s78, s76, s75
	s_addc_u32 s79, s77, 0
	global_load_dword v55, v238, s[78:79] offset:960
	s_waitcnt vmcnt(30)
	v_bfe_u32 v57, v37, 16, 16
	v_lshl_add_u32 v58, v57, 3, 0
	s_waitcnt vmcnt(29)
	v_bfe_u32 v57, v38, 16, 16
	v_bfe_u32 v56, v36, 16, 16
	v_lshl_add_u32 v60, v57, 3, 0
	s_waitcnt vmcnt(28)
	v_bfe_u32 v57, v39, 16, 16
	v_lshl_add_u32 v56, v56, 3, 0
	v_lshl_add_u32 v62, v57, 3, 0
	ds_read_b64 v[56:57], v56
	ds_read_b64 v[58:59], v58
	ds_read_b64 v[60:61], v60
	ds_read_b64 v[62:63], v62
	v_perm_b32 v36, v36, v36, s63
	s_waitcnt lgkmcnt(3)
	v_perm_b32 v88, 0, v56, v169
	v_perm_b32 v56, 0, v56, v170
	v_perm_b32 v89, 0, v57, v169
	v_perm_b32 v57, 0, v57, v170
	v_pk_fma_f16 v88, v36, v88, 0
	v_pk_fma_f16 v56, v36, v56, 0
	v_pk_fma_f16 v89, v36, v89, 0
	v_pk_fma_f16 v36, v36, v57, 0
	v_perm_b32 v37, v37, v37, s63
	s_waitcnt lgkmcnt(2)
	v_perm_b32 v57, 0, v58, v169
	v_perm_b32 v58, 0, v58, v170
	v_pk_fma_f16 v56, v37, v58, v56
	v_perm_b32 v58, 0, v59, v169
	v_perm_b32 v59, 0, v59, v170
	v_pk_fma_f16 v57, v37, v57, v88
	v_pk_fma_f16 v58, v37, v58, v89
	v_pk_fma_f16 v36, v37, v59, v36
	v_perm_b32 v37, v38, v38, s63
	s_waitcnt lgkmcnt(1)
	v_perm_b32 v38, 0, v60, v169
	v_pk_fma_f16 v38, v37, v38, v57
	v_perm_b32 v57, 0, v60, v170
	s_waitcnt vmcnt(26)
	v_bfe_u32 v65, v41, 16, 16
	v_pk_fma_f16 v56, v37, v57, v56
	v_perm_b32 v57, 0, v61, v169
	v_lshl_add_u32 v66, v65, 3, 0
	s_waitcnt vmcnt(25)
	v_bfe_u32 v65, v42, 16, 16
	v_pk_fma_f16 v57, v37, v57, v58
	v_perm_b32 v58, 0, v61, v170
	v_bfe_u32 v64, v40, 16, 16
	v_lshl_add_u32 v68, v65, 3, 0
	s_waitcnt vmcnt(24)
	v_bfe_u32 v65, v44, 16, 16
	v_pk_fma_f16 v36, v37, v58, v36
	v_perm_b32 v37, v39, v39, s63
	s_waitcnt lgkmcnt(0)
	v_perm_b32 v39, 0, v62, v169
	v_lshl_add_u32 v64, v64, 3, 0
	v_lshl_add_u32 v70, v65, 3, 0
	v_pk_fma_f16 v38, v37, v39, v38
	v_perm_b32 v39, 0, v62, v170
	ds_read_b64 v[64:65], v64
	ds_read_b64 v[66:67], v66
	ds_read_b64 v[68:69], v68
	ds_read_b64 v[70:71], v70
	v_pk_fma_f16 v39, v37, v39, v56
	v_perm_b32 v56, 0, v63, v169
	v_pk_fma_f16 v56, v37, v56, v57
	v_perm_b32 v57, 0, v63, v170
	v_pk_fma_f16 v36, v37, v57, v36
	v_perm_b32 v37, v40, v40, s63
	s_waitcnt lgkmcnt(3)
	v_perm_b32 v40, 0, v64, v169
	v_pk_fma_f16 v38, v37, v40, v38
	v_perm_b32 v40, 0, v64, v170
	v_pk_fma_f16 v39, v37, v40, v39
	v_perm_b32 v40, 0, v65, v169
	v_pk_fma_f16 v40, v37, v40, v56
	v_perm_b32 v56, 0, v65, v170
	v_pk_fma_f16 v36, v37, v56, v36
	v_perm_b32 v37, v41, v41, s63
	s_waitcnt lgkmcnt(2)
	v_perm_b32 v41, 0, v66, v169
	v_pk_fma_f16 v38, v37, v41, v38
	v_perm_b32 v41, 0, v66, v170
	v_pk_fma_f16 v39, v37, v41, v39
	v_perm_b32 v41, 0, v67, v169
	v_pk_fma_f16 v40, v37, v41, v40
	v_perm_b32 v41, 0, v67, v170
	v_pk_fma_f16 v36, v37, v41, v36
	v_perm_b32 v37, v42, v42, s63
	s_waitcnt lgkmcnt(1)
	v_perm_b32 v41, 0, v68, v169
	v_pk_fma_f16 v38, v37, v41, v38
	v_perm_b32 v41, 0, v68, v170
	s_waitcnt vmcnt(22)
	v_bfe_u32 v73, v45, 16, 16
	v_pk_fma_f16 v39, v37, v41, v39
	v_perm_b32 v41, 0, v69, v169
	v_lshl_add_u32 v74, v73, 3, 0
	s_waitcnt vmcnt(21)
	v_bfe_u32 v73, v46, 16, 16
	v_pk_fma_f16 v40, v37, v41, v40
	v_perm_b32 v41, 0, v69, v170
	v_bfe_u32 v72, v43, 16, 16
	v_lshl_add_u32 v76, v73, 3, 0
	s_waitcnt vmcnt(20)
	v_bfe_u32 v73, v47, 16, 16
	v_pk_fma_f16 v36, v37, v41, v36
	v_perm_b32 v37, v44, v44, s63
	s_waitcnt lgkmcnt(0)
	v_perm_b32 v41, 0, v70, v169
	v_lshl_add_u32 v72, v72, 3, 0
	v_lshl_add_u32 v78, v73, 3, 0
	v_pk_fma_f16 v38, v37, v41, v38
	v_perm_b32 v41, 0, v70, v170
	ds_read_b64 v[72:73], v72
	ds_read_b64 v[74:75], v74
	ds_read_b64 v[76:77], v76
	ds_read_b64 v[78:79], v78
	v_pk_fma_f16 v39, v37, v41, v39
	v_perm_b32 v41, 0, v71, v169
	v_pk_fma_f16 v40, v37, v41, v40
	v_perm_b32 v41, 0, v71, v170
	v_pk_fma_f16 v36, v37, v41, v36
	v_perm_b32 v37, v43, v43, s63
	s_waitcnt lgkmcnt(3)
	v_perm_b32 v41, 0, v72, v169
	v_pk_fma_f16 v38, v37, v41, v38
	v_perm_b32 v41, 0, v72, v170
	v_pk_fma_f16 v39, v37, v41, v39
	v_perm_b32 v41, 0, v73, v169
	v_pk_fma_f16 v40, v37, v41, v40
	v_perm_b32 v41, 0, v73, v170
	v_pk_fma_f16 v36, v37, v41, v36
	v_perm_b32 v37, v45, v45, s63
	s_waitcnt lgkmcnt(2)
; #define VL_LOAD(wr, C) do { _Pragma("unroll") for (int i = 0; i < 16; ++i) wr[i] = wp[(size_t)((C) * 16 + i) * MROWS]; } while (0)
; #define VL_LOAD(wr, C) do { _Pragma("unroll") for (int i = 0; i < 16; ++i) wr[i] = wp[(size_t)((C) * 16 + i) * MROWS]; } while (0)
; template <bool RUN_L = true, bool RUN_G = true, bool DRY = false>
; __device__ __forceinline__ void phase_vaccH(unsigned char* ws, LAS unsigned char* lds, int layer, int G) {
;     ...
;                     VL_LOAD(wa, (c + 2) & 7);
	v_perm_b32 v41, 0, v74, v169
	v_pk_fma_f16 v38, v37, v41, v38
	v_perm_b32 v41, 0, v74, v170
	v_pk_fma_f16 v39, v37, v41, v39
	v_perm_b32 v41, 0, v75, v169
	v_pk_fma_f16 v40, v37, v41, v40
	v_perm_b32 v41, 0, v75, v170
	v_pk_fma_f16 v36, v37, v41, v36
	v_perm_b32 v37, v46, v46, s63
	s_waitcnt lgkmcnt(1)
	v_perm_b32 v41, 0, v76, v169
	v_pk_fma_f16 v38, v37, v41, v38
	v_perm_b32 v41, 0, v76, v170
	s_waitcnt vmcnt(18)
	v_bfe_u32 v81, v49, 16, 16
	v_pk_fma_f16 v39, v37, v41, v39
	v_perm_b32 v41, 0, v77, v169
	v_lshl_add_u32 v82, v81, 3, 0
	s_waitcnt vmcnt(17)
	v_bfe_u32 v81, v50, 16, 16
	v_pk_fma_f16 v40, v37, v41, v40
	v_perm_b32 v41, 0, v77, v170
	v_bfe_u32 v80, v48, 16, 16
	v_lshl_add_u32 v84, v81, 3, 0
	s_waitcnt vmcnt(16)
	v_bfe_u32 v81, v51, 16, 16
	v_pk_fma_f16 v36, v37, v41, v36
	v_perm_b32 v37, v47, v47, s63
	s_waitcnt lgkmcnt(0)
	v_perm_b32 v41, 0, v78, v169
	v_lshl_add_u32 v80, v80, 3, 0
	v_lshl_add_u32 v86, v81, 3, 0
	v_pk_fma_f16 v38, v37, v41, v38
	v_perm_b32 v41, 0, v78, v170
	ds_read_b64 v[80:81], v80
	ds_read_b64 v[82:83], v82
	ds_read_b64 v[84:85], v84
	ds_read_b64 v[86:87], v86
	v_pk_fma_f16 v39, v37, v41, v39
	v_perm_b32 v41, 0, v79, v169
	v_pk_fma_f16 v40, v37, v41, v40
	v_perm_b32 v41, 0, v79, v170
	v_pk_fma_f16 v36, v37, v41, v36
	v_perm_b32 v37, v48, v48, s63
	s_waitcnt lgkmcnt(3)
	v_perm_b32 v41, 0, v80, v169
	v_pk_fma_f16 v38, v37, v41, v38
	v_perm_b32 v41, 0, v80, v170
	v_pk_fma_f16 v39, v37, v41, v39
	v_perm_b32 v41, 0, v81, v169
	v_pk_fma_f16 v40, v37, v41, v40
	v_perm_b32 v41, 0, v81, v170
	v_pk_fma_f16 v36, v37, v41, v36
	v_perm_b32 v37, v49, v49, s63
	s_waitcnt lgkmcnt(2)
	v_perm_b32 v41, 0, v82, v169
	v_pk_fma_f16 v38, v37, v41, v38
	v_perm_b32 v41, 0, v82, v170
	v_pk_fma_f16 v39, v37, v41, v39
	v_perm_b32 v41, 0, v83, v169
	v_pk_fma_f16 v40, v37, v41, v40
	v_perm_b32 v41, 0, v83, v170
	v_pk_fma_f16 v36, v37, v41, v36
	v_perm_b32 v37, v50, v50, s63
	s_waitcnt lgkmcnt(1)
	v_perm_b32 v41, 0, v84, v169
	v_pk_fma_f16 v38, v37, v41, v38
	v_perm_b32 v41, 0, v84, v170
	v_pk_fma_f16 v39, v37, v41, v39
	v_perm_b32 v41, 0, v85, v169
	v_pk_fma_f16 v40, v37, v41, v40
	v_perm_b32 v41, 0, v85, v170
	v_pk_fma_f16 v36, v37, v41, v36
	v_perm_b32 v37, v51, v51, s63
	s_waitcnt lgkmcnt(0)
	v_perm_b32 v41, 0, v86, v169
	v_pk_fma_f16 v58, v37, v41, v38
	v_perm_b32 v38, 0, v86, v170
	v_pk_fma_f16 v59, v37, v38, v39
	v_perm_b32 v38, 0, v87, v169
	v_pk_fma_f16 v60, v37, v38, v40
	v_perm_b32 v38, 0, v87, v170
	v_pk_fma_f16 v61, v37, v38, v36
	s_and_b32 s8, s46, 0x60
	s_mul_i32 s8, s8, 0x8040
	s_add_u32 s98, s16, s8
	s_addc_u32 s99, s17, 0
	global_load_dword v36, v238, s[98:99]
	s_add_u32 s78, s98, s62
	s_addc_u32 s79, s99, 0
	global_load_dword v37, v238, s[78:79] offset:64
	s_add_u32 s78, s98, s56
	s_addc_u32 s79, s99, 0
	global_load_dword v38, v238, s[78:79] offset:128
	s_add_u32 s78, s98, s57
	s_addc_u32 s79, s99, 0
	global_load_dword v39, v238, s[78:79] offset:192
	s_add_u32 s78, s98, s64
	s_addc_u32 s79, s99, 0
	global_load_dword v40, v238, s[78:79] offset:256
	s_add_u32 s78, s98, s65
	s_addc_u32 s79, s99, 0
	global_load_dword v41, v238, s[78:79] offset:320
	s_add_u32 s78, s98, s66
	s_addc_u32 s79, s99, 0
	global_load_dword v42, v238, s[78:79] offset:384
	s_add_u32 s78, s98, s67
	s_addc_u32 s79, s99, 0
	global_load_dword v44, v238, s[78:79] offset:448
	s_add_u32 s78, s98, s68
	s_addc_u32 s79, s99, 0
	global_load_dword v43, v238, s[78:79] offset:512
	s_add_u32 s78, s98, s69
	s_addc_u32 s79, s99, 0
	global_load_dword v45, v238, s[78:79] offset:576
	s_add_u32 s78, s98, s70
	s_addc_u32 s79, s99, 0
	global_load_dword v46, v238, s[78:79] offset:640
	s_add_u32 s78, s98, s71
	s_addc_u32 s79, s99, 0
	global_load_dword v47, v238, s[78:79] offset:704
	s_add_u32 s78, s98, s72
	s_addc_u32 s79, s99, 0
	global_load_dword v48, v238, s[78:79] offset:768
	s_add_u32 s78, s98, s73
	s_addc_u32 s79, s99, 0
	global_load_dword v49, v238, s[78:79] offset:832
	s_add_u32 s78, s98, s74
	s_addc_u32 s79, s99, 0
	global_load_dword v50, v238, s[78:79] offset:896
	s_add_u32 s78, s98, s75
	s_addc_u32 s79, s99, 0
	global_load_dword v51, v238, s[78:79] offset:960
	s_waitcnt vmcnt(30)
	v_bfe_u32 v57, v31, 16, 16
	s_waitcnt vmcnt(29)
	v_bfe_u32 v62, v30, 16, 16
	s_waitcnt vmcnt(28)
	v_bfe_u32 v63, v29, 16, 16
	s_waitcnt vmcnt(27)
	v_bfe_u32 v64, v28, 16, 16
	v_perm_b32 v85, v31, v31, s63
	v_perm_b32 v86, v30, v30, s63
	v_perm_b32 v87, v29, v29, s63
	v_perm_b32 v88, v28, v28, s63
	v_cvt_f32_f16_e32 v28, v60
	v_lshrrev_b32_e32 v29, 16, v60
	v_cvt_f32_f16_e32 v29, v29
	v_cvt_f32_f16_e32 v30, v61
	v_lshrrev_b32_e32 v31, 16, v61
	v_cvt_f32_f16_e32 v31, v31
	v_bfe_u32 v56, v24, 16, 16
	s_waitcnt vmcnt(26)
	v_bfe_u32 v65, v27, 16, 16
	s_waitcnt vmcnt(25)
	v_bfe_u32 v66, v26, 16, 16
	s_waitcnt vmcnt(24)
	v_bfe_u32 v67, v25, 16, 16
	s_waitcnt vmcnt(23)
	v_bfe_u32 v68, v54, 16, 16
	s_waitcnt vmcnt(22)
	v_bfe_u32 v69, v53, 16, 16
	s_waitcnt vmcnt(21)
	v_bfe_u32 v70, v52, 16, 16
	s_waitcnt vmcnt(20)
	v_bfe_u32 v71, v35, 16, 16
	s_waitcnt vmcnt(19)
	v_bfe_u32 v72, v34, 16, 16
	s_waitcnt vmcnt(18)
	v_bfe_u32 v73, v33, 16, 16
	s_waitcnt vmcnt(17)
	v_bfe_u32 v74, v32, 16, 16
	s_waitcnt vmcnt(16)
; #define VL_LOAD(wr, C) do { _Pragma("unroll") for (int i = 0; i < 16; ++i) wr[i] = wp[(size_t)((C) * 16 + i) * MROWS]; } while (0)
; #define VL_LOAD(wr, C) do { _Pragma("unroll") for (int i = 0; i < 16; ++i) wr[i] = wp[(size_t)((C) * 16 + i) * MROWS]; } while (0)
; template <bool RUN_L = true, bool RUN_G = true, bool DRY = false>
; __device__ __forceinline__ void phase_vaccH(unsigned char* ws, LAS unsigned char* lds, int layer, int G) {
;     ...
; #pragma unroll 1
;                 for (int c = 0; c < 8; c += 2) {
;                     VL_LOAD(wb, c + 1);
;                     __builtin_amdgcn_sched_barrier(0);
;                     VL_CHUNK(wa);
;                     __builtin_amdgcn_sched_barrier(0);
;                     VL_LOAD(wa, (c + 2) & 7);
;                     __builtin_amdgcn_sched_barrier(0);
;                     VL_CHUNK(wb);
;                     __builtin_amdgcn_sched_barrier(0);
;                 }
	v_bfe_u32 v75, v55, 16, 16
	v_perm_b32 v84, v24, v24, s63
	v_perm_b32 v91, v25, v25, s63
	v_perm_b32 v92, v54, v54, s63
	v_perm_b32 v94, v52, v52, s63
	v_perm_b32 v96, v34, v34, s63
	v_perm_b32 v98, v32, v32, s63
	v_cvt_f32_f16_e32 v24, v58
	v_lshrrev_b32_e32 v25, 16, v58
	v_cvt_f32_f16_e32 v25, v25
	v_lshl_add_u32 v32, v56, 3, 0
	v_lshl_add_u32 v34, v57, 3, 0
	v_lshl_add_u32 v52, v62, 3, 0
	v_lshl_add_u32 v54, v63, 3, 0
	v_lshl_add_u32 v56, v64, 3, 0
	v_lshl_add_u32 v58, v65, 3, 0
	v_lshl_add_u32 v60, v66, 3, 0
	v_lshl_add_u32 v62, v67, 3, 0
	v_lshl_add_u32 v64, v68, 3, 0
	v_lshl_add_u32 v66, v69, 3, 0
	v_lshl_add_u32 v68, v70, 3, 0
	v_lshl_add_u32 v70, v71, 3, 0
	v_lshl_add_u32 v72, v72, 3, 0
	v_lshl_add_u32 v76, v73, 3, 0
	v_lshl_add_u32 v77, v74, 3, 0
	v_lshl_add_u32 v78, v75, 3, 0
	v_perm_b32 v89, v27, v27, s63
	v_perm_b32 v90, v26, v26, s63
	v_perm_b32 v93, v53, v53, s63
	v_perm_b32 v95, v35, v35, s63
	v_perm_b32 v97, v33, v33, s63
	v_perm_b32 v99, v55, v55, s63
	v_cvt_f32_f16_e32 v26, v59
	v_lshrrev_b32_e32 v27, 16, v59
	v_cvt_f32_f16_e32 v27, v27
	ds_read_b64 v[32:33], v32
	ds_read_b64 v[34:35], v34
	ds_read_b64 v[52:53], v52
	ds_read_b64 v[54:55], v54
	ds_read_b64 v[56:57], v56
	ds_read_b64 v[58:59], v58
	ds_read_b64 v[60:61], v60
	ds_read_b64 v[62:63], v62
	ds_read_b64 v[64:65], v64
	ds_read_b64 v[66:67], v66
	ds_read_b64 v[68:69], v68
	ds_read_b64 v[70:71], v70
	ds_read_b64 v[72:73], v72
	ds_read_b64 v[74:75], v76
	ds_read_b64 v[76:77], v77
	ds_read_b64 v[78:79], v78
	v_pk_add_f32 v[22:23], v[22:23], v[28:29]
	v_pk_add_f32 v[20:21], v[20:21], v[30:31]
	s_waitcnt lgkmcnt(14)
	v_perm_b32 v28, 0, v32, v169
	v_perm_b32 v29, 0, v32, v170
	v_perm_b32 v30, 0, v33, v169
	v_perm_b32 v31, 0, v33, v170
	v_perm_b32 v32, 0, v34, v169
	v_perm_b32 v33, 0, v34, v170
	v_perm_b32 v34, 0, v35, v169
	v_perm_b32 v35, 0, v35, v170
	v_pk_fma_f16 v28, v84, v28, 0
	v_pk_fma_f16 v29, v84, v29, 0
	v_pk_fma_f16 v30, v84, v30, 0
	v_pk_fma_f16 v31, v84, v31, 0
	s_waitcnt lgkmcnt(13)
	v_perm_b32 v100, 0, v52, v169
	v_perm_b32 v52, 0, v52, v170
	v_perm_b32 v101, 0, v53, v169
	v_perm_b32 v53, 0, v53, v170
	v_pk_fma_f16 v28, v85, v32, v28
	v_pk_fma_f16 v29, v85, v33, v29
	v_pk_fma_f16 v30, v85, v34, v30
	v_pk_fma_f16 v31, v85, v35, v31
	s_waitcnt lgkmcnt(12)
	v_perm_b32 v102, 0, v54, v169
	v_perm_b32 v54, 0, v54, v170
	v_perm_b32 v103, 0, v55, v169
	v_perm_b32 v55, 0, v55, v170
	v_pk_fma_f16 v28, v86, v100, v28
	v_pk_fma_f16 v29, v86, v52, v29
	v_pk_fma_f16 v30, v86, v101, v30
	v_pk_fma_f16 v31, v86, v53, v31
	s_waitcnt lgkmcnt(11)
	v_perm_b32 v104, 0, v56, v169
	v_perm_b32 v56, 0, v56, v170
	v_perm_b32 v105, 0, v57, v169
	v_perm_b32 v57, 0, v57, v170
	v_pk_fma_f16 v28, v87, v102, v28
	v_pk_fma_f16 v29, v87, v54, v29
	v_pk_fma_f16 v30, v87, v103, v30
	v_pk_fma_f16 v31, v87, v55, v31
	s_waitcnt lgkmcnt(10)
	v_perm_b32 v106, 0, v58, v169
	v_perm_b32 v58, 0, v58, v170
	v_perm_b32 v107, 0, v59, v169
	v_perm_b32 v59, 0, v59, v170
	v_pk_fma_f16 v28, v88, v104, v28
	v_pk_fma_f16 v29, v88, v56, v29
	v_pk_fma_f16 v30, v88, v105, v30
	v_pk_fma_f16 v31, v88, v57, v31
	s_waitcnt lgkmcnt(9)
	v_perm_b32 v108, 0, v60, v169
	v_perm_b32 v60, 0, v60, v170
	v_perm_b32 v109, 0, v61, v169
	v_perm_b32 v61, 0, v61, v170
	v_pk_fma_f16 v28, v89, v106, v28
	v_pk_fma_f16 v29, v89, v58, v29
	v_pk_fma_f16 v30, v89, v107, v30
	v_pk_fma_f16 v31, v89, v59, v31
	s_waitcnt lgkmcnt(8)
	v_perm_b32 v110, 0, v62, v169
	v_perm_b32 v62, 0, v62, v170
	v_perm_b32 v111, 0, v63, v169
	v_perm_b32 v63, 0, v63, v170
	v_pk_fma_f16 v28, v90, v108, v28
	v_pk_fma_f16 v29, v90, v60, v29
	v_pk_fma_f16 v30, v90, v109, v30
	v_pk_fma_f16 v31, v90, v61, v31
	s_waitcnt lgkmcnt(7)
	v_perm_b32 v112, 0, v64, v169
	v_perm_b32 v64, 0, v64, v170
	v_perm_b32 v113, 0, v65, v169
	v_perm_b32 v65, 0, v65, v170
	v_pk_fma_f16 v28, v91, v110, v28
	v_pk_fma_f16 v29, v91, v62, v29
	v_pk_fma_f16 v30, v91, v111, v30
	v_pk_fma_f16 v31, v91, v63, v31
	s_waitcnt lgkmcnt(6)
	v_perm_b32 v114, 0, v66, v169
	v_perm_b32 v66, 0, v66, v170
	v_perm_b32 v115, 0, v67, v169
	v_perm_b32 v67, 0, v67, v170
	v_pk_fma_f16 v28, v92, v112, v28
	v_pk_fma_f16 v29, v92, v64, v29
	v_pk_fma_f16 v30, v92, v113, v30
	v_pk_fma_f16 v31, v92, v65, v31
	s_waitcnt lgkmcnt(5)
	v_perm_b32 v116, 0, v68, v169
	v_perm_b32 v68, 0, v68, v170
	v_perm_b32 v117, 0, v69, v169
	v_perm_b32 v69, 0, v69, v170
	v_pk_fma_f16 v28, v93, v114, v28
	v_pk_fma_f16 v29, v93, v66, v29
	v_pk_fma_f16 v30, v93, v115, v30
	v_pk_fma_f16 v31, v93, v67, v31
	s_waitcnt lgkmcnt(4)
	v_perm_b32 v118, 0, v70, v169
	v_perm_b32 v70, 0, v70, v170
	v_perm_b32 v119, 0, v71, v169
	v_perm_b32 v71, 0, v71, v170
	v_pk_fma_f16 v28, v94, v116, v28
	v_pk_fma_f16 v29, v94, v68, v29
	v_pk_fma_f16 v30, v94, v117, v30
	v_pk_fma_f16 v31, v94, v69, v31
	s_waitcnt lgkmcnt(3)
	v_perm_b32 v120, 0, v72, v169
	v_perm_b32 v72, 0, v72, v170
	v_perm_b32 v121, 0, v73, v169
	v_perm_b32 v73, 0, v73, v170
	v_pk_fma_f16 v28, v95, v118, v28
	v_pk_fma_f16 v29, v95, v70, v29
	v_pk_fma_f16 v30, v95, v119, v30
	v_pk_fma_f16 v31, v95, v71, v31
	s_waitcnt lgkmcnt(2)
	v_perm_b32 v122, 0, v74, v169
	v_perm_b32 v74, 0, v74, v170
	v_perm_b32 v123, 0, v75, v169
	v_perm_b32 v75, 0, v75, v170
	v_pk_fma_f16 v28, v96, v120, v28
	v_pk_fma_f16 v29, v96, v72, v29
	v_pk_fma_f16 v30, v96, v121, v30
	v_pk_fma_f16 v31, v96, v73, v31
	s_waitcnt lgkmcnt(1)
	v_perm_b32 v124, 0, v76, v169
	v_perm_b32 v76, 0, v76, v170
	v_perm_b32 v125, 0, v77, v169
	v_perm_b32 v77, 0, v77, v170
	v_pk_fma_f16 v28, v97, v122, v28
	v_pk_fma_f16 v29, v97, v74, v29
	v_pk_fma_f16 v30, v97, v123, v30
	v_pk_fma_f16 v31, v97, v75, v31
	s_waitcnt lgkmcnt(0)
	v_perm_b32 v126, 0, v78, v169
	v_perm_b32 v78, 0, v78, v170
	v_perm_b32 v127, 0, v79, v169
	v_perm_b32 v79, 0, v79, v170
	v_pk_fma_f16 v28, v98, v124, v28
	v_pk_fma_f16 v29, v98, v76, v29
	v_pk_fma_f16 v30, v98, v125, v30
	v_pk_fma_f16 v31, v98, v77, v31
	v_pk_fma_f16 v33, v99, v126, v28
	v_pk_fma_f16 v52, v99, v78, v29
	v_pk_fma_f16 v29, v99, v127, v30
	v_pk_fma_f16 v31, v99, v79, v31
	v_cvt_f32_f16_e32 v32, v33
	v_cvt_f32_f16_e32 v30, v52
	v_cvt_f32_f16_e32 v28, v29
	v_cvt_f32_f16_e32 v34, v31
	v_lshrrev_b32_e32 v35, 16, v31
	v_cvt_f32_f16_e32 v35, v35
	v_lshrrev_b32_e32 v29, 16, v29
	v_cvt_f32_f16_e32 v29, v29
	v_lshrrev_b32_e32 v31, 16, v52
	v_cvt_f32_f16_e32 v31, v31
	v_lshrrev_b32_e32 v33, 16, v33
	v_cvt_f32_f16_e32 v33, v33
	v_pk_add_f32 v[80:81], v[18:19], v[24:25]
	v_pk_add_f32 v[82:83], v[16:17], v[26:27]
	v_pk_add_f32 v[20:21], v[20:21], v[34:35]
	v_pk_add_f32 v[22:23], v[22:23], v[28:29]
	v_pk_add_f32 v[34:35], v[82:83], v[30:31]
	v_pk_add_f32 v[28:29], v[80:81], v[32:33]
	s_add_u32 s76, s76, s20
	s_addc_u32 s77, s77, s21
	s_add_i32 s46, s46, 32
	s_add_i32 s47, s47, 2
	s_cmp_lt_u32 s47, 6
	v_lshl_add_u64 v[14:15], v[14:15], 0, s[20:21]
	s_cbranch_scc1 .LBB0_1242
; template <bool RUN_L = true, bool RUN_G = true, bool DRY = false>
; __device__ __forceinline__ void phase_vaccH(unsigned char* ws, LAS unsigned char* lds, int layer, int G) {
;     ...
;                 if (valid) { hp[0] = h0 + (f32x4){accf[0], accf[1], accf[2], accf[3]}; hp[1] = h1 + (f32x4){accf[4], accf[5], accf[6], accf[7]}; }
	s_and_saveexec_b64 s[46:47], s[6:7]
	s_cbranch_execz .LBB0_1240
	v_pk_add_f32 v[12:13], v[18:19], v[24:25]
	v_pk_add_f32 v[14:15], v[16:17], v[26:27]
	v_pk_add_f32 v[12:13], v[12:13], v[32:33]
	v_pk_add_f32 v[14:15], v[14:15], v[30:31]
	v_pk_add_f32 v[6:7], v[6:7], v[12:13]
	v_pk_add_f32 v[8:9], v[8:9], v[14:15]
	v_pk_add_f32 v[4:5], v[4:5], v[20:21]
	v_pk_add_f32 v[2:3], v[2:3], v[22:23]
	global_store_dwordx4 v[10:11], v[6:9], off
	global_store_dwordx4 v[10:11], v[2:5], off offset:16
	s_branch .LBB0_1240

; #define LAS __attribute__((address_space(3)))
; template <bool RUN_L = true, bool RUN_G = true, bool DRY = false>
; __device__ __forceinline__ void phase_vaccH(unsigned char* ws, LAS unsigned char* lds, int layer, int G) {
;     ...
;     for (int cg = blockIdx.x; cg < NGRP; cg += G) {
;         __syncthreads();
;         { const u32x4* src = (const u32x4*)(pvl + (size_t)cg * (NEXP * 8)) + tid; u32x4 t_[16];
; #pragma unroll
;           for (int i = 0; i < 16; ++i) t_[i] = src[512 * i];
; #pragma unroll
;           for (int i = 0; i < 16; ++i) ((LAS u32x4*)lds)[tid + 512 * i] = t_[i]; }
;         __syncthreads();
;         if (wid < 4) { if (RUN_L) {
.LBB0_1976:
	s_ashr_i32 s23, s22, 31
	s_lshl_b64 s[24:25], s[22:23], 17
	s_waitcnt vmcnt(15)
	v_lshl_add_u64 v[58:59], v[130:131], 0, s[24:25]
	s_waitcnt vmcnt(2)
	v_add_co_u32_e32 v6, vcc, 0x2000, v58
	s_nop 1
	v_addc_co_u32_e32 v7, vcc, 0, v59, vcc
	v_add_co_u32_e32 v10, vcc, 0x4000, v58
	s_barrier
	s_waitcnt vmcnt(2)
	v_addc_co_u32_e32 v11, vcc, 0, v59, vcc
	v_add_co_u32_e32 v14, vcc, 0x6000, v58
	s_nop 1
	v_addc_co_u32_e32 v15, vcc, 0, v59, vcc
	v_add_co_u32_e32 v18, vcc, 0x8000, v58
	global_load_dwordx4 v[2:5], v[58:59], off
	s_nop 0
	global_load_dwordx4 v[6:9], v[6:7], off
	v_addc_co_u32_e32 v19, vcc, 0, v59, vcc
	v_add_co_u32_e32 v22, vcc, 0xa000, v58
	global_load_dwordx4 v[10:13], v[10:11], off
	s_nop 0
	global_load_dwordx4 v[14:17], v[14:15], off
	v_addc_co_u32_e32 v23, vcc, 0, v59, vcc
	v_add_co_u32_e32 v26, vcc, 0xc000, v58
	global_load_dwordx4 v[18:21], v[18:19], off
	s_nop 0
	global_load_dwordx4 v[22:25], v[22:23], off
	v_addc_co_u32_e32 v27, vcc, 0, v59, vcc
	v_add_co_u32_e32 v30, vcc, 0xe000, v58
	s_mov_b64 s[28:29], -1
	s_nop 0
	v_addc_co_u32_e32 v31, vcc, 0, v59, vcc
	v_add_co_u32_e32 v34, vcc, s41, v58
	global_load_dwordx4 v[26:29], v[26:27], off
	s_nop 0
	global_load_dwordx4 v[30:33], v[30:31], off
	v_addc_co_u32_e32 v35, vcc, 0, v59, vcc
	v_add_co_u32_e32 v38, vcc, s42, v58
	s_nop 1
	v_addc_co_u32_e32 v39, vcc, 0, v59, vcc
	v_add_co_u32_e32 v42, vcc, s43, v58
	global_load_dwordx4 v[34:37], v[34:35], off
	s_nop 0
	global_load_dwordx4 v[38:41], v[38:39], off
	s_waitcnt vmcnt(11)
	v_addc_co_u32_e32 v43, vcc, 0, v59, vcc
	v_add_co_u32_e32 v46, vcc, s44, v58
	s_nop 1
	v_addc_co_u32_e32 v47, vcc, 0, v59, vcc
	v_add_co_u32_e32 v50, vcc, s45, v58
	global_load_dwordx4 v[42:45], v[42:43], off
	s_nop 0
	global_load_dwordx4 v[46:49], v[46:47], off
	v_addc_co_u32_e32 v51, vcc, 0, v59, vcc
	v_add_co_u32_e32 v54, vcc, s46, v58
	s_nop 1
	v_addc_co_u32_e32 v55, vcc, 0, v59, vcc
	v_add_co_u32_e32 v60, vcc, s47, v58
	global_load_dwordx4 v[50:53], v[50:51], off
	s_nop 0
	global_load_dwordx4 v[54:57], v[54:55], off
	v_addc_co_u32_e32 v61, vcc, 0, v59, vcc
	v_add_co_u32_e32 v62, vcc, s48, v58
	s_nop 1
	v_addc_co_u32_e32 v63, vcc, 0, v59, vcc
	global_load_dwordx4 v[58:61], v[60:61], off
	s_nop 0
	global_load_dwordx4 v[62:65], v[62:63], off
	s_and_b64 vcc, exec, s[10:11]
	s_waitcnt vmcnt(15)
	ds_write_b128 v158, v[2:5]
	s_waitcnt vmcnt(14)
	ds_write_b128 v158, v[6:9] offset:8192
	s_waitcnt vmcnt(13)
	ds_write_b128 v158, v[10:13] offset:16384
	s_waitcnt vmcnt(12)
	ds_write_b128 v158, v[14:17] offset:24576
	s_waitcnt vmcnt(11)
	ds_write_b128 v158, v[18:21] offset:32768
	s_waitcnt vmcnt(10)
	ds_write_b128 v158, v[22:25] offset:40960
	s_waitcnt vmcnt(9)
	ds_write_b128 v158, v[26:29] offset:49152
	s_waitcnt vmcnt(8)
	ds_write_b128 v158, v[30:33] offset:57344
	s_waitcnt vmcnt(7)
	ds_write_b128 v160, v[34:37]
	s_waitcnt vmcnt(6)
	ds_write_b128 v161, v[38:41]
	s_waitcnt vmcnt(5)
	ds_write_b128 v162, v[42:45]
	s_waitcnt vmcnt(4)
	ds_write_b128 v163, v[46:49]
	s_waitcnt vmcnt(3)
	ds_write_b128 v164, v[50:53]
	s_waitcnt vmcnt(2)
	ds_write_b128 v165, v[54:57]
	s_waitcnt vmcnt(1)
	ds_write_b128 v166, v[58:61]
	s_waitcnt vmcnt(0)
	ds_write_b128 v167, v[62:65]
	s_waitcnt lgkmcnt(0)
	s_barrier
	s_cbranch_vccz .LBB0_1983
	s_or_b64 s[6:7], s[12:13], s[6:7]
	s_and_b64 vcc, exec, s[6:7]
	s_cbranch_vccnz .LBB0_1982
; #define VD_IDS(pw, IT) do { const int t_ = (IT) - ((IT) / MROWS) * MROWS; const unsigned* wp_ = WLP + (size_t)t_ * 128 + r8 * 16 + (lane & 3); \
;         pw[0] = wp_[0]; pw[1] = wp_[4]; pw[2] = wp_[8]; pw[3] = wp_[12]; } while (0)
; #define VD_IDS(pw, IT) do { const int t_ = (IT) - ((IT) / MROWS) * MROWS; const unsigned* wp_ = WLP + (size_t)t_ * 128 + r8 * 16 + (lane & 3); \
;         pw[0] = wp_[0]; pw[1] = wp_[4]; pw[2] = wp_[8]; pw[3] = wp_[12]; } while (0)
; template <bool RUN_L = true, bool RUN_G = true, bool DRY = false>
; __device__ __forceinline__ void phase_vaccH(unsigned char* ws, LAS unsigned char* lds, int layer, int G) {
;     ...
;             if (g < NIT) {
;                 u32x4 ra[16], rc[16]; unsigned pka[16], pkc[16]; f32x2 hva, hvc; f32x2* hpa; f32x2* hpc;
;                 unsigned pw0[4], pw1[4];
;                 VD_IDS(pw0, g);
;                 { const int i1c = g + NG < NIT ? g + NG : g; VD_IDS(pw1, i1c); }
;                 VD_ISSUE(ra, pka, hva, hpa, pw0, g);
	global_load_dword v2, v[136:137], off
	global_load_dword v3, v[136:137], off offset:16
	global_load_dword v4, v[136:137], off offset:32
	global_load_dword v5, v[136:137], off offset:48
	global_load_dword v191, v[138:139], off offset:48
	global_load_dword v193, v[138:139], off offset:32
	global_load_dword v194, v[138:139], off offset:16
	global_load_dword v195, v[138:139], off
	v_mov_b64_e32 v[156:157], v[142:143]
	s_mov_b32 s6, s35
	s_waitcnt vmcnt(7)
	v_mov_b32_dpp v187, v2 quad_perm:[0,0,0,0] row_mask:0xf bank_mask:0xf bound_ctrl:1
	v_mov_b32_dpp v186, v2 quad_perm:[1,1,1,1] row_mask:0xf bank_mask:0xf bound_ctrl:1
	v_mov_b32_dpp v185, v2 quad_perm:[2,2,2,2] row_mask:0xf bank_mask:0xf bound_ctrl:1
	s_waitcnt vmcnt(4)
	v_mov_b32_dpp v172, v5 quad_perm:[3,3,3,3] row_mask:0xf bank_mask:0xf bound_ctrl:1
	v_mov_b32_dpp v173, v5 quad_perm:[2,2,2,2] row_mask:0xf bank_mask:0xf bound_ctrl:1
	v_lshrrev_b32_e32 v132, 16, v172
	v_lshlrev_b32_e32 v132, v168, v132
	v_mov_b32_dpp v184, v2 quad_perm:[3,3,3,3] row_mask:0xf bank_mask:0xf bound_ctrl:1
	v_mov_b32_dpp v183, v3 quad_perm:[0,0,0,0] row_mask:0xf bank_mask:0xf bound_ctrl:1
	v_mov_b32_dpp v182, v3 quad_perm:[1,1,1,1] row_mask:0xf bank_mask:0xf bound_ctrl:1
	v_mov_b32_dpp v181, v3 quad_perm:[2,2,2,2] row_mask:0xf bank_mask:0xf bound_ctrl:1
	v_mov_b32_dpp v180, v3 quad_perm:[3,3,3,3] row_mask:0xf bank_mask:0xf bound_ctrl:1
	v_mov_b32_dpp v174, v5 quad_perm:[1,1,1,1] row_mask:0xf bank_mask:0xf bound_ctrl:1
	v_lshl_add_u64 v[2:3], v[140:141], 0, v[132:133]
	v_lshrrev_b32_e32 v132, 16, v173
	v_lshlrev_b32_e32 v132, v168, v132
	v_mov_b32_dpp v175, v5 quad_perm:[0,0,0,0] row_mask:0xf bank_mask:0xf bound_ctrl:1
	v_lshl_add_u64 v[6:7], v[140:141], 0, v[132:133]
	v_lshrrev_b32_e32 v132, 16, v174
	v_lshlrev_b32_e32 v132, v168, v132
	v_mov_b32_dpp v176, v4 quad_perm:[3,3,3,3] row_mask:0xf bank_mask:0xf bound_ctrl:1
	v_lshl_add_u64 v[10:11], v[140:141], 0, v[132:133]
	v_lshrrev_b32_e32 v132, 16, v175
	v_lshlrev_b32_e32 v132, v168, v132
	v_mov_b32_dpp v177, v4 quad_perm:[2,2,2,2] row_mask:0xf bank_mask:0xf bound_ctrl:1
	v_lshl_add_u64 v[14:15], v[140:141], 0, v[132:133]
	v_lshrrev_b32_e32 v132, 16, v176
	v_lshlrev_b32_e32 v132, v168, v132
	v_mov_b32_dpp v178, v4 quad_perm:[1,1,1,1] row_mask:0xf bank_mask:0xf bound_ctrl:1
	v_lshl_add_u64 v[18:19], v[140:141], 0, v[132:133]
	v_lshrrev_b32_e32 v132, 16, v177
	v_lshlrev_b32_e32 v132, v168, v132
	v_mov_b32_dpp v179, v4 quad_perm:[0,0,0,0] row_mask:0xf bank_mask:0xf bound_ctrl:1
	v_lshl_add_u64 v[22:23], v[140:141], 0, v[132:133]
	v_lshrrev_b32_e32 v132, 16, v178
	v_lshlrev_b32_e32 v132, v168, v132
	v_lshl_add_u64 v[26:27], v[140:141], 0, v[132:133]
	v_lshrrev_b32_e32 v132, 16, v179
	v_lshlrev_b32_e32 v132, v168, v132
	v_lshl_add_u64 v[30:31], v[140:141], 0, v[132:133]
	v_lshrrev_b32_e32 v132, 16, v180
	v_lshlrev_b32_e32 v132, v168, v132
	v_lshl_add_u64 v[34:35], v[140:141], 0, v[132:133]
	v_lshrrev_b32_e32 v132, 16, v181
	v_lshlrev_b32_e32 v132, v168, v132
	v_lshl_add_u64 v[38:39], v[140:141], 0, v[132:133]
	v_lshrrev_b32_e32 v132, 16, v182
	v_lshlrev_b32_e32 v132, v168, v132
	v_lshl_add_u64 v[42:43], v[140:141], 0, v[132:133]
	v_lshrrev_b32_e32 v132, 16, v183
	v_lshlrev_b32_e32 v132, v168, v132
	v_lshl_add_u64 v[46:47], v[140:141], 0, v[132:133]
	v_lshrrev_b32_e32 v132, 16, v184
	v_lshlrev_b32_e32 v132, v168, v132
	v_lshl_add_u64 v[50:51], v[140:141], 0, v[132:133]
	v_lshrrev_b32_e32 v132, 16, v185
	v_lshlrev_b32_e32 v132, v168, v132
	v_lshl_add_u64 v[54:55], v[140:141], 0, v[132:133]
	v_lshrrev_b32_e32 v132, 16, v186
	v_lshlrev_b32_e32 v132, v168, v132
	v_lshl_add_u64 v[58:59], v[140:141], 0, v[132:133]
	v_lshrrev_b32_e32 v132, 16, v187
	v_lshlrev_b32_e32 v132, v168, v132
	v_lshl_add_u64 v[62:63], v[140:141], 0, v[132:133]
	global_load_dwordx2 v[150:151], v[142:143], off
	s_nop 0
	global_load_dwordx4 v[2:5], v[2:3], off
	s_nop 0
	global_load_dwordx4 v[6:9], v[6:7], off
	s_nop 0
	global_load_dwordx4 v[10:13], v[10:11], off
	s_nop 0
	global_load_dwordx4 v[14:17], v[14:15], off
	s_nop 0
	global_load_dwordx4 v[18:21], v[18:19], off
	s_nop 0
	global_load_dwordx4 v[22:25], v[22:23], off
	s_nop 0
	global_load_dwordx4 v[26:29], v[26:27], off
	s_nop 0
	global_load_dwordx4 v[30:33], v[30:31], off
	s_nop 0
	global_load_dwordx4 v[34:37], v[34:35], off
	s_nop 0
	global_load_dwordx4 v[38:41], v[38:39], off
	s_nop 0
	global_load_dwordx4 v[42:45], v[42:43], off
	s_nop 0
	global_load_dwordx4 v[46:49], v[46:47], off
	s_nop 0
	global_load_dwordx4 v[50:53], v[50:51], off
	s_nop 0
	global_load_dwordx4 v[54:57], v[54:55], off
	s_nop 0
	global_load_dwordx4 v[58:61], v[58:59], off
	s_nop 0
	global_load_dwordx4 v[62:65], v[62:63], off
	s_branch .LBB0_1980

; #define VD_IDS(pw, IT) do { const int t_ = (IT) - ((IT) / MROWS) * MROWS; const unsigned* wp_ = WLP + (size_t)t_ * 128 + r8 * 16 + (lane & 3); \
;         pw[0] = wp_[0]; pw[1] = wp_[4]; pw[2] = wp_[8]; pw[3] = wp_[12]; } while (0)
; #define VD_IDS(pw, IT) do { const int t_ = (IT) - ((IT) / MROWS) * MROWS; const unsigned* wp_ = WLP + (size_t)t_ * 128 + r8 * 16 + (lane & 3); \
;         pw[0] = wp_[0]; pw[1] = wp_[4]; pw[2] = wp_[8]; pw[3] = wp_[12]; } while (0)
; template <bool RUN_L = true, bool RUN_G = true, bool DRY = false>
; __device__ __forceinline__ void phase_vaccH(unsigned char* ws, LAS unsigned char* lds, int layer, int G) {
;     ...
;                 for (int item = g; item < NIT; item += 2 * NG) {
;                     const int i1 = item + NG, i2 = item + 2 * NG, i3 = item + 3 * NG;
;                     const bool v1 = i1 < NIT;
;                     const int i1c = v1 ? i1 : item, i2c = i2 < NIT ? i2 : item, i3c = i3 < NIT ? i3 : item;
;                     VD_IDS(pw0, i2c);
;                     __builtin_amdgcn_sched_barrier(0);
;                     VD_ISSUE(rc, pkc, hvc, hpc, pw1, i1c);
.LBB0_1980:
	s_add_i32 s8, s6, s38
	s_add_i32 s7, s49, s6
	s_add_i32 s23, s50, s6
	s_cmpk_lt_i32 s8, 0x4020
	s_cselect_b32 s30, s8, s6
	s_cmpk_lt_i32 s7, 0x4020
	s_cselect_b32 s7, s7, s6
	s_mul_hi_i32 s24, s7, 0x7fc01ff1
	s_lshr_b32 s25, s24, 31
	s_ashr_i32 s24, s24, 12
	s_add_i32 s33, s24, s25
	s_mul_i32 s24, s33, 0xffffdff0
	s_add_i32 s24, s24, s7
	s_ashr_i32 s25, s24, 31
	s_lshl_b64 s[28:29], s[24:25], 9
	v_lshl_add_u64 v[66:67], v[144:145], 0, s[28:29]
	global_load_dword v211, v[66:67], off
	global_load_dword v210, v[66:67], off offset:16
	global_load_dword v209, v[66:67], off offset:32
	global_load_dword v208, v[66:67], off offset:48
	s_mul_hi_i32 s7, s30, 0x7fc01ff1
	s_lshr_b32 s28, s7, 31
	s_ashr_i32 s7, s7, 12
	s_add_i32 s7, s7, s28
	s_lshl_b32 s28, s7, 10
	s_or_b32 s66, s28, s40
	s_ashr_i32 s67, s66, 31
	s_cmpk_lt_i32 s23, 0x4020
	s_mulk_i32 s7, 0xdff0
	s_cselect_b32 s23, s23, s6
	s_add_i32 s6, s7, s30
	s_ashr_i32 s7, s6, 31
	s_lshl_b64 s[6:7], s[6:7], 14
	s_add_u32 s28, s94, s6
	s_addc_u32 s29, s95, s7
	s_lshl_b64 s[6:7], s[66:67], 2
	s_add_u32 s36, s28, s6
	s_mul_hi_i32 s6, s23, 0x7fc01ff1
	s_addc_u32 s37, s29, s7
	s_lshr_b32 s7, s6, 31
	s_ashr_i32 s6, s6, 12
	s_add_i32 s6, s6, s7
	s_mulk_i32 s6, 0x2010
	s_sub_i32 s6, s23, s6
	s_ashr_i32 s7, s6, 31
	s_lshl_b64 s[30:31], s[6:7], 9
	s_lshl_b32 s6, s33, 10
	s_or_b32 s28, s6, s40
	s_ashr_i32 s29, s28, 31
	s_lshl_b64 s[6:7], s[24:25], 14
	s_add_u32 s23, s94, s6
	s_addc_u32 s24, s95, s7
	s_lshl_b64 s[6:7], s[28:29], 2
	s_add_u32 s6, s23, s6
	s_addc_u32 s7, s24, s7
	s_cmpk_gt_i32 s8, 0x401f
	s_waitcnt vmcnt(21)
	v_mov_b32_dpp v207, v195 quad_perm:[0,0,0,0] row_mask:0xf bank_mask:0xf bound_ctrl:1
	v_mov_b32_dpp v206, v195 quad_perm:[1,1,1,1] row_mask:0xf bank_mask:0xf bound_ctrl:1
	v_lshl_add_u64 v[66:67], v[134:135], 0, s[66:67]
	v_lshrrev_b32_e32 v132, 16, v207
	v_lshlrev_b32_e32 v132, v168, v132
	v_mov_b32_dpp v205, v195 quad_perm:[2,2,2,2] row_mask:0xf bank_mask:0xf bound_ctrl:1
	s_waitcnt lgkmcnt(0)
	v_lshl_add_u64 v[68:69], v[66:67], 0, v[132:133]
	v_lshrrev_b32_e32 v132, 16, v206
	v_lshlrev_b32_e32 v132, v168, v132
	v_mov_b32_dpp v204, v195 quad_perm:[3,3,3,3] row_mask:0xf bank_mask:0xf bound_ctrl:1
	v_lshl_add_u64 v[70:71], v[66:67], 0, v[132:133]
	v_lshrrev_b32_e32 v132, 16, v205
	v_lshlrev_b32_e32 v132, v168, v132
	v_mov_b32_dpp v203, v194 quad_perm:[0,0,0,0] row_mask:0xf bank_mask:0xf bound_ctrl:1
	global_load_dwordx4 v[126:129], v[68:69], off
	global_load_dwordx4 v[122:125], v[70:71], off
	v_lshl_add_u64 v[68:69], v[66:67], 0, v[132:133]
	v_lshrrev_b32_e32 v132, 16, v204
	v_lshlrev_b32_e32 v132, v168, v132
	v_mov_b32_dpp v202, v194 quad_perm:[1,1,1,1] row_mask:0xf bank_mask:0xf bound_ctrl:1
	v_lshl_add_u64 v[70:71], v[66:67], 0, v[132:133]
	v_lshrrev_b32_e32 v132, 16, v203
	v_lshlrev_b32_e32 v132, v168, v132
	v_mov_b32_dpp v201, v194 quad_perm:[2,2,2,2] row_mask:0xf bank_mask:0xf bound_ctrl:1
	global_load_dwordx4 v[118:121], v[68:69], off
	global_load_dwordx4 v[114:117], v[70:71], off
	v_lshl_add_u64 v[68:69], v[66:67], 0, v[132:133]
	v_lshrrev_b32_e32 v132, 16, v202
	v_lshlrev_b32_e32 v132, v168, v132
	v_mov_b32_dpp v200, v194 quad_perm:[3,3,3,3] row_mask:0xf bank_mask:0xf bound_ctrl:1
	v_lshl_add_u64 v[70:71], v[66:67], 0, v[132:133]
	v_lshrrev_b32_e32 v132, 16, v201
	v_lshlrev_b32_e32 v132, v168, v132
	v_mov_b32_dpp v199, v193 quad_perm:[0,0,0,0] row_mask:0xf bank_mask:0xf bound_ctrl:1
	global_load_dwordx4 v[110:113], v[68:69], off
	global_load_dwordx4 v[106:109], v[70:71], off
	v_lshl_add_u64 v[68:69], v[66:67], 0, v[132:133]
	v_lshrrev_b32_e32 v132, 16, v200
	v_lshlrev_b32_e32 v132, v168, v132
	v_mov_b32_dpp v198, v193 quad_perm:[1,1,1,1] row_mask:0xf bank_mask:0xf bound_ctrl:1
	v_lshl_add_u64 v[70:71], v[66:67], 0, v[132:133]
	v_lshrrev_b32_e32 v132, 16, v199
	v_lshlrev_b32_e32 v132, v168, v132
	v_mov_b32_dpp v197, v193 quad_perm:[2,2,2,2] row_mask:0xf bank_mask:0xf bound_ctrl:1
	global_load_dwordx4 v[102:105], v[68:69], off
	global_load_dwordx4 v[98:101], v[70:71], off
	v_lshl_add_u64 v[68:69], v[66:67], 0, v[132:133]
	v_lshrrev_b32_e32 v132, 16, v198
	v_lshlrev_b32_e32 v132, v168, v132
	v_mov_b32_dpp v196, v193 quad_perm:[3,3,3,3] row_mask:0xf bank_mask:0xf bound_ctrl:1
	v_lshl_add_u64 v[70:71], v[66:67], 0, v[132:133]
	v_lshrrev_b32_e32 v132, 16, v197
	v_lshlrev_b32_e32 v132, v168, v132
	v_mov_b32_dpp v192, v191 quad_perm:[0,0,0,0] row_mask:0xf bank_mask:0xf bound_ctrl:1
	global_load_dwordx4 v[94:97], v[68:69], off
	global_load_dwordx4 v[90:93], v[70:71], off
	v_lshl_add_u64 v[68:69], v[66:67], 0, v[132:133]
	v_lshrrev_b32_e32 v132, 16, v196
	v_lshlrev_b32_e32 v132, v168, v132
	v_mov_b32_dpp v190, v191 quad_perm:[1,1,1,1] row_mask:0xf bank_mask:0xf bound_ctrl:1
	v_lshl_add_u64 v[70:71], v[66:67], 0, v[132:133]
	v_lshrrev_b32_e32 v132, 16, v192
	v_lshlrev_b32_e32 v132, v168, v132
	v_mov_b32_e32 v147, v133
	v_mov_b32_dpp v189, v191 quad_perm:[2,2,2,2] row_mask:0xf bank_mask:0xf bound_ctrl:1
	global_load_dwordx4 v[86:89], v[68:69], off
	global_load_dwordx4 v[82:85], v[70:71], off
	v_lshl_add_u64 v[68:69], v[66:67], 0, v[132:133]
	v_lshrrev_b32_e32 v132, 16, v190
	v_lshlrev_b32_e32 v132, v168, v132
	v_lshl_add_u64 v[152:153], s[36:37], 0, v[146:147]
	v_mov_b32_e32 v149, v133
	v_mov_b32_dpp v188, v191 quad_perm:[3,3,3,3] row_mask:0xf bank_mask:0xf bound_ctrl:1
	v_lshl_add_u64 v[70:71], v[66:67], 0, v[132:133]
	v_lshrrev_b32_e32 v132, 16, v189
	v_lshlrev_b32_e32 v132, v168, v132
	v_lshl_add_u64 v[154:155], v[152:153], 0, v[148:149]
	global_load_dwordx4 v[78:81], v[68:69], off
	global_load_dwordx4 v[74:77], v[70:71], off
	v_lshl_add_u64 v[68:69], v[66:67], 0, v[132:133]
	v_lshrrev_b32_e32 v132, 16, v188
	v_lshlrev_b32_e32 v132, v168, v132
	v_add_co_u32_e32 v152, vcc, s51, v154
	v_lshl_add_u64 v[66:67], v[66:67], 0, v[132:133]
	s_nop 0
	v_addc_co_u32_e32 v153, vcc, 0, v155, vcc
	global_load_dwordx4 v[70:73], v[68:69], off
	s_nop 0
	global_load_dwordx4 v[66:69], v[66:67], off
	s_nop 0
	global_load_dwordx2 v[152:153], v[152:153], off
	v_perm_b32 v132, v187, v187, s53
	s_waitcnt vmcnt(21)
	v_perm_b32 v187, 0, v62, v169
	v_perm_b32 v62, 0, v62, v170
	v_perm_b32 v191, 0, v63, v169
	v_perm_b32 v63, 0, v63, v170
	v_perm_b32 v193, 0, v64, v169
	v_perm_b32 v64, 0, v64, v170
	v_perm_b32 v194, 0, v65, v169
	v_perm_b32 v65, 0, v65, v170
	v_pk_fma_f16 v187, v187, v132, 0
	v_pk_fma_f16 v62, v62, v132, 0
	v_pk_fma_f16 v191, v191, v132, 0
	v_pk_fma_f16 v63, v63, v132, 0
	v_pk_fma_f16 v193, v193, v132, 0
	v_pk_fma_f16 v64, v64, v132, 0
	v_pk_fma_f16 v194, v194, v132, 0
	v_pk_fma_f16 v65, v65, v132, 0
	v_perm_b32 v132, v186, v186, s53
	v_perm_b32 v186, 0, v58, v169
	v_perm_b32 v58, 0, v58, v170
	v_pk_fma_f16 v58, v58, v132, v62
	v_perm_b32 v62, 0, v59, v169
	v_perm_b32 v59, 0, v59, v170
	v_pk_fma_f16 v59, v59, v132, v63
	v_perm_b32 v63, 0, v60, v169
	v_perm_b32 v60, 0, v60, v170
	v_pk_fma_f16 v60, v60, v132, v64
	v_perm_b32 v64, 0, v61, v169
	v_perm_b32 v61, 0, v61, v170
	v_pk_fma_f16 v186, v186, v132, v187
	v_pk_fma_f16 v62, v62, v132, v191
	v_pk_fma_f16 v63, v63, v132, v193
	v_pk_fma_f16 v64, v64, v132, v194
	v_pk_fma_f16 v61, v61, v132, v65
	v_perm_b32 v65, v185, v185, s53
	v_perm_b32 v132, 0, v54, v169
	v_perm_b32 v54, 0, v54, v170
	v_pk_fma_f16 v54, v54, v65, v58
	v_perm_b32 v58, 0, v55, v169
	v_perm_b32 v55, 0, v55, v170
	v_pk_fma_f16 v55, v55, v65, v59
	v_perm_b32 v59, 0, v56, v169
	v_perm_b32 v56, 0, v56, v170
	v_pk_fma_f16 v56, v56, v65, v60
	v_perm_b32 v60, 0, v57, v169
	v_perm_b32 v57, 0, v57, v170
	v_pk_fma_f16 v58, v58, v65, v62
	v_pk_fma_f16 v57, v57, v65, v61
	v_perm_b32 v61, v184, v184, s53
	v_perm_b32 v62, 0, v50, v169
	v_perm_b32 v50, 0, v50, v170
	v_pk_fma_f16 v50, v50, v61, v54
	v_perm_b32 v54, 0, v51, v169
	v_perm_b32 v51, 0, v51, v170
	v_pk_fma_f16 v51, v51, v61, v55
	v_perm_b32 v55, 0, v52, v169
	v_perm_b32 v52, 0, v52, v170
	v_pk_fma_f16 v52, v52, v61, v56
	v_perm_b32 v56, 0, v53, v169
	v_perm_b32 v53, 0, v53, v170
	v_pk_fma_f16 v54, v54, v61, v58
	v_pk_fma_f16 v53, v53, v61, v57
	v_perm_b32 v57, v183, v183, s53
	v_perm_b32 v58, 0, v46, v169
	v_perm_b32 v46, 0, v46, v170
	v_pk_fma_f16 v46, v46, v57, v50
	v_perm_b32 v50, 0, v47, v169
	v_perm_b32 v47, 0, v47, v170
	v_pk_fma_f16 v47, v47, v57, v51
	v_perm_b32 v51, 0, v48, v169
	v_perm_b32 v48, 0, v48, v170
	v_pk_fma_f16 v48, v48, v57, v52
	v_perm_b32 v52, 0, v49, v169
	v_perm_b32 v49, 0, v49, v170
	v_pk_fma_f16 v50, v50, v57, v54
	v_pk_fma_f16 v49, v49, v57, v53
	v_perm_b32 v53, v182, v182, s53
	v_perm_b32 v54, 0, v42, v169
	v_perm_b32 v42, 0, v42, v170
	v_pk_fma_f16 v42, v42, v53, v46
	v_perm_b32 v46, 0, v43, v169
	v_perm_b32 v43, 0, v43, v170
	v_pk_fma_f16 v43, v43, v53, v47
	v_perm_b32 v47, 0, v44, v169
	v_perm_b32 v44, 0, v44, v170
	v_pk_fma_f16 v44, v44, v53, v48
	v_perm_b32 v48, 0, v45, v169
	v_perm_b32 v45, 0, v45, v170
	v_pk_fma_f16 v46, v46, v53, v50
	v_pk_fma_f16 v45, v45, v53, v49
	v_perm_b32 v49, v181, v181, s53
	v_perm_b32 v50, 0, v38, v169
	v_perm_b32 v38, 0, v38, v170
	v_pk_fma_f16 v38, v38, v49, v42
	v_perm_b32 v42, 0, v39, v169
	v_perm_b32 v39, 0, v39, v170
	v_pk_fma_f16 v39, v39, v49, v43
	v_perm_b32 v43, 0, v40, v169
	v_perm_b32 v40, 0, v40, v170
	v_pk_fma_f16 v40, v40, v49, v44
	v_perm_b32 v44, 0, v41, v169
	v_perm_b32 v41, 0, v41, v170
	v_pk_fma_f16 v42, v42, v49, v46
	v_pk_fma_f16 v41, v41, v49, v45
	v_perm_b32 v45, v180, v180, s53
	v_perm_b32 v46, 0, v34, v169
	v_perm_b32 v34, 0, v34, v170
	v_pk_fma_f16 v34, v34, v45, v38
	v_perm_b32 v38, 0, v35, v169
	v_perm_b32 v35, 0, v35, v170
	v_pk_fma_f16 v35, v35, v45, v39
	v_perm_b32 v39, 0, v36, v169
	v_perm_b32 v36, 0, v36, v170
	v_pk_fma_f16 v36, v36, v45, v40
	v_perm_b32 v40, 0, v37, v169
	v_perm_b32 v37, 0, v37, v170
	v_pk_fma_f16 v38, v38, v45, v42
	v_pk_fma_f16 v37, v37, v45, v41
	v_perm_b32 v41, v179, v179, s53
	v_perm_b32 v42, 0, v30, v169
	v_perm_b32 v30, 0, v30, v170
	v_pk_fma_f16 v30, v30, v41, v34
	v_perm_b32 v34, 0, v31, v169
	v_perm_b32 v31, 0, v31, v170
	v_pk_fma_f16 v31, v31, v41, v35
	v_perm_b32 v35, 0, v32, v169
	v_perm_b32 v32, 0, v32, v170
	v_pk_fma_f16 v32, v32, v41, v36
	v_perm_b32 v36, 0, v33, v169
	v_perm_b32 v33, 0, v33, v170
	v_pk_fma_f16 v34, v34, v41, v38
	v_pk_fma_f16 v33, v33, v41, v37
	v_perm_b32 v37, v178, v178, s53
	v_perm_b32 v38, 0, v26, v169
	v_perm_b32 v26, 0, v26, v170
	v_pk_fma_f16 v26, v26, v37, v30
	v_perm_b32 v30, 0, v27, v169
	v_perm_b32 v27, 0, v27, v170
	v_pk_fma_f16 v27, v27, v37, v31
	v_perm_b32 v31, 0, v28, v169
	v_perm_b32 v28, 0, v28, v170
	v_pk_fma_f16 v28, v28, v37, v32
	v_perm_b32 v32, 0, v29, v169
	v_perm_b32 v29, 0, v29, v170
	v_pk_fma_f16 v30, v30, v37, v34
	v_pk_fma_f16 v29, v29, v37, v33
	v_perm_b32 v33, v177, v177, s53
	v_perm_b32 v34, 0, v22, v169
	v_perm_b32 v22, 0, v22, v170
	v_pk_fma_f16 v22, v22, v33, v26
	v_perm_b32 v26, 0, v23, v169
	v_perm_b32 v23, 0, v23, v170
	v_pk_fma_f16 v23, v23, v33, v27
	v_perm_b32 v27, 0, v24, v169
	v_perm_b32 v24, 0, v24, v170
	v_pk_fma_f16 v24, v24, v33, v28
	v_perm_b32 v28, 0, v25, v169
	v_perm_b32 v25, 0, v25, v170
	v_pk_fma_f16 v26, v26, v33, v30
	v_pk_fma_f16 v25, v25, v33, v29
	v_perm_b32 v29, v176, v176, s53
	v_perm_b32 v30, 0, v18, v169
	v_perm_b32 v18, 0, v18, v170
	v_pk_fma_f16 v18, v18, v29, v22
	v_perm_b32 v22, 0, v19, v169
	v_perm_b32 v19, 0, v19, v170
	v_pk_fma_f16 v19, v19, v29, v23
	v_perm_b32 v23, 0, v20, v169
	v_perm_b32 v20, 0, v20, v170
	v_pk_fma_f16 v20, v20, v29, v24
	v_perm_b32 v24, 0, v21, v169
	v_perm_b32 v21, 0, v21, v170
	v_pk_fma_f16 v22, v22, v29, v26
	v_pk_fma_f16 v21, v21, v29, v25
	v_perm_b32 v25, v175, v175, s53
	v_perm_b32 v26, 0, v14, v169
	v_perm_b32 v14, 0, v14, v170
	v_pk_fma_f16 v14, v14, v25, v18
	v_perm_b32 v18, 0, v15, v169
	v_perm_b32 v15, 0, v15, v170
	v_pk_fma_f16 v15, v15, v25, v19
	v_perm_b32 v19, 0, v16, v169
	v_perm_b32 v16, 0, v16, v170
	v_pk_fma_f16 v132, v132, v65, v186
	v_pk_fma_f16 v59, v59, v65, v63
	v_pk_fma_f16 v60, v60, v65, v64
	v_pk_fma_f16 v16, v16, v25, v20
	v_perm_b32 v20, 0, v17, v169
	v_perm_b32 v17, 0, v17, v170
	v_pk_fma_f16 v62, v62, v61, v132
	v_pk_fma_f16 v55, v55, v61, v59
	v_pk_fma_f16 v56, v56, v61, v60
	v_pk_fma_f16 v18, v18, v25, v22
	v_pk_fma_f16 v17, v17, v25, v21
	v_perm_b32 v21, v174, v174, s53
	v_perm_b32 v22, 0, v10, v169
	v_perm_b32 v10, 0, v10, v170
	v_pk_fma_f16 v58, v58, v57, v62
	v_pk_fma_f16 v51, v51, v57, v55
	v_pk_fma_f16 v52, v52, v57, v56
	v_pk_fma_f16 v10, v10, v21, v14
	v_perm_b32 v14, 0, v11, v169
	v_perm_b32 v11, 0, v11, v170
	v_pk_fma_f16 v54, v54, v53, v58
	v_pk_fma_f16 v47, v47, v53, v51
	v_pk_fma_f16 v48, v48, v53, v52
	v_pk_fma_f16 v11, v11, v21, v15
	v_perm_b32 v15, 0, v12, v169
	v_perm_b32 v12, 0, v12, v170
	v_pk_fma_f16 v50, v50, v49, v54
	v_pk_fma_f16 v43, v43, v49, v47
	v_pk_fma_f16 v44, v44, v49, v48
	v_pk_fma_f16 v12, v12, v21, v16
	v_perm_b32 v16, 0, v13, v169
	v_perm_b32 v13, 0, v13, v170
	v_pk_fma_f16 v46, v46, v45, v50
	v_pk_fma_f16 v39, v39, v45, v43
	v_pk_fma_f16 v40, v40, v45, v44
	v_pk_fma_f16 v14, v14, v21, v18
	v_pk_fma_f16 v13, v13, v21, v17
	v_perm_b32 v17, v173, v173, s53
	v_perm_b32 v18, 0, v6, v169
	v_perm_b32 v6, 0, v6, v170
	v_pk_fma_f16 v42, v42, v41, v46
	v_pk_fma_f16 v35, v35, v41, v39
	v_pk_fma_f16 v36, v36, v41, v40
	v_pk_fma_f16 v6, v6, v17, v10
	v_perm_b32 v10, 0, v7, v169
	v_perm_b32 v7, 0, v7, v170
	v_pk_fma_f16 v38, v38, v37, v42
	v_pk_fma_f16 v31, v31, v37, v35
	v_pk_fma_f16 v32, v32, v37, v36
	v_pk_fma_f16 v7, v7, v17, v11
	v_perm_b32 v11, 0, v8, v169
	v_perm_b32 v8, 0, v8, v170
	v_pk_fma_f16 v34, v34, v33, v38
	v_pk_fma_f16 v27, v27, v33, v31
	v_pk_fma_f16 v28, v28, v33, v32
	v_pk_fma_f16 v8, v8, v17, v12
	v_perm_b32 v12, 0, v9, v169
	v_perm_b32 v9, 0, v9, v170
	v_pk_fma_f16 v30, v30, v29, v34
	v_pk_fma_f16 v23, v23, v29, v27
	v_pk_fma_f16 v24, v24, v29, v28
	v_pk_fma_f16 v10, v10, v17, v14
	v_pk_fma_f16 v9, v9, v17, v13
	v_perm_b32 v13, v172, v172, s53
	v_perm_b32 v14, 0, v2, v169
	v_perm_b32 v2, 0, v2, v170
	v_pk_fma_f16 v26, v26, v25, v30
	v_pk_fma_f16 v19, v19, v25, v23
	v_pk_fma_f16 v20, v20, v25, v24
	v_pk_fma_f16 v2, v2, v13, v6
	v_perm_b32 v6, 0, v3, v169
	v_perm_b32 v3, 0, v3, v170
	v_pk_fma_f16 v22, v22, v21, v26
	v_pk_fma_f16 v15, v15, v21, v19
	v_pk_fma_f16 v16, v16, v21, v20
	v_pk_fma_f16 v3, v3, v13, v7
	v_perm_b32 v7, 0, v4, v169
	v_perm_b32 v4, 0, v4, v170
	v_pk_fma_f16 v18, v18, v17, v22
	v_pk_fma_f16 v11, v11, v17, v15
	v_pk_fma_f16 v12, v12, v17, v16
	v_pk_fma_f16 v4, v4, v13, v8
	v_perm_b32 v8, 0, v5, v169
	v_perm_b32 v5, 0, v5, v170
	v_pk_fma_f16 v14, v14, v13, v18
	v_pk_fma_f16 v6, v6, v13, v10
	v_pk_fma_f16 v7, v7, v13, v11
	v_pk_fma_f16 v8, v8, v13, v12
	v_pk_fma_f16 v5, v5, v13, v9
	v_cvt_f32_f16_e32 v9, v14
	v_lshrrev_b32_e32 v10, 16, v14
	v_cvt_f32_f16_e32 v10, v10
	v_cvt_f32_f16_e32 v11, v2
	v_lshrrev_b32_e32 v12, 16, v2
	v_cvt_f32_f16_e32 v12, v12
	v_cvt_f32_f16_e32 v13, v6
	v_lshrrev_b32_e32 v14, 16, v6
	v_cvt_f32_f16_e32 v14, v14
	v_cvt_f32_f16_e32 v15, v3
	v_lshrrev_b32_e32 v16, 16, v3
	v_cvt_f32_f16_e32 v16, v16
	v_cvt_f32_f16_e32 v2, v7
	v_lshrrev_b32_e32 v3, 16, v7
	v_cvt_f32_f16_e32 v3, v3
	v_cvt_f32_f16_e32 v6, v4
	v_lshrrev_b32_e32 v7, 16, v4
	v_cvt_f32_f16_e32 v7, v7
	v_cvt_f32_f16_e32 v17, v8
	v_lshrrev_b32_e32 v8, 16, v8
	v_cvt_f32_f16_e32 v8, v8
	v_cvt_f32_f16_e32 v18, v5
	v_lshrrev_b32_e32 v19, 16, v5
	v_cvt_f32_f16_e32 v19, v19
	v_permlane32_swap_b32_e32 v9, v2
	v_permlane32_swap_b32_e32 v10, v3
	v_permlane32_swap_b32_e32 v11, v6
	v_permlane32_swap_b32_e32 v12, v7
	v_permlane32_swap_b32_e32 v13, v17
	v_permlane32_swap_b32_e32 v14, v8
	v_permlane32_swap_b32_e32 v15, v18
	v_permlane32_swap_b32_e32 v16, v19
	v_add_f32_e32 v2, v9, v2
	v_add_f32_e32 v3, v10, v3
	v_add_f32_e32 v4, v11, v6
	v_add_f32_e32 v5, v12, v7
	v_add_f32_e32 v6, v13, v17
	v_add_f32_e32 v7, v14, v8
	v_add_f32_e32 v8, v15, v18
	v_add_f32_e32 v9, v16, v19
	v_permlane16_swap_b32_e32 v2, v6
	v_permlane16_swap_b32_e32 v3, v7
	v_permlane16_swap_b32_e32 v4, v8
	v_permlane16_swap_b32_e32 v5, v9
	v_pk_add_f32 v[2:3], v[2:3], v[6:7]
	v_pk_add_f32 v[4:5], v[4:5], v[8:9]
	s_nop 0
	v_cndmask_b32_e64 v6, v2, v4, s[4:5]
	v_cndmask_b32_e64 v7, v3, v5, s[4:5]
	ds_bpermute_b32 v6, v159, v6
	ds_bpermute_b32 v7, v159, v7
	v_cndmask_b32_e64 v3, v5, v3, s[4:5]
	v_cndmask_b32_e64 v2, v4, v2, s[4:5]
	s_waitcnt lgkmcnt(0)
	v_pk_add_f32 v[2:3], v[2:3], v[6:7]
	s_nop 0
	v_pk_add_f32 v[2:3], v[150:151], v[2:3]
	global_store_dwordx2 v[156:157], v[2:3], off
	v_lshl_add_u64 v[2:3], v[144:145], 0, s[30:31]
	global_load_dword v195, v[2:3], off
	global_load_dword v194, v[2:3], off offset:16
	global_load_dword v193, v[2:3], off offset:32
	global_load_dword v191, v[2:3], off offset:48
	s_waitcnt vmcnt(25)
	v_mov_b32_dpp v187, v211 quad_perm:[0,0,0,0] row_mask:0xf bank_mask:0xf bound_ctrl:1
	v_mov_b32_dpp v186, v211 quad_perm:[1,1,1,1] row_mask:0xf bank_mask:0xf bound_ctrl:1
	v_lshl_add_u64 v[2:3], v[134:135], 0, s[28:29]
	v_lshrrev_b32_e32 v132, 16, v187
	v_lshlrev_b32_e32 v132, v168, v132
	v_mov_b32_dpp v185, v211 quad_perm:[2,2,2,2] row_mask:0xf bank_mask:0xf bound_ctrl:1
	v_lshl_add_u64 v[4:5], v[2:3], 0, v[132:133]
	v_lshrrev_b32_e32 v132, 16, v186
	v_lshlrev_b32_e32 v132, v168, v132
	v_mov_b32_dpp v184, v211 quad_perm:[3,3,3,3] row_mask:0xf bank_mask:0xf bound_ctrl:1
	v_lshl_add_u64 v[6:7], v[2:3], 0, v[132:133]
	v_lshrrev_b32_e32 v132, 16, v185
	v_lshlrev_b32_e32 v132, v168, v132
	s_waitcnt vmcnt(24)
	v_mov_b32_dpp v183, v210 quad_perm:[0,0,0,0] row_mask:0xf bank_mask:0xf bound_ctrl:1
	global_load_dwordx4 v[62:65], v[4:5], off
	global_load_dwordx4 v[58:61], v[6:7], off
	v_lshl_add_u64 v[4:5], v[2:3], 0, v[132:133]
	v_lshrrev_b32_e32 v132, 16, v184
	v_lshlrev_b32_e32 v132, v168, v132
	v_mov_b32_dpp v182, v210 quad_perm:[1,1,1,1] row_mask:0xf bank_mask:0xf bound_ctrl:1
	v_lshl_add_u64 v[6:7], v[2:3], 0, v[132:133]
	v_lshrrev_b32_e32 v132, 16, v183
	v_lshlrev_b32_e32 v132, v168, v132
	v_mov_b32_dpp v181, v210 quad_perm:[2,2,2,2] row_mask:0xf bank_mask:0xf bound_ctrl:1
	global_load_dwordx4 v[54:57], v[4:5], off
	global_load_dwordx4 v[50:53], v[6:7], off
	v_lshl_add_u64 v[4:5], v[2:3], 0, v[132:133]
	v_lshrrev_b32_e32 v132, 16, v182
	v_lshlrev_b32_e32 v132, v168, v132
	v_mov_b32_dpp v180, v210 quad_perm:[3,3,3,3] row_mask:0xf bank_mask:0xf bound_ctrl:1
	v_lshl_add_u64 v[6:7], v[2:3], 0, v[132:133]
	v_lshrrev_b32_e32 v132, 16, v181
	v_lshlrev_b32_e32 v132, v168, v132
	s_waitcnt vmcnt(27)
	v_mov_b32_dpp v179, v209 quad_perm:[0,0,0,0] row_mask:0xf bank_mask:0xf bound_ctrl:1
	global_load_dwordx4 v[46:49], v[4:5], off
	global_load_dwordx4 v[42:45], v[6:7], off
	v_lshl_add_u64 v[4:5], v[2:3], 0, v[132:133]
	v_lshrrev_b32_e32 v132, 16, v180
	v_lshlrev_b32_e32 v132, v168, v132
	v_mov_b32_dpp v178, v209 quad_perm:[1,1,1,1] row_mask:0xf bank_mask:0xf bound_ctrl:1
	v_lshl_add_u64 v[6:7], v[2:3], 0, v[132:133]
	v_lshrrev_b32_e32 v132, 16, v179
	v_lshlrev_b32_e32 v132, v168, v132
	v_mov_b32_dpp v177, v209 quad_perm:[2,2,2,2] row_mask:0xf bank_mask:0xf bound_ctrl:1
	global_load_dwordx4 v[38:41], v[4:5], off
	global_load_dwordx4 v[34:37], v[6:7], off
	v_lshl_add_u64 v[4:5], v[2:3], 0, v[132:133]
	v_lshrrev_b32_e32 v132, 16, v178
	v_lshlrev_b32_e32 v132, v168, v132
	v_mov_b32_dpp v176, v209 quad_perm:[3,3,3,3] row_mask:0xf bank_mask:0xf bound_ctrl:1
	v_lshl_add_u64 v[6:7], v[2:3], 0, v[132:133]
	v_lshrrev_b32_e32 v132, 16, v177
	v_lshlrev_b32_e32 v132, v168, v132
	s_waitcnt vmcnt(30)
	v_mov_b32_dpp v175, v208 quad_perm:[0,0,0,0] row_mask:0xf bank_mask:0xf bound_ctrl:1
	global_load_dwordx4 v[30:33], v[4:5], off
	global_load_dwordx4 v[26:29], v[6:7], off
	v_lshl_add_u64 v[4:5], v[2:3], 0, v[132:133]
	v_lshrrev_b32_e32 v132, 16, v176
	v_lshlrev_b32_e32 v132, v168, v132
	v_mov_b32_dpp v174, v208 quad_perm:[1,1,1,1] row_mask:0xf bank_mask:0xf bound_ctrl:1
	v_lshl_add_u64 v[6:7], v[2:3], 0, v[132:133]
	v_lshrrev_b32_e32 v132, 16, v175
	v_lshlrev_b32_e32 v132, v168, v132
	v_mov_b32_dpp v173, v208 quad_perm:[2,2,2,2] row_mask:0xf bank_mask:0xf bound_ctrl:1
	global_load_dwordx4 v[22:25], v[4:5], off
	global_load_dwordx4 v[18:21], v[6:7], off
	v_lshl_add_u64 v[4:5], v[2:3], 0, v[132:133]
	v_lshrrev_b32_e32 v132, 16, v174
	v_lshlrev_b32_e32 v132, v168, v132
	v_lshl_add_u64 v[150:151], s[6:7], 0, v[146:147]
	v_mov_b32_dpp v172, v208 quad_perm:[3,3,3,3] row_mask:0xf bank_mask:0xf bound_ctrl:1
	v_lshl_add_u64 v[6:7], v[2:3], 0, v[132:133]
	v_lshrrev_b32_e32 v132, 16, v173
	v_lshlrev_b32_e32 v132, v168, v132
	v_lshl_add_u64 v[156:157], v[150:151], 0, v[148:149]
	global_load_dwordx4 v[14:17], v[4:5], off
	global_load_dwordx4 v[10:13], v[6:7], off
	v_lshl_add_u64 v[4:5], v[2:3], 0, v[132:133]
	v_lshrrev_b32_e32 v132, 16, v172
	v_lshlrev_b32_e32 v132, v168, v132
	v_add_co_u32_e32 v150, vcc, s51, v156
	v_lshl_add_u64 v[2:3], v[2:3], 0, v[132:133]
	s_nop 0
	v_addc_co_u32_e32 v151, vcc, 0, v157, vcc
	global_load_dwordx4 v[6:9], v[4:5], off
	s_nop 0
	global_load_dwordx4 v[2:5], v[2:3], off
	s_nop 0
	global_load_dwordx2 v[150:151], v[150:151], off
	v_perm_b32 v132, v207, v207, s53
	s_waitcnt vmcnt(38)
	v_perm_b32 v147, 0, v126, v169
	v_perm_b32 v126, 0, v126, v170
	v_perm_b32 v149, 0, v127, v169
	v_perm_b32 v127, 0, v127, v170
	v_perm_b32 v207, 0, v128, v169
	v_perm_b32 v128, 0, v128, v170
	v_perm_b32 v208, 0, v129, v169
	v_perm_b32 v129, 0, v129, v170
	v_pk_fma_f16 v147, v132, v147, 0
	v_pk_fma_f16 v126, v132, v126, 0
	v_pk_fma_f16 v149, v132, v149, 0
	v_pk_fma_f16 v127, v132, v127, 0
	v_pk_fma_f16 v207, v132, v207, 0
	v_pk_fma_f16 v128, v132, v128, 0
	v_pk_fma_f16 v208, v132, v208, 0
	v_pk_fma_f16 v129, v132, v129, 0
	v_perm_b32 v132, v206, v206, s53
	s_waitcnt vmcnt(37)
	v_perm_b32 v206, 0, v122, v169
	v_perm_b32 v122, 0, v122, v170
	v_pk_fma_f16 v122, v132, v122, v126
	v_perm_b32 v126, 0, v123, v169
	v_perm_b32 v123, 0, v123, v170
	v_pk_fma_f16 v123, v132, v123, v127
	v_perm_b32 v127, 0, v124, v169
	v_perm_b32 v124, 0, v124, v170
	v_pk_fma_f16 v124, v132, v124, v128
	v_perm_b32 v128, 0, v125, v169
	v_perm_b32 v125, 0, v125, v170
	v_pk_fma_f16 v147, v132, v206, v147
	v_pk_fma_f16 v126, v132, v126, v149
	v_pk_fma_f16 v127, v132, v127, v207
	v_pk_fma_f16 v128, v132, v128, v208
	v_pk_fma_f16 v125, v132, v125, v129
	v_perm_b32 v129, v205, v205, s53
	s_waitcnt vmcnt(36)
	v_perm_b32 v132, 0, v118, v169
	v_perm_b32 v118, 0, v118, v170
	v_pk_fma_f16 v118, v129, v118, v122
	v_perm_b32 v122, 0, v119, v169
	v_perm_b32 v119, 0, v119, v170
	v_pk_fma_f16 v119, v129, v119, v123
	v_perm_b32 v123, 0, v120, v169
	v_perm_b32 v120, 0, v120, v170
	v_pk_fma_f16 v120, v129, v120, v124
	v_perm_b32 v124, 0, v121, v169
	v_perm_b32 v121, 0, v121, v170
	v_pk_fma_f16 v122, v129, v122, v126
	v_pk_fma_f16 v121, v129, v121, v125
	v_perm_b32 v125, v204, v204, s53
	s_waitcnt vmcnt(35)
	v_perm_b32 v126, 0, v114, v169
	v_perm_b32 v114, 0, v114, v170
	v_pk_fma_f16 v114, v125, v114, v118
	v_perm_b32 v118, 0, v115, v169
	v_perm_b32 v115, 0, v115, v170
	v_pk_fma_f16 v115, v125, v115, v119
	v_perm_b32 v119, 0, v116, v169
	v_perm_b32 v116, 0, v116, v170
	v_pk_fma_f16 v116, v125, v116, v120
	v_perm_b32 v120, 0, v117, v169
	v_perm_b32 v117, 0, v117, v170
	v_pk_fma_f16 v118, v125, v118, v122
	v_pk_fma_f16 v117, v125, v117, v121
	v_perm_b32 v121, v203, v203, s53
	s_waitcnt vmcnt(34)
	v_perm_b32 v122, 0, v110, v169
	v_perm_b32 v110, 0, v110, v170
	v_pk_fma_f16 v110, v121, v110, v114
	v_perm_b32 v114, 0, v111, v169
	v_perm_b32 v111, 0, v111, v170
	v_pk_fma_f16 v111, v121, v111, v115
	v_perm_b32 v115, 0, v112, v169
	v_perm_b32 v112, 0, v112, v170
	v_pk_fma_f16 v112, v121, v112, v116
	v_perm_b32 v116, 0, v113, v169
	v_perm_b32 v113, 0, v113, v170
	v_pk_fma_f16 v114, v121, v114, v118
	v_pk_fma_f16 v113, v121, v113, v117
	v_perm_b32 v117, v202, v202, s53
	s_waitcnt vmcnt(33)
	v_perm_b32 v118, 0, v106, v169
	v_perm_b32 v106, 0, v106, v170
	v_pk_fma_f16 v106, v117, v106, v110
	v_perm_b32 v110, 0, v107, v169
	v_perm_b32 v107, 0, v107, v170
	v_pk_fma_f16 v107, v117, v107, v111
	v_perm_b32 v111, 0, v108, v169
	v_perm_b32 v108, 0, v108, v170
	v_pk_fma_f16 v108, v117, v108, v112
	v_perm_b32 v112, 0, v109, v169
	v_perm_b32 v109, 0, v109, v170
	v_pk_fma_f16 v110, v117, v110, v114
	v_pk_fma_f16 v109, v117, v109, v113
	v_perm_b32 v113, v201, v201, s53
	s_waitcnt vmcnt(32)
	v_perm_b32 v114, 0, v102, v169
	v_perm_b32 v102, 0, v102, v170
	v_pk_fma_f16 v102, v113, v102, v106
	v_perm_b32 v106, 0, v103, v169
	v_perm_b32 v103, 0, v103, v170
	v_pk_fma_f16 v103, v113, v103, v107
	v_perm_b32 v107, 0, v104, v169
	v_perm_b32 v104, 0, v104, v170
	v_pk_fma_f16 v104, v113, v104, v108
	v_perm_b32 v108, 0, v105, v169
	v_perm_b32 v105, 0, v105, v170
	v_pk_fma_f16 v106, v113, v106, v110
	v_pk_fma_f16 v105, v113, v105, v109
	v_perm_b32 v109, v200, v200, s53
	s_waitcnt vmcnt(31)
	v_perm_b32 v110, 0, v98, v169
	v_perm_b32 v98, 0, v98, v170
	v_pk_fma_f16 v98, v109, v98, v102
	v_perm_b32 v102, 0, v99, v169
	v_perm_b32 v99, 0, v99, v170
	v_pk_fma_f16 v99, v109, v99, v103
	v_perm_b32 v103, 0, v100, v169
	v_perm_b32 v100, 0, v100, v170
	v_pk_fma_f16 v100, v109, v100, v104
	v_perm_b32 v104, 0, v101, v169
	v_perm_b32 v101, 0, v101, v170
	v_pk_fma_f16 v102, v109, v102, v106
	v_pk_fma_f16 v101, v109, v101, v105
	v_perm_b32 v105, v199, v199, s53
	s_waitcnt vmcnt(30)
	v_perm_b32 v106, 0, v94, v169
	v_perm_b32 v94, 0, v94, v170
	v_pk_fma_f16 v94, v105, v94, v98
	v_perm_b32 v98, 0, v95, v169
	v_perm_b32 v95, 0, v95, v170
	v_pk_fma_f16 v95, v105, v95, v99
	v_perm_b32 v99, 0, v96, v169
	v_perm_b32 v96, 0, v96, v170
	v_pk_fma_f16 v96, v105, v96, v100
	v_perm_b32 v100, 0, v97, v169
	v_perm_b32 v97, 0, v97, v170
	v_pk_fma_f16 v98, v105, v98, v102
	v_pk_fma_f16 v97, v105, v97, v101
	v_perm_b32 v101, v198, v198, s53
	s_waitcnt vmcnt(29)
	v_perm_b32 v102, 0, v90, v169
	v_perm_b32 v90, 0, v90, v170
	v_pk_fma_f16 v90, v101, v90, v94
	v_perm_b32 v94, 0, v91, v169
	v_perm_b32 v91, 0, v91, v170
	v_pk_fma_f16 v91, v101, v91, v95
	v_perm_b32 v95, 0, v92, v169
	v_perm_b32 v92, 0, v92, v170
	v_pk_fma_f16 v92, v101, v92, v96
	v_perm_b32 v96, 0, v93, v169
	v_perm_b32 v93, 0, v93, v170
	v_pk_fma_f16 v94, v101, v94, v98
	v_pk_fma_f16 v93, v101, v93, v97
	v_perm_b32 v97, v197, v197, s53
	s_waitcnt vmcnt(28)
	v_perm_b32 v98, 0, v86, v169
	v_perm_b32 v86, 0, v86, v170
	v_pk_fma_f16 v86, v97, v86, v90
	v_perm_b32 v90, 0, v87, v169
	v_perm_b32 v87, 0, v87, v170
	v_pk_fma_f16 v87, v97, v87, v91
	v_perm_b32 v91, 0, v88, v169
	v_perm_b32 v88, 0, v88, v170
	v_pk_fma_f16 v88, v97, v88, v92
	v_perm_b32 v92, 0, v89, v169
	v_perm_b32 v89, 0, v89, v170
	v_pk_fma_f16 v90, v97, v90, v94
	v_pk_fma_f16 v89, v97, v89, v93
	v_perm_b32 v93, v196, v196, s53
	s_waitcnt vmcnt(27)
	v_perm_b32 v94, 0, v82, v169
	v_perm_b32 v82, 0, v82, v170
	v_pk_fma_f16 v82, v93, v82, v86
	v_perm_b32 v86, 0, v83, v169
	v_perm_b32 v83, 0, v83, v170
	v_pk_fma_f16 v83, v93, v83, v87
	v_perm_b32 v87, 0, v84, v169
	v_perm_b32 v84, 0, v84, v170
	v_pk_fma_f16 v84, v93, v84, v88
	v_perm_b32 v88, 0, v85, v169
	v_perm_b32 v85, 0, v85, v170
	v_pk_fma_f16 v86, v93, v86, v90
	v_pk_fma_f16 v85, v93, v85, v89
	v_perm_b32 v89, v192, v192, s53
	s_waitcnt vmcnt(26)
	v_perm_b32 v90, 0, v78, v169
	v_perm_b32 v78, 0, v78, v170
	v_pk_fma_f16 v78, v89, v78, v82
	v_perm_b32 v82, 0, v79, v169
	v_perm_b32 v79, 0, v79, v170
	v_pk_fma_f16 v79, v89, v79, v83
	v_perm_b32 v83, 0, v80, v169
	v_perm_b32 v80, 0, v80, v170
	v_pk_fma_f16 v132, v129, v132, v147
	v_pk_fma_f16 v123, v129, v123, v127
	v_pk_fma_f16 v124, v129, v124, v128
	v_pk_fma_f16 v80, v89, v80, v84
	v_perm_b32 v84, 0, v81, v169
	v_perm_b32 v81, 0, v81, v170
	v_pk_fma_f16 v126, v125, v126, v132
	v_pk_fma_f16 v119, v125, v119, v123
	v_pk_fma_f16 v120, v125, v120, v124
	v_pk_fma_f16 v82, v89, v82, v86
	v_pk_fma_f16 v81, v89, v81, v85
	v_perm_b32 v85, v190, v190, s53
	s_waitcnt vmcnt(25)
; template <bool RUN_L = true, bool RUN_G = true, bool DRY = false>
; __device__ __forceinline__ void phase_vaccH(unsigned char* ws, LAS unsigned char* lds, int layer, int G) {
;     ...
;                     VD_ISSUE(ra, pka, hva, hpa, pw0, i2c);
;                     __builtin_amdgcn_sched_barrier(0);
;                     VD_COMP(rc, pkc, hvc, hpc, v1);
	v_perm_b32 v86, 0, v74, v169
	v_perm_b32 v74, 0, v74, v170
	v_pk_fma_f16 v122, v121, v122, v126
	v_pk_fma_f16 v115, v121, v115, v119
	v_pk_fma_f16 v116, v121, v116, v120
	v_pk_fma_f16 v74, v85, v74, v78
	v_perm_b32 v78, 0, v75, v169
	v_perm_b32 v75, 0, v75, v170
	v_pk_fma_f16 v118, v117, v118, v122
	v_pk_fma_f16 v111, v117, v111, v115
	v_pk_fma_f16 v112, v117, v112, v116
	v_pk_fma_f16 v75, v85, v75, v79
	v_perm_b32 v79, 0, v76, v169
	v_perm_b32 v76, 0, v76, v170
	v_pk_fma_f16 v114, v113, v114, v118
	v_pk_fma_f16 v107, v113, v107, v111
	v_pk_fma_f16 v108, v113, v108, v112
	v_pk_fma_f16 v76, v85, v76, v80
	v_perm_b32 v80, 0, v77, v169
	v_perm_b32 v77, 0, v77, v170
	v_pk_fma_f16 v110, v109, v110, v114
	v_pk_fma_f16 v103, v109, v103, v107
	v_pk_fma_f16 v104, v109, v104, v108
	v_pk_fma_f16 v78, v85, v78, v82
	v_pk_fma_f16 v77, v85, v77, v81
	v_perm_b32 v81, v189, v189, s53
	s_waitcnt vmcnt(24)
	v_perm_b32 v82, 0, v70, v169
	v_perm_b32 v70, 0, v70, v170
	v_pk_fma_f16 v106, v105, v106, v110
	v_pk_fma_f16 v99, v105, v99, v103
	v_pk_fma_f16 v100, v105, v100, v104
	v_pk_fma_f16 v70, v81, v70, v74
	v_perm_b32 v74, 0, v71, v169
	v_perm_b32 v71, 0, v71, v170
	v_pk_fma_f16 v102, v101, v102, v106
	v_pk_fma_f16 v95, v101, v95, v99
	v_pk_fma_f16 v96, v101, v96, v100
	v_pk_fma_f16 v71, v81, v71, v75
	v_perm_b32 v75, 0, v72, v169
	v_perm_b32 v72, 0, v72, v170
	v_pk_fma_f16 v98, v97, v98, v102
	v_pk_fma_f16 v91, v97, v91, v95
	v_pk_fma_f16 v92, v97, v92, v96
	v_pk_fma_f16 v72, v81, v72, v76
	v_perm_b32 v76, 0, v73, v169
	v_perm_b32 v73, 0, v73, v170
	v_pk_fma_f16 v94, v93, v94, v98
	v_pk_fma_f16 v87, v93, v87, v91
	v_pk_fma_f16 v88, v93, v88, v92
	v_pk_fma_f16 v74, v81, v74, v78
	v_pk_fma_f16 v73, v81, v73, v77
	v_perm_b32 v77, v188, v188, s53
	s_waitcnt vmcnt(23)
	v_perm_b32 v78, 0, v66, v169
	v_perm_b32 v66, 0, v66, v170
	v_pk_fma_f16 v90, v89, v90, v94
	v_pk_fma_f16 v83, v89, v83, v87
	v_pk_fma_f16 v84, v89, v84, v88
	v_pk_fma_f16 v66, v77, v66, v70
	v_perm_b32 v70, 0, v67, v169
	v_perm_b32 v67, 0, v67, v170
	v_pk_fma_f16 v86, v85, v86, v90
	v_pk_fma_f16 v79, v85, v79, v83
	v_pk_fma_f16 v80, v85, v80, v84
	v_pk_fma_f16 v67, v77, v67, v71
	v_perm_b32 v71, 0, v68, v169
	v_perm_b32 v68, 0, v68, v170
	v_pk_fma_f16 v82, v81, v82, v86
	v_pk_fma_f16 v75, v81, v75, v79
	v_pk_fma_f16 v76, v81, v76, v80
	v_pk_fma_f16 v68, v77, v68, v72
	v_perm_b32 v72, 0, v69, v169
	v_perm_b32 v69, 0, v69, v170
	v_pk_fma_f16 v78, v77, v78, v82
	v_pk_fma_f16 v70, v77, v70, v74
	v_pk_fma_f16 v71, v77, v71, v75
	v_pk_fma_f16 v72, v77, v72, v76
	v_pk_fma_f16 v69, v77, v69, v73
	v_cvt_f32_f16_e32 v73, v78
	v_lshrrev_b32_e32 v74, 16, v78
	v_cvt_f32_f16_e32 v74, v74
	v_cvt_f32_f16_e32 v75, v66
	v_lshrrev_b32_e32 v76, 16, v66
	v_cvt_f32_f16_e32 v76, v76
	v_cvt_f32_f16_e32 v77, v70
	v_lshrrev_b32_e32 v78, 16, v70
	v_cvt_f32_f16_e32 v78, v78
	v_cvt_f32_f16_e32 v79, v67
	v_lshrrev_b32_e32 v80, 16, v67
	v_cvt_f32_f16_e32 v80, v80
	v_cvt_f32_f16_e32 v66, v71
	v_lshrrev_b32_e32 v67, 16, v71
	v_cvt_f32_f16_e32 v67, v67
	v_cvt_f32_f16_e32 v70, v68
	v_lshrrev_b32_e32 v71, 16, v68
	v_cvt_f32_f16_e32 v71, v71
	v_cvt_f32_f16_e32 v81, v72
	v_lshrrev_b32_e32 v72, 16, v72
	v_cvt_f32_f16_e32 v72, v72
	v_cvt_f32_f16_e32 v82, v69
	v_lshrrev_b32_e32 v83, 16, v69
	v_cvt_f32_f16_e32 v83, v83
	v_permlane32_swap_b32_e32 v73, v66
	v_permlane32_swap_b32_e32 v74, v67
	v_permlane32_swap_b32_e32 v75, v70
	v_permlane32_swap_b32_e32 v76, v71
	v_permlane32_swap_b32_e32 v77, v81
	v_permlane32_swap_b32_e32 v78, v72
	v_permlane32_swap_b32_e32 v79, v82
	v_permlane32_swap_b32_e32 v80, v83
	v_add_f32_e32 v66, v73, v66
	v_add_f32_e32 v67, v74, v67
	v_add_f32_e32 v68, v75, v70
	v_add_f32_e32 v69, v76, v71
	v_add_f32_e32 v70, v77, v81
	v_add_f32_e32 v71, v78, v72
	v_add_f32_e32 v72, v79, v82
	v_add_f32_e32 v73, v80, v83
	v_permlane16_swap_b32_e32 v66, v70
	v_permlane16_swap_b32_e32 v67, v71
	v_permlane16_swap_b32_e32 v68, v72
	v_permlane16_swap_b32_e32 v69, v73
	v_pk_add_f32 v[66:67], v[66:67], v[70:71]
	v_pk_add_f32 v[70:71], v[68:69], v[72:73]
	s_nop 0
	v_cndmask_b32_e64 v68, v66, v70, s[4:5]
	v_cndmask_b32_e64 v69, v67, v71, s[4:5]
	ds_bpermute_b32 v68, v159, v68
	ds_bpermute_b32 v69, v159, v69
	s_cbranch_scc1 .LBB0_1979
	v_cndmask_b32_e64 v67, v71, v67, s[4:5]
	v_cndmask_b32_e64 v66, v70, v66, s[4:5]
	s_waitcnt lgkmcnt(0)
	v_pk_add_f32 v[66:67], v[66:67], v[68:69]
	v_lshl_add_u64 v[72:73], v[154:155], 0, s[14:15]
	s_waitcnt vmcnt(22)
	v_pk_add_f32 v[66:67], v[152:153], v[66:67]
	global_store_dwordx2 v[72:73], v[66:67], off
	s_branch .LBB0_1979

; #define VL_LOAD(wr, C) do { _Pragma("unroll") for (int i = 0; i < 16; ++i) wr[i] = wp[(size_t)((C) * 16 + i) * MROWS]; } while (0)
; #define VL_LOAD(wr, C) do { _Pragma("unroll") for (int i = 0; i < 16; ++i) wr[i] = wp[(size_t)((C) * 16 + i) * MROWS]; } while (0)
; template <bool RUN_L = true, bool RUN_G = true, bool DRY = false>
; __device__ __forceinline__ void phase_vaccH(unsigned char* ws, LAS unsigned char* lds, int layer, int G) {
;     ...
;                 VL_LOAD(wa, 0);
; #pragma unroll 1
;                 for (int c = 0; c < 8; c += 2) {
;                     VL_LOAD(wb, c + 1);
;                     __builtin_amdgcn_sched_barrier(0);
;                     VL_CHUNK(wa);
.LBB0_1987:
	s_add_u32 s78, s76, s52
	s_addc_u32 s79, s77, 0
	global_load_dword v72, v238, s[78:79] offset:64
	s_add_u32 s78, s76, s41
	s_addc_u32 s79, s77, 0
	global_load_dword v73, v238, s[78:79] offset:128
	s_add_u32 s78, s76, s45
	s_addc_u32 s79, s77, 0
	global_load_dword v74, v238, s[78:79] offset:192
	s_add_u32 s78, s76, s54
	s_addc_u32 s79, s77, 0
	global_load_dword v75, v238, s[78:79] offset:256
	s_add_u32 s78, s76, s55
	s_addc_u32 s79, s77, 0
	global_load_dword v76, v238, s[78:79] offset:320
	s_add_u32 s78, s76, s56
	s_addc_u32 s79, s77, 0
	global_load_dword v77, v238, s[78:79] offset:384
	s_add_u32 s78, s76, s57
	s_addc_u32 s79, s77, 0
	global_load_dword v78, v238, s[78:79] offset:448
	s_add_u32 s78, s76, s58
	s_addc_u32 s79, s77, 0
	global_load_dword v79, v238, s[78:79] offset:512
	global_load_dword v80, v238, s[76:77]
	s_add_u32 s78, s76, s59
	s_addc_u32 s79, s77, 0
	global_load_dword v81, v238, s[78:79] offset:576
	s_add_u32 s78, s76, s60
	s_addc_u32 s79, s77, 0
	global_load_dword v82, v238, s[78:79] offset:640
	s_add_u32 s78, s76, s61
	s_addc_u32 s79, s77, 0
	global_load_dword v83, v238, s[78:79] offset:704
	s_add_u32 s78, s76, s62
	s_addc_u32 s79, s77, 0
	global_load_dword v84, v238, s[78:79] offset:768
	s_add_u32 s78, s76, s63
	s_addc_u32 s79, s77, 0
	global_load_dword v85, v238, s[78:79] offset:832
	s_add_u32 s78, s76, s64
	s_addc_u32 s79, s77, 0
	global_load_dword v86, v238, s[78:79] offset:896
	s_add_u32 s78, s76, s65
	s_addc_u32 s79, s77, 0
	global_load_dword v87, v238, s[78:79] offset:960
	v_mov_b32_e32 v17, v31
	v_mov_b32_e32 v16, v30
	v_mov_b32_e32 v19, v29
	v_mov_b32_e32 v18, v28
	s_waitcnt vmcnt(30)
	v_bfe_u32 v25, v44, 16, 16
	v_lshl_add_u32 v26, v25, 3, 0
	s_waitcnt vmcnt(29)
	v_bfe_u32 v25, v42, 16, 16
	v_bfe_u32 v24, v46, 16, 16
	v_lshl_add_u32 v28, v25, 3, 0
	s_waitcnt vmcnt(28)
	v_bfe_u32 v25, v40, 16, 16
	v_lshl_add_u32 v24, v24, 3, 0
	v_lshl_add_u32 v30, v25, 3, 0
	ds_read_b64 v[24:25], v24
	ds_read_b64 v[26:27], v26
	ds_read_b64 v[28:29], v28
	ds_read_b64 v[30:31], v30
	v_perm_b32 v46, v46, v46, s53
	s_waitcnt lgkmcnt(3)
	v_perm_b32 v88, 0, v24, v169
	v_perm_b32 v24, 0, v24, v170
	v_perm_b32 v89, 0, v25, v169
	v_perm_b32 v25, 0, v25, v170
	v_pk_fma_f16 v88, v46, v88, 0
	v_pk_fma_f16 v24, v46, v24, 0
	v_pk_fma_f16 v89, v46, v89, 0
	v_pk_fma_f16 v25, v46, v25, 0
	v_perm_b32 v44, v44, v44, s53
	s_waitcnt lgkmcnt(2)
	v_perm_b32 v46, 0, v26, v169
	v_perm_b32 v26, 0, v26, v170
	v_pk_fma_f16 v24, v44, v26, v24
	v_perm_b32 v26, 0, v27, v169
	v_perm_b32 v27, 0, v27, v170
	s_waitcnt vmcnt(26)
	v_bfe_u32 v33, v38, 16, 16
	v_pk_fma_f16 v25, v44, v27, v25
	v_perm_b32 v27, v42, v42, s53
	s_waitcnt lgkmcnt(1)
	v_perm_b32 v42, 0, v28, v169
	v_perm_b32 v28, 0, v28, v170
	v_lshl_add_u32 v34, v33, 3, 0
	s_waitcnt vmcnt(25)
	v_bfe_u32 v33, v37, 16, 16
	v_pk_fma_f16 v26, v44, v26, v89
	v_pk_fma_f16 v24, v27, v28, v24
	v_perm_b32 v28, 0, v29, v169
	v_bfe_u32 v32, v39, 16, 16
	v_lshl_add_u32 v52, v33, 3, 0
	s_waitcnt vmcnt(24)
	v_bfe_u32 v33, v36, 16, 16
	v_pk_fma_f16 v46, v44, v46, v88
	v_pk_fma_f16 v26, v27, v28, v26
	v_perm_b32 v28, 0, v29, v170
	v_lshl_add_u32 v32, v32, 3, 0
	v_lshl_add_u32 v54, v33, 3, 0
	v_pk_fma_f16 v42, v27, v42, v46
	v_pk_fma_f16 v25, v27, v28, v25
	v_perm_b32 v27, v40, v40, s53
	s_waitcnt lgkmcnt(0)
	v_perm_b32 v29, 0, v30, v170
	ds_read_b64 v[32:33], v32
	ds_read_b64 v[34:35], v34
	ds_read_b64 v[52:53], v52
	ds_read_b64 v[54:55], v54
	v_pk_fma_f16 v24, v27, v29, v24
	v_perm_b32 v29, 0, v31, v169
	v_perm_b32 v28, 0, v30, v169
	v_pk_fma_f16 v26, v27, v29, v26
	v_perm_b32 v29, 0, v31, v170
	v_pk_fma_f16 v28, v27, v28, v42
	v_pk_fma_f16 v25, v27, v29, v25
	v_perm_b32 v27, v39, v39, s53
	s_waitcnt lgkmcnt(3)
	v_perm_b32 v29, 0, v32, v169
	v_pk_fma_f16 v28, v27, v29, v28
	v_perm_b32 v29, 0, v32, v170
	v_pk_fma_f16 v24, v27, v29, v24
	v_perm_b32 v29, 0, v33, v169
	v_pk_fma_f16 v26, v27, v29, v26
	v_perm_b32 v29, 0, v33, v170
	v_pk_fma_f16 v25, v27, v29, v25
	v_perm_b32 v27, v38, v38, s53
	s_waitcnt lgkmcnt(2)
	v_perm_b32 v29, 0, v34, v169
	v_pk_fma_f16 v28, v27, v29, v28
	v_perm_b32 v29, 0, v34, v170
	v_pk_fma_f16 v24, v27, v29, v24
	v_perm_b32 v29, 0, v35, v169
	v_pk_fma_f16 v26, v27, v29, v26
	v_perm_b32 v29, 0, v35, v170
	v_pk_fma_f16 v25, v27, v29, v25
	v_perm_b32 v27, v37, v37, s53
	s_waitcnt lgkmcnt(1)
	v_perm_b32 v29, 0, v52, v169
	v_pk_fma_f16 v28, v27, v29, v28
	v_perm_b32 v29, 0, v52, v170
	s_waitcnt vmcnt(22)
	v_bfe_u32 v57, v50, 16, 16
	v_pk_fma_f16 v24, v27, v29, v24
	v_perm_b32 v29, 0, v53, v169
	v_lshl_add_u32 v58, v57, 3, 0
	s_waitcnt vmcnt(21)
	v_bfe_u32 v57, v49, 16, 16
	v_pk_fma_f16 v26, v27, v29, v26
	v_perm_b32 v29, 0, v53, v170
	v_bfe_u32 v56, v51, 16, 16
	v_lshl_add_u32 v60, v57, 3, 0
	s_waitcnt vmcnt(20)
	v_bfe_u32 v57, v48, 16, 16
	v_pk_fma_f16 v25, v27, v29, v25
	v_perm_b32 v27, v36, v36, s53
	s_waitcnt lgkmcnt(0)
	v_perm_b32 v29, 0, v54, v169
	v_lshl_add_u32 v56, v56, 3, 0
	v_lshl_add_u32 v62, v57, 3, 0
	v_pk_fma_f16 v28, v27, v29, v28
	v_perm_b32 v29, 0, v54, v170
	ds_read_b64 v[56:57], v56
	ds_read_b64 v[58:59], v58
	ds_read_b64 v[60:61], v60
	ds_read_b64 v[62:63], v62
	v_pk_fma_f16 v24, v27, v29, v24
	v_perm_b32 v29, 0, v55, v169
	v_pk_fma_f16 v26, v27, v29, v26
	v_perm_b32 v29, 0, v55, v170
	v_pk_fma_f16 v25, v27, v29, v25
	v_perm_b32 v27, v51, v51, s53
	s_waitcnt lgkmcnt(3)
	v_perm_b32 v29, 0, v56, v169
	v_pk_fma_f16 v28, v27, v29, v28
	v_perm_b32 v29, 0, v56, v170
	v_pk_fma_f16 v24, v27, v29, v24
	v_perm_b32 v29, 0, v57, v169
	v_pk_fma_f16 v26, v27, v29, v26
	v_perm_b32 v29, 0, v57, v170
	v_pk_fma_f16 v25, v27, v29, v25
	v_perm_b32 v27, v50, v50, s53
	s_waitcnt lgkmcnt(2)
; #define VL_LOAD(wr, C) do { _Pragma("unroll") for (int i = 0; i < 16; ++i) wr[i] = wp[(size_t)((C) * 16 + i) * MROWS]; } while (0)
; #define VL_LOAD(wr, C) do { _Pragma("unroll") for (int i = 0; i < 16; ++i) wr[i] = wp[(size_t)((C) * 16 + i) * MROWS]; } while (0)
; template <bool RUN_L = true, bool RUN_G = true, bool DRY = false>
; __device__ __forceinline__ void phase_vaccH(unsigned char* ws, LAS unsigned char* lds, int layer, int G) {
;     ...
;                 for (int c = 0; c < 8; c += 2) {
;                     VL_LOAD(wb, c + 1);
;                     __builtin_amdgcn_sched_barrier(0);
;                     VL_CHUNK(wa);
;                     __builtin_amdgcn_sched_barrier(0);
;                     VL_LOAD(wa, (c + 2) & 7);
;                     __builtin_amdgcn_sched_barrier(0);
;                     VL_CHUNK(wb);
	v_perm_b32 v29, 0, v58, v169
	v_pk_fma_f16 v28, v27, v29, v28
	v_perm_b32 v29, 0, v58, v170
	v_pk_fma_f16 v24, v27, v29, v24
	v_perm_b32 v29, 0, v59, v169
	v_pk_fma_f16 v26, v27, v29, v26
	v_perm_b32 v29, 0, v59, v170
	v_pk_fma_f16 v25, v27, v29, v25
	v_perm_b32 v27, v49, v49, s53
	s_waitcnt lgkmcnt(1)
	v_perm_b32 v29, 0, v60, v169
	v_pk_fma_f16 v28, v27, v29, v28
	v_perm_b32 v29, 0, v60, v170
	s_waitcnt vmcnt(18)
	v_bfe_u32 v65, v45, 16, 16
	v_pk_fma_f16 v24, v27, v29, v24
	v_perm_b32 v29, 0, v61, v169
	v_lshl_add_u32 v66, v65, 3, 0
	s_waitcnt vmcnt(17)
	v_bfe_u32 v65, v43, 16, 16
	v_pk_fma_f16 v26, v27, v29, v26
	v_perm_b32 v29, 0, v61, v170
	v_bfe_u32 v64, v47, 16, 16
	v_lshl_add_u32 v68, v65, 3, 0
	s_waitcnt vmcnt(16)
	v_bfe_u32 v65, v41, 16, 16
	v_pk_fma_f16 v25, v27, v29, v25
	v_perm_b32 v27, v48, v48, s53
	s_waitcnt lgkmcnt(0)
	v_perm_b32 v29, 0, v62, v169
	v_lshl_add_u32 v64, v64, 3, 0
	v_lshl_add_u32 v70, v65, 3, 0
	v_pk_fma_f16 v28, v27, v29, v28
	v_perm_b32 v29, 0, v62, v170
	ds_read_b64 v[64:65], v64
	ds_read_b64 v[66:67], v66
	ds_read_b64 v[68:69], v68
	ds_read_b64 v[70:71], v70
	v_pk_fma_f16 v24, v27, v29, v24
	v_perm_b32 v29, 0, v63, v169
	v_pk_fma_f16 v26, v27, v29, v26
	v_perm_b32 v29, 0, v63, v170
	v_pk_fma_f16 v25, v27, v29, v25
	v_perm_b32 v27, v47, v47, s53
	s_waitcnt lgkmcnt(3)
	v_perm_b32 v29, 0, v64, v169
	v_pk_fma_f16 v28, v27, v29, v28
	v_perm_b32 v29, 0, v64, v170
	v_pk_fma_f16 v24, v27, v29, v24
	v_perm_b32 v29, 0, v65, v169
	v_pk_fma_f16 v26, v27, v29, v26
	v_perm_b32 v29, 0, v65, v170
	v_pk_fma_f16 v25, v27, v29, v25
	v_perm_b32 v27, v45, v45, s53
	s_waitcnt lgkmcnt(2)
	v_perm_b32 v29, 0, v66, v169
	v_pk_fma_f16 v28, v27, v29, v28
	v_perm_b32 v29, 0, v66, v170
	v_pk_fma_f16 v24, v27, v29, v24
	v_perm_b32 v29, 0, v67, v169
	v_pk_fma_f16 v26, v27, v29, v26
	v_perm_b32 v29, 0, v67, v170
	v_pk_fma_f16 v25, v27, v29, v25
	v_perm_b32 v27, v43, v43, s53
	s_waitcnt lgkmcnt(1)
	v_perm_b32 v29, 0, v68, v169
	v_pk_fma_f16 v28, v27, v29, v28
	v_perm_b32 v29, 0, v68, v170
	v_pk_fma_f16 v24, v27, v29, v24
	v_perm_b32 v29, 0, v69, v169
	v_pk_fma_f16 v26, v27, v29, v26
	v_perm_b32 v29, 0, v69, v170
	v_pk_fma_f16 v25, v27, v29, v25
	v_perm_b32 v27, v41, v41, s53
	s_waitcnt lgkmcnt(0)
	v_perm_b32 v29, 0, v70, v169
	v_pk_fma_f16 v56, v27, v29, v28
	v_perm_b32 v28, 0, v70, v170
	v_pk_fma_f16 v57, v27, v28, v24
	v_perm_b32 v24, 0, v71, v169
	v_pk_fma_f16 v58, v27, v24, v26
	v_perm_b32 v24, 0, v71, v170
	v_pk_fma_f16 v59, v27, v24, v25
	s_and_b32 s8, s30, 0x60
	s_mul_i32 s8, s8, 0x8040
	s_add_u32 s98, s16, s8
	s_addc_u32 s99, s17, 0
	global_load_dword v46, v238, s[98:99]
	s_add_u32 s78, s98, s52
	s_addc_u32 s79, s99, 0
	global_load_dword v44, v238, s[78:79] offset:64
	s_add_u32 s78, s98, s41
	s_addc_u32 s79, s99, 0
	global_load_dword v42, v238, s[78:79] offset:128
	s_add_u32 s78, s98, s45
	s_addc_u32 s79, s99, 0
	global_load_dword v40, v238, s[78:79] offset:192
	s_add_u32 s78, s98, s54
	s_addc_u32 s79, s99, 0
	global_load_dword v39, v238, s[78:79] offset:256
	s_add_u32 s78, s98, s55
	s_addc_u32 s79, s99, 0
	global_load_dword v38, v238, s[78:79] offset:320
	s_add_u32 s78, s98, s56
	s_addc_u32 s79, s99, 0
	global_load_dword v37, v238, s[78:79] offset:384
	s_add_u32 s78, s98, s57
	s_addc_u32 s79, s99, 0
	global_load_dword v36, v238, s[78:79] offset:448
	s_add_u32 s78, s98, s58
	s_addc_u32 s79, s99, 0
	global_load_dword v51, v238, s[78:79] offset:512
	s_add_u32 s78, s98, s59
	s_addc_u32 s79, s99, 0
	global_load_dword v50, v238, s[78:79] offset:576
	s_add_u32 s78, s98, s60
	s_addc_u32 s79, s99, 0
	global_load_dword v49, v238, s[78:79] offset:640
	s_add_u32 s78, s98, s61
	s_addc_u32 s79, s99, 0
	global_load_dword v48, v238, s[78:79] offset:704
	s_add_u32 s78, s98, s62
	s_addc_u32 s79, s99, 0
	global_load_dword v47, v238, s[78:79] offset:768
	s_add_u32 s78, s98, s63
	s_addc_u32 s79, s99, 0
	global_load_dword v45, v238, s[78:79] offset:832
	s_add_u32 s78, s98, s64
	s_addc_u32 s79, s99, 0
	global_load_dword v43, v238, s[78:79] offset:896
	s_add_u32 s78, s98, s65
	s_addc_u32 s79, s99, 0
	global_load_dword v41, v238, s[78:79] offset:960
	v_cvt_f32_f16_e32 v28, v58
	v_lshrrev_b32_e32 v29, 16, v58
	v_cvt_f32_f16_e32 v29, v29
	v_cvt_f32_f16_e32 v30, v59
	v_lshrrev_b32_e32 v31, 16, v59
	v_cvt_f32_f16_e32 v31, v31
	s_waitcnt vmcnt(23)
	v_bfe_u32 v32, v80, 16, 16
	v_bfe_u32 v33, v72, 16, 16
	v_bfe_u32 v34, v73, 16, 16
	v_bfe_u32 v35, v74, 16, 16
	v_bfe_u32 v52, v75, 16, 16
	v_bfe_u32 v53, v76, 16, 16
	v_bfe_u32 v54, v77, 16, 16
	v_bfe_u32 v55, v78, 16, 16
	v_bfe_u32 v60, v79, 16, 16
	s_waitcnt vmcnt(22)
	v_bfe_u32 v61, v81, 16, 16
	s_waitcnt vmcnt(21)
	v_bfe_u32 v62, v82, 16, 16
	s_waitcnt vmcnt(20)
	v_bfe_u32 v63, v83, 16, 16
	s_waitcnt vmcnt(19)
	v_bfe_u32 v64, v84, 16, 16
	s_waitcnt vmcnt(18)
	v_bfe_u32 v65, v85, 16, 16
	s_waitcnt vmcnt(17)
	v_bfe_u32 v66, v86, 16, 16
	s_waitcnt vmcnt(16)
	v_bfe_u32 v67, v87, 16, 16
	v_perm_b32 v89, v72, v72, s53
	v_perm_b32 v90, v73, v73, s53
	v_perm_b32 v91, v74, v74, s53
	v_perm_b32 v92, v75, v75, s53
	v_perm_b32 v93, v76, v76, s53
	v_perm_b32 v94, v77, v77, s53
	v_perm_b32 v95, v78, v78, s53
	v_cvt_f32_f16_e32 v24, v56
	v_lshrrev_b32_e32 v25, 16, v56
	v_cvt_f32_f16_e32 v25, v25
	v_cvt_f32_f16_e32 v26, v57
	v_lshrrev_b32_e32 v27, 16, v57
	v_cvt_f32_f16_e32 v27, v27
	v_lshl_add_u32 v32, v32, 3, 0
	v_lshl_add_u32 v56, v33, 3, 0
	v_lshl_add_u32 v57, v34, 3, 0
	v_lshl_add_u32 v58, v35, 3, 0
	v_lshl_add_u32 v59, v52, 3, 0
	v_lshl_add_u32 v68, v53, 3, 0
	v_lshl_add_u32 v69, v54, 3, 0
	v_lshl_add_u32 v70, v55, 3, 0
	v_lshl_add_u32 v71, v60, 3, 0
	v_lshl_add_u32 v72, v61, 3, 0
	v_lshl_add_u32 v73, v62, 3, 0
	v_lshl_add_u32 v74, v63, 3, 0
	v_lshl_add_u32 v75, v64, 3, 0
	v_lshl_add_u32 v76, v65, 3, 0
	v_lshl_add_u32 v77, v66, 3, 0
	v_lshl_add_u32 v78, v67, 3, 0
	v_perm_b32 v88, v80, v80, s53
	v_perm_b32 v96, v79, v79, s53
	ds_read_b64 v[32:33], v32
	ds_read_b64 v[34:35], v56
	ds_read_b64 v[52:53], v57
	ds_read_b64 v[54:55], v58
	ds_read_b64 v[56:57], v59
	ds_read_b64 v[58:59], v68
	ds_read_b64 v[60:61], v69
	ds_read_b64 v[62:63], v70
	ds_read_b64 v[64:65], v71
	ds_read_b64 v[66:67], v72
	ds_read_b64 v[68:69], v73
	ds_read_b64 v[70:71], v74
	ds_read_b64 v[72:73], v75
	ds_read_b64 v[74:75], v76
	ds_read_b64 v[76:77], v77
	ds_read_b64 v[78:79], v78
	v_pk_add_f32 v[22:23], v[22:23], v[28:29]
	v_pk_add_f32 v[20:21], v[20:21], v[30:31]
	s_waitcnt lgkmcnt(14)
; #define VL_LOAD(wr, C) do { _Pragma("unroll") for (int i = 0; i < 16; ++i) wr[i] = wp[(size_t)((C) * 16 + i) * MROWS]; } while (0)
; #define VL_LOAD(wr, C) do { _Pragma("unroll") for (int i = 0; i < 16; ++i) wr[i] = wp[(size_t)((C) * 16 + i) * MROWS]; } while (0)
; template <bool RUN_L = true, bool RUN_G = true, bool DRY = false>
; __device__ __forceinline__ void phase_vaccH(unsigned char* ws, LAS unsigned char* lds, int layer, int G) {
;     ...
;                 for (int c = 0; c < 8; c += 2) {
;                     VL_LOAD(wb, c + 1);
;                     __builtin_amdgcn_sched_barrier(0);
;                     VL_CHUNK(wa);
;                     __builtin_amdgcn_sched_barrier(0);
;                     VL_LOAD(wa, (c + 2) & 7);
;                     __builtin_amdgcn_sched_barrier(0);
;                     VL_CHUNK(wb);
;                     __builtin_amdgcn_sched_barrier(0);
;                 }
;                 if (valid) { hp[0] = h0 + (f32x4){accf[0], accf[1], accf[2], accf[3]}; hp[1] = h1 + (f32x4){accf[4], accf[5], accf[6], accf[7]}; }
	v_perm_b32 v28, 0, v32, v169
	v_perm_b32 v29, 0, v32, v170
	v_perm_b32 v30, 0, v33, v169
	v_perm_b32 v31, 0, v33, v170
	v_perm_b32 v32, 0, v34, v169
	v_perm_b32 v33, 0, v34, v170
	v_perm_b32 v34, 0, v35, v169
	v_perm_b32 v35, 0, v35, v170
	v_pk_fma_f16 v28, v88, v28, 0
	v_pk_fma_f16 v29, v88, v29, 0
	v_pk_fma_f16 v30, v88, v30, 0
	v_pk_fma_f16 v31, v88, v31, 0
	s_waitcnt lgkmcnt(13)
	v_perm_b32 v100, 0, v52, v169
	v_perm_b32 v52, 0, v52, v170
	v_perm_b32 v101, 0, v53, v169
	v_perm_b32 v53, 0, v53, v170
	v_pk_fma_f16 v28, v89, v32, v28
	v_pk_fma_f16 v29, v89, v33, v29
	v_pk_fma_f16 v30, v89, v34, v30
	v_pk_fma_f16 v31, v89, v35, v31
	s_waitcnt lgkmcnt(12)
	v_perm_b32 v102, 0, v54, v169
	v_perm_b32 v54, 0, v54, v170
	v_perm_b32 v103, 0, v55, v169
	v_perm_b32 v55, 0, v55, v170
	v_pk_fma_f16 v28, v90, v100, v28
	v_pk_fma_f16 v29, v90, v52, v29
	v_pk_fma_f16 v30, v90, v101, v30
	v_pk_fma_f16 v31, v90, v53, v31
	s_waitcnt lgkmcnt(11)
	v_perm_b32 v104, 0, v56, v169
	v_perm_b32 v56, 0, v56, v170
	v_perm_b32 v105, 0, v57, v169
	v_perm_b32 v57, 0, v57, v170
	v_pk_fma_f16 v28, v91, v102, v28
	v_pk_fma_f16 v29, v91, v54, v29
	v_pk_fma_f16 v30, v91, v103, v30
	v_pk_fma_f16 v31, v91, v55, v31
	s_waitcnt lgkmcnt(10)
	v_perm_b32 v106, 0, v58, v169
	v_perm_b32 v58, 0, v58, v170
	v_perm_b32 v107, 0, v59, v169
	v_perm_b32 v59, 0, v59, v170
	v_pk_fma_f16 v28, v92, v104, v28
	v_pk_fma_f16 v29, v92, v56, v29
	v_pk_fma_f16 v30, v92, v105, v30
	v_pk_fma_f16 v31, v92, v57, v31
	s_waitcnt lgkmcnt(9)
	v_perm_b32 v108, 0, v60, v169
	v_perm_b32 v60, 0, v60, v170
	v_perm_b32 v109, 0, v61, v169
	v_perm_b32 v61, 0, v61, v170
	v_pk_fma_f16 v28, v93, v106, v28
	v_pk_fma_f16 v29, v93, v58, v29
	v_pk_fma_f16 v30, v93, v107, v30
	v_pk_fma_f16 v31, v93, v59, v31
	s_waitcnt lgkmcnt(8)
	v_perm_b32 v110, 0, v62, v169
	v_perm_b32 v62, 0, v62, v170
	v_perm_b32 v111, 0, v63, v169
	v_perm_b32 v63, 0, v63, v170
	v_pk_fma_f16 v28, v94, v108, v28
	v_pk_fma_f16 v29, v94, v60, v29
	v_pk_fma_f16 v30, v94, v109, v30
	v_pk_fma_f16 v31, v94, v61, v31
	s_waitcnt lgkmcnt(7)
	v_perm_b32 v112, 0, v64, v169
	v_perm_b32 v64, 0, v64, v170
	v_perm_b32 v113, 0, v65, v169
	v_perm_b32 v65, 0, v65, v170
	v_pk_fma_f16 v28, v95, v110, v28
	v_pk_fma_f16 v29, v95, v62, v29
	v_pk_fma_f16 v30, v95, v111, v30
	v_pk_fma_f16 v31, v95, v63, v31
	v_perm_b32 v97, v81, v81, s53
	s_waitcnt lgkmcnt(6)
	v_perm_b32 v114, 0, v66, v169
	v_perm_b32 v66, 0, v66, v170
	v_perm_b32 v115, 0, v67, v169
	v_perm_b32 v67, 0, v67, v170
	v_pk_fma_f16 v28, v96, v112, v28
	v_pk_fma_f16 v29, v96, v64, v29
	v_pk_fma_f16 v30, v96, v113, v30
	v_pk_fma_f16 v31, v96, v65, v31
	v_perm_b32 v98, v82, v82, s53
	s_waitcnt lgkmcnt(5)
	v_perm_b32 v116, 0, v68, v169
	v_perm_b32 v68, 0, v68, v170
	v_perm_b32 v117, 0, v69, v169
	v_perm_b32 v69, 0, v69, v170
	v_pk_fma_f16 v28, v97, v114, v28
	v_pk_fma_f16 v29, v97, v66, v29
	v_pk_fma_f16 v30, v97, v115, v30
	v_pk_fma_f16 v31, v97, v67, v31
	v_perm_b32 v99, v83, v83, s53
	s_waitcnt lgkmcnt(4)
	v_perm_b32 v118, 0, v70, v169
	v_perm_b32 v70, 0, v70, v170
	v_perm_b32 v119, 0, v71, v169
	v_perm_b32 v71, 0, v71, v170
	v_pk_fma_f16 v28, v98, v116, v28
	v_pk_fma_f16 v29, v98, v68, v29
	v_pk_fma_f16 v30, v98, v117, v30
	v_pk_fma_f16 v31, v98, v69, v31
	v_perm_b32 v84, v84, v84, s53
	s_waitcnt lgkmcnt(3)
	v_perm_b32 v120, 0, v72, v169
	v_perm_b32 v72, 0, v72, v170
	v_perm_b32 v121, 0, v73, v169
	v_perm_b32 v73, 0, v73, v170
	v_pk_fma_f16 v28, v99, v118, v28
	v_pk_fma_f16 v29, v99, v70, v29
	v_pk_fma_f16 v30, v99, v119, v30
	v_pk_fma_f16 v31, v99, v71, v31
	v_perm_b32 v85, v85, v85, s53
	s_waitcnt lgkmcnt(2)
	v_perm_b32 v122, 0, v74, v169
	v_perm_b32 v74, 0, v74, v170
	v_perm_b32 v123, 0, v75, v169
	v_perm_b32 v75, 0, v75, v170
	v_pk_fma_f16 v28, v84, v120, v28
	v_pk_fma_f16 v29, v84, v72, v29
	v_pk_fma_f16 v30, v84, v121, v30
	v_pk_fma_f16 v31, v84, v73, v31
	v_perm_b32 v86, v86, v86, s53
	s_waitcnt lgkmcnt(1)
	v_perm_b32 v124, 0, v76, v169
	v_perm_b32 v76, 0, v76, v170
	v_perm_b32 v125, 0, v77, v169
	v_perm_b32 v77, 0, v77, v170
	v_pk_fma_f16 v28, v85, v122, v28
	v_pk_fma_f16 v29, v85, v74, v29
	v_pk_fma_f16 v30, v85, v123, v30
	v_pk_fma_f16 v31, v85, v75, v31
	v_perm_b32 v87, v87, v87, s53
	s_waitcnt lgkmcnt(0)
	v_perm_b32 v126, 0, v78, v169
	v_perm_b32 v78, 0, v78, v170
	v_perm_b32 v127, 0, v79, v169
	v_perm_b32 v79, 0, v79, v170
	v_pk_fma_f16 v28, v86, v124, v28
	v_pk_fma_f16 v29, v86, v76, v29
	v_pk_fma_f16 v30, v86, v125, v30
	v_pk_fma_f16 v31, v86, v77, v31
	v_pk_fma_f16 v35, v87, v126, v28
	v_pk_fma_f16 v33, v87, v78, v29
	v_pk_fma_f16 v29, v87, v127, v30
	v_pk_fma_f16 v31, v87, v79, v31
	v_cvt_f32_f16_e32 v34, v35
	v_cvt_f32_f16_e32 v32, v33
	v_cvt_f32_f16_e32 v28, v29
	v_cvt_f32_f16_e32 v30, v31
	v_lshrrev_b32_e32 v31, 16, v31
	v_cvt_f32_f16_e32 v31, v31
	v_lshrrev_b32_e32 v29, 16, v29
	v_cvt_f32_f16_e32 v29, v29
	v_lshrrev_b32_e32 v33, 16, v33
	v_cvt_f32_f16_e32 v33, v33
	v_lshrrev_b32_e32 v35, 16, v35
	v_cvt_f32_f16_e32 v35, v35
	v_pk_add_f32 v[80:81], v[18:19], v[24:25]
	v_pk_add_f32 v[82:83], v[16:17], v[26:27]
	v_pk_add_f32 v[20:21], v[20:21], v[30:31]
	v_pk_add_f32 v[22:23], v[22:23], v[28:29]
	v_pk_add_f32 v[30:31], v[82:83], v[32:33]
	v_pk_add_f32 v[28:29], v[80:81], v[34:35]
	s_add_u32 s76, s76, s20
	s_addc_u32 s77, s77, s21
	s_add_i32 s30, s30, 32
	s_add_i32 s31, s31, 2
	s_cmp_lt_u32 s31, 6
	v_lshl_add_u64 v[14:15], v[14:15], 0, s[20:21]
	s_cbranch_scc1 .LBB0_1987
	s_and_saveexec_b64 s[30:31], s[6:7]
	s_cbranch_execz .LBB0_1985
	v_pk_add_f32 v[12:13], v[18:19], v[24:25]
	v_pk_add_f32 v[14:15], v[16:17], v[26:27]
	v_pk_add_f32 v[12:13], v[12:13], v[34:35]
	v_pk_add_f32 v[14:15], v[14:15], v[32:33]
	v_pk_add_f32 v[6:7], v[6:7], v[12:13]
	v_pk_add_f32 v[8:9], v[8:9], v[14:15]
	v_pk_add_f32 v[4:5], v[4:5], v[20:21]
	v_pk_add_f32 v[2:3], v[2:3], v[22:23]
	global_store_dwordx4 v[10:11], v[6:9], off
	global_store_dwordx4 v[10:11], v[2:5], off offset:16
	s_branch .LBB0_1985
